# row sums by 4x v_mfma_f32_16x16x32_bf16 on a lane-masked ones operand instead of 8x 4x4x4 (fewer issue slots), rescale/final through per-wave LDS scratch
# speedup vs baseline: 1.0058x; 1.0052x over previous
;     ...
;   bf16x8 ones = {0x3F80, 0x3F80, 0x3F80, 0x3F80, 0x3F80, 0x3F80, 0x3F80, 0x3F80};
;   asm volatile("" : "+v"(ones));
; __device__ __forceinline__ void p2_attention(const Frame& F, KArgs a) {
;     const float lam = __uint_as_float(__builtin_amdgcn_readfirstlane(__float_as_uint(expf(wave_sum(a->in[5][F.lane] * a->in[6][F.lane])) - expf(wave_sum(a->in[7][F.lane] * a->in[8][F.lane])) + LAM_INIT)));
;     ...
;     for (int L = F.vcu; L < 1024; L += F.G) { const int i = L >> 8, v = L & 255, x = v >> 5, qb = v & 31, b = x >> 1; attn_unit_B<ATT_DUMMY>(F, a, b, 4 * (x & 1) + i, qb, lam, (att::bf16*)a->out); }
;     ...
;     for (int L = F.vcu; L < 1024; L += F.G) { const int i = L >> 8, v = L & 255, x = v >> 5, qb = v & 31, b = x >> 1; attn_unit_A<ATT_DUMMY>(F, a, b, 4 * (x & 1) + i, qb, (att::bf16*)a->out); }
;     ...
;     for (int L = F.vcu; L < 2048; L += F.G) {
.LBB0_256:
	s_cmp_lt_i32 s20, 4
	s_cselect_b64 s[24:25], -1, 0
	s_and_b64 s[4:5], s[24:25], s[4:5]
	s_andn2_b64 vcc, exec, s[4:5]
	s_cbranch_vccnz .LBB0_339
	s_mov_b64 s[26:27], s[0:1]
	s_waitcnt lgkmcnt(0)
	s_load_dwordx8 s[4:11], s[26:27], 0x28
	v_lshlrev_b32_e32 v1, 2, v202
	s_mov_b32 s3, 0x3fb8aa3b
	s_cmpk_gt_i32 s30, 0x7ff
	s_waitcnt lgkmcnt(0)
	global_load_dword v2, v1, s[4:5]
	global_load_dword v3, v1, s[6:7]
	global_load_dword v4, v1, s[8:9]
	global_load_dword v5, v1, s[10:11]
	v_mbcnt_lo_u32_b32 v1, -1, 0
	v_mbcnt_hi_u32_b32 v6, -1, v1
	v_and_b32_e32 v1, 64, v6
	v_xor_b32_e32 v7, 1, v6
	s_waitcnt vmcnt(0)
	v_add_u32_e32 v13, 64, v1
	v_cmp_lt_i32_e32 vcc, v7, v13
	v_xor_b32_e32 v8, 2, v6
	v_xor_b32_e32 v9, 4, v6
	v_cndmask_b32_e32 v1, v6, v7, vcc
	v_lshlrev_b32_e32 v1, 2, v1
	v_cmp_lt_i32_e32 vcc, v8, v13
	v_xor_b32_e32 v10, 8, v6
	v_xor_b32_e32 v11, 16, v6
	v_cndmask_b32_e32 v8, v6, v8, vcc
	v_lshlrev_b32_e32 v203, 2, v8
	v_cmp_lt_i32_e32 vcc, v9, v13
	v_xor_b32_e32 v12, 32, v6
	s_mov_b32 s4, 0xc2ce8ed0
	s_mov_b32 s7, 0
	v_mul_f32_e32 v7, v2, v3
	ds_bpermute_b32 v7, v1, v7
	v_mul_f32_e32 v14, v4, v5
	ds_bpermute_b32 v14, v1, v14
	s_waitcnt lgkmcnt(1)
	v_fmac_f32_e32 v7, v2, v3
	ds_bpermute_b32 v2, v203, v7
	s_waitcnt lgkmcnt(1)
	v_fmac_f32_e32 v14, v4, v5
	ds_bpermute_b32 v3, v203, v14
	v_cndmask_b32_e32 v4, v6, v9, vcc
	v_lshlrev_b32_e32 v204, 2, v4
	s_waitcnt lgkmcnt(1)
	v_add_f32_e32 v2, v7, v2
	ds_bpermute_b32 v4, v204, v2
	s_waitcnt lgkmcnt(1)
	v_add_f32_e32 v3, v14, v3
	ds_bpermute_b32 v5, v204, v3
	v_cmp_lt_i32_e32 vcc, v10, v13
	s_waitcnt lgkmcnt(1)
	v_add_f32_e32 v2, v2, v4
	v_cndmask_b32_e32 v7, v6, v10, vcc
	v_lshlrev_b32_e32 v205, 2, v7
	s_waitcnt lgkmcnt(0)
	v_add_f32_e32 v3, v3, v5
	ds_bpermute_b32 v4, v205, v2
	ds_bpermute_b32 v5, v205, v3
	v_cmp_lt_i32_e32 vcc, v11, v13
	s_waitcnt lgkmcnt(1)
	v_add_f32_e32 v2, v2, v4
	v_cndmask_b32_e32 v7, v6, v11, vcc
	v_lshlrev_b32_e32 v206, 2, v7
	s_waitcnt lgkmcnt(0)
	v_add_f32_e32 v3, v3, v5
	ds_bpermute_b32 v4, v206, v2
	ds_bpermute_b32 v5, v206, v3
	v_cmp_lt_i32_e32 vcc, v12, v13
	s_waitcnt lgkmcnt(1)
	v_add_f32_e32 v2, v2, v4
	v_cndmask_b32_e32 v6, v6, v12, vcc
	v_lshlrev_b32_e32 v207, 2, v6
	s_waitcnt lgkmcnt(0)
	v_add_f32_e32 v3, v3, v5
	ds_bpermute_b32 v4, v207, v2
	ds_bpermute_b32 v5, v207, v3
	s_waitcnt lgkmcnt(1)
	v_add_f32_e32 v2, v2, v4
	s_waitcnt lgkmcnt(0)
	v_add_f32_e32 v3, v3, v5
	v_mul_f32_e32 v4, 0x3fb8aa3b, v2
	v_mul_f32_e32 v5, 0x3fb8aa3b, v3
	v_fma_f32 v6, v2, s3, -v4
	v_rndne_f32_e32 v7, v4
	v_fma_f32 v8, v3, s3, -v5
	v_rndne_f32_e32 v9, v5
	v_fmac_f32_e32 v6, 0x32a5705f, v2
	v_sub_f32_e32 v4, v4, v7
	v_fmac_f32_e32 v8, 0x32a5705f, v3
	v_sub_f32_e32 v5, v5, v9
	v_add_f32_e32 v4, v4, v6
	v_cvt_i32_f32_e32 v7, v7
	v_add_f32_e32 v5, v5, v8
	v_exp_f32_e32 v4, v4
	v_cvt_i32_f32_e32 v9, v9
	v_exp_f32_e32 v5, v5
	v_cmp_ngt_f32_e32 vcc, s4, v2
	v_ldexp_f32 v4, v4, v7
	s_mov_b32 s3, 0x42b17218
	v_ldexp_f32 v5, v5, v9
	v_cndmask_b32_e32 v4, 0, v4, vcc
	v_cmp_ngt_f32_e32 vcc, s4, v3
	v_mov_b32_e32 v6, 0x7f800000
	s_nop 0
	v_cndmask_b32_e32 v5, 0, v5, vcc
	v_cmp_nlt_f32_e32 vcc, s3, v2
	s_nop 1
	v_cndmask_b32_e32 v2, v6, v4, vcc
	v_cmp_nlt_f32_e32 vcc, s3, v3
	s_nop 1
	v_cndmask_b32_e32 v3, v6, v5, vcc
	v_sub_f32_e32 v2, v2, v3
	s_nop 0
	v_readfirstlane_b32 s3, v2
	s_cbranch_scc1 .LBB0_339
	v_mov_b32_e32 v2, 0x3e4ccccd
	v_add_f32_e32 v208, s3, v2
	s_movk_i32 s3, 0xffe0
	v_mov_b32_e32 v185, 0
	s_movk_i32 s23, 0x3f00
	v_mov_b32_e32 v209, 0x358637bd
	s_mov_b32 s29, 0xf800000
	v_mov_b32_e32 v210, 0x260
	s_mov_b32 s31, 0x3e0293ee
	s_mov_b32 s41, 0x7ffffc
	s_movk_i32 s52, 0xe0
	s_mov_b32 s11, 0x20000
	s_brev_b32 s10, -2
	s_movk_i32 s53, 0x4000
	s_movk_i32 s54, 0x110
	s_mov_b32 s55, 0x8000
	s_mov_b32 s56, 0xc000
	s_mov_b32 s57, 0x10000
	s_mov_b32 s58, 0x14000
	s_mov_b32 s59, 0x18000
	s_mov_b32 s60, 0x41380000
	s_mov_b64 s[38:39], 0x10800000
	s_movk_i32 s61, 0x7fff
	s_mov_b32 s62, 0x10800000
	s_mov_b32 s63, 0x10801000
	s_mov_b32 s64, 0x10802000
	s_mov_b32 s65, 0x10803000
	s_mov_b32 s66, 0x10808000
	s_mov_b32 s67, 0x10809000
	s_mov_b32 s68, 0x1080a000
	s_mov_b32 s69, 0x1080b000
	s_mov_b32 s74, 0x10810000
	s_mov_b32 s75, 0x10811000
	s_mov_b32 s76, 0x10812000
	s_mov_b32 s77, 0x10813000
	s_mov_b32 s78, 0x10818000
	s_mov_b32 s79, 0x10819000
	s_mov_b32 s80, 0x1081a000
	s_mov_b32 s81, 0x1081b000
	s_mov_b32 s40, 0x3e38aa3b
	s_movk_i32 s82, 0x90
	s_mov_b32 s83, 0x40000
	s_mov_b32 s84, 0x30000
	s_mov_b32 s85, 0x60000
	s_mov_b32 s86, 0x50000
	s_mov_b64 s[42:43], 0x10800800
	v_lshrrev_b32_e32 v131, 4, v0
	v_xor_b32_e32 v131, v131, v0
	v_and_b32_e32 v131, 1, v131
	v_mov_b32_e32 v130, 0x3f803f80
	v_cmp_eq_u32_e64 s[98:99], 0, v131
	s_nop 3
	v_cndmask_b32_e64 v130, 0, v130, s[98:99]
	s_mov_b32 s87, s30
	s_branch .LBB0_261
; #define ATT_BAR() do { ATT_SBAR(); asm volatile("s_barrier" ::: "memory"); ATT_SBAR(); } while (0)
; __device__ __forceinline__ float bflo(unsigned w) { return __uint_as_float(w << 16); }
; __device__ __forceinline__ float bfhi(unsigned w) { return __uint_as_float(w & 0xffff0000u); }
;     ...
;   ATT_XSECTION(false);
;   ATT_BAR();
;   if (grp == 0) ATT_BAR();
; #pragma unroll
;   for (int r = 0; r < 16; ++r) rli[r] = __builtin_amdgcn_rcpf(lacc[r]);
;     ...
;     asm volatile("s_waitcnt lgkmcnt(0)" ::: "memory");
;     float ss[16];
; #pragma unroll
;     for (int r = 0; r < 16; ++r) ss[r] = 0.f;
; #pragma unroll
;     for (int d0 = 0; d0 < 4; ++d0)
; #pragma unroll
;         for (int r = 0; r < 16; r += 2) { const unsigned w = stash[(d0 * 8 + (r >> 1)) * 64 + lane_];
;             const float x0 = bflo(w) - lam * (o[d0][r] * rli[r]), x1 = bfhi(w) - lam * (o[d0][r + 1] * rli[r + 1]);
;             o[d0][r] = x0; o[d0][r + 1] = x1; ss[r] += x0 * x0; ss[r + 1] += x1 * x1; }
; #pragma unroll
;     for (int r = 0; r < 16; ++r) { float s = ss[r]; s += __shfl_xor(s, 1); s += __shfl_xor(s, 2); s += __shfl_xor(s, 4); s += __shfl_xor(s, 8); s += __shfl_xor(s, 16);
;         ss[r] = (1.0f - LAM_INIT) * __builtin_amdgcn_rsqf(s * (1.0f / 128.0f) + EPS); }
.LBB0_259:
	s_nop 7
	s_nop 1
	v_and_b32_e32 v244, 63, v0
	v_lshrrev_b32_e32 v245, 4, v244
	v_and_b32_e32 v244, 1, v244
	v_lshlrev_b32_e32 v244, 6, v244
	v_lshl_add_u32 v244, v245, 4, v244
	v_add_u32_e32 v244, s6, v244
	ds_write_b128 v244, v[240:243]
	v_add_u32_e32 v245, s6, v184
	s_waitcnt lgkmcnt(0)
	ds_read_b128 v[18:21], v245
	ds_read_b128 v[22:25], v245 offset:32
	ds_read_b128 v[26:29], v245 offset:64
	ds_read_b128 v[30:33], v245 offset:96
	s_waitcnt lgkmcnt(0)
	s_waitcnt lgkmcnt(0)
	s_nop 8
	v_rcp_f32_e32 v90, v18
	v_rcp_f32_e32 v91, v19
	ds_read2st64_b32 v[18:19], v165 offset1:1
	v_rcp_f32_e32 v92, v20
	v_rcp_f32_e32 v93, v21
	v_rcp_f32_e32 v94, v22
	v_rcp_f32_e32 v95, v23
	s_waitcnt lgkmcnt(0)
	v_lshlrev_b32_e32 v22, 16, v18
	v_mul_f32_e32 v23, v66, v90
	v_rcp_f32_e32 v96, v24
	v_rcp_f32_e32 v97, v25
	ds_read2st64_b32 v[20:21], v165 offset0:2 offset1:3
	ds_read2st64_b32 v[24:25], v165 offset0:4 offset1:5
	ds_read2st64_b32 v[88:89], v165 offset0:6 offset1:7
	v_fma_f32 v84, -v208, v23, v22
	v_and_b32_e32 v18, 0xffff0000, v18
	v_mul_f32_e32 v22, v67, v91
	v_fma_f32 v83, -v208, v22, v18
	v_lshlrev_b32_e32 v18, 16, v19
	v_mul_f32_e32 v22, v68, v92
	v_fma_f32 v68, -v208, v22, v18
	v_and_b32_e32 v18, 0xffff0000, v19
	v_mul_f32_e32 v19, v69, v93
	v_rcp_f32_e32 v98, v26
	v_fma_f32 v67, -v208, v19, v18
	s_waitcnt lgkmcnt(2)
	v_lshlrev_b32_e32 v18, 16, v20
	v_mul_f32_e32 v19, v70, v94
	v_rcp_f32_e32 v99, v27
	v_fma_f32 v66, -v208, v19, v18
	v_and_b32_e32 v18, 0xffff0000, v20
	v_mul_f32_e32 v19, v71, v95
	v_rcp_f32_e32 v100, v28
	v_rcp_f32_e32 v86, v32
	v_fma_f32 v32, -v208, v19, v18
	v_lshlrev_b32_e32 v18, 16, v21
	v_mul_f32_e32 v19, v72, v96
	v_rcp_f32_e32 v101, v29
	v_rcp_f32_e32 v102, v30
	v_fma_f32 v30, -v208, v19, v18
	v_and_b32_e32 v18, 0xffff0000, v21
	v_mul_f32_e32 v19, v73, v97
	v_fma_f32 v28, -v208, v19, v18
	s_waitcnt lgkmcnt(1)
	v_lshlrev_b32_e32 v18, 16, v24
	v_mul_f32_e32 v19, v74, v98
	v_rcp_f32_e32 v87, v31
	v_fma_f32 v26, -v208, v19, v18
	v_and_b32_e32 v18, 0xffff0000, v24
	v_mul_f32_e32 v19, v75, v99
	v_fma_f32 v24, -v208, v19, v18
	v_lshlrev_b32_e32 v18, 16, v25
	v_mul_f32_e32 v19, v76, v100
	v_rcp_f32_e32 v85, v33
	v_fma_f32 v23, -v208, v19, v18
	v_and_b32_e32 v18, 0xffff0000, v25
	v_mul_f32_e32 v19, v77, v101
	ds_read2st64_b32 v[74:75], v165 offset0:8 offset1:9
	v_fma_f32 v22, -v208, v19, v18
	s_waitcnt lgkmcnt(1)
	v_lshlrev_b32_e32 v18, 16, v88
	v_mul_f32_e32 v19, v78, v102
	v_fma_f32 v21, -v208, v19, v18
	v_and_b32_e32 v18, 0xffff0000, v88
	v_mul_f32_e32 v19, v79, v87
	v_fma_f32 v20, -v208, v19, v18
	v_lshlrev_b32_e32 v18, 16, v89
	v_mul_f32_e32 v19, v80, v86
	v_fma_f32 v19, -v208, v19, v18
	v_and_b32_e32 v18, 0xffff0000, v89
	v_mul_f32_e32 v25, v81, v85
	v_fma_f32 v18, -v208, v25, v18
	s_waitcnt lgkmcnt(0)
	v_lshlrev_b32_e32 v25, 16, v74
	v_mul_f32_e32 v27, v50, v90
	ds_read2st64_b32 v[76:77], v165 offset0:10 offset1:11
	ds_read2st64_b32 v[78:79], v165 offset0:12 offset1:13
	ds_read2st64_b32 v[80:81], v165 offset0:14 offset1:15
	v_fma_f32 v73, -v208, v27, v25
	v_and_b32_e32 v25, 0xffff0000, v74
	v_mul_f32_e32 v27, v51, v91
	v_fma_f32 v72, -v208, v27, v25
	v_lshlrev_b32_e32 v25, 16, v75
	v_mul_f32_e32 v27, v52, v92
	v_fma_f32 v71, -v208, v27, v25
	v_and_b32_e32 v25, 0xffff0000, v75
	v_mul_f32_e32 v27, v53, v93
	v_fma_f32 v70, -v208, v27, v25
	s_waitcnt lgkmcnt(2)
	v_lshlrev_b32_e32 v25, 16, v76
	v_mul_f32_e32 v27, v54, v94
	v_fma_f32 v69, -v208, v27, v25
	v_and_b32_e32 v25, 0xffff0000, v76
	v_mul_f32_e32 v27, v55, v95
	v_fma_f32 v55, -v208, v27, v25
	v_lshlrev_b32_e32 v25, 16, v77
	v_mul_f32_e32 v27, v56, v96
	v_fma_f32 v54, -v208, v27, v25
	v_and_b32_e32 v25, 0xffff0000, v77
	v_mul_f32_e32 v27, v57, v97
	v_fma_f32 v53, -v208, v27, v25
	s_waitcnt lgkmcnt(1)
	v_lshlrev_b32_e32 v25, 16, v78
	v_mul_f32_e32 v27, v58, v98
	v_fma_f32 v52, -v208, v27, v25
	v_and_b32_e32 v25, 0xffff0000, v78
	v_mul_f32_e32 v27, v59, v99
	v_fma_f32 v51, -v208, v27, v25
	v_lshlrev_b32_e32 v25, 16, v79
	v_mul_f32_e32 v27, v60, v100
	v_fma_f32 v50, -v208, v27, v25
	v_and_b32_e32 v25, 0xffff0000, v79
	v_mul_f32_e32 v27, v61, v101
	v_fma_f32 v33, -v208, v27, v25
	s_waitcnt lgkmcnt(0)
	v_lshlrev_b32_e32 v25, 16, v80
	v_mul_f32_e32 v27, v62, v102
	v_fma_f32 v31, -v208, v27, v25
	v_and_b32_e32 v25, 0xffff0000, v80
	v_mul_f32_e32 v27, v63, v87
	v_fma_f32 v29, -v208, v27, v25
	v_lshlrev_b32_e32 v25, 16, v81
	v_mul_f32_e32 v27, v64, v86
	v_fma_f32 v27, -v208, v27, v25
	v_and_b32_e32 v25, 0xffff0000, v81
	v_mul_f32_e32 v56, v65, v85
	v_fma_f32 v25, -v208, v56, v25
	ds_read2st64_b32 v[56:57], v165 offset0:16 offset1:17
	v_mul_f32_e32 v34, v34, v90
	ds_read2st64_b32 v[78:79], v165 offset0:18 offset1:19
	ds_read2st64_b32 v[80:81], v165 offset0:20 offset1:21
	ds_read2st64_b32 v[88:89], v165 offset0:22 offset1:23
	v_mul_f32_e32 v35, v35, v91
	v_mul_f32_e32 v2, v2, v90
	s_waitcnt lgkmcnt(3)
	v_lshlrev_b32_e32 v58, 16, v56
	v_fma_f32 v65, -v208, v34, v58
	v_and_b32_e32 v34, 0xffff0000, v56
	v_fma_f32 v62, -v208, v35, v34
	v_lshlrev_b32_e32 v34, 16, v57
	v_mul_f32_e32 v35, v36, v92
	v_fma_f32 v61, -v208, v35, v34
	v_and_b32_e32 v34, 0xffff0000, v57
	v_mul_f32_e32 v35, v37, v93
	v_fma_f32 v60, -v208, v35, v34
	s_waitcnt lgkmcnt(2)
	v_lshlrev_b32_e32 v34, 16, v78
	v_mul_f32_e32 v35, v38, v94
	v_fma_f32 v59, -v208, v35, v34
	v_and_b32_e32 v34, 0xffff0000, v78
	v_mul_f32_e32 v35, v39, v95
	v_fma_f32 v58, -v208, v35, v34
	v_lshlrev_b32_e32 v34, 16, v79
	v_mul_f32_e32 v35, v40, v96
	v_fma_f32 v57, -v208, v35, v34
	v_and_b32_e32 v34, 0xffff0000, v79
	v_mul_f32_e32 v35, v41, v97
	v_fma_f32 v56, -v208, v35, v34
	s_waitcnt lgkmcnt(1)
; __device__ __forceinline__ float bflo(unsigned w) { return __uint_as_float(w << 16); }
; __device__ __forceinline__ float bfhi(unsigned w) { return __uint_as_float(w & 0xffff0000u); }
;     ...
;     asm volatile("s_waitcnt lgkmcnt(0)" ::: "memory");
;     float ss[16];
; #pragma unroll
;     for (int r = 0; r < 16; ++r) ss[r] = 0.f;
; #pragma unroll
;     for (int d0 = 0; d0 < 4; ++d0)
; #pragma unroll
;         for (int r = 0; r < 16; r += 2) { const unsigned w = stash[(d0 * 8 + (r >> 1)) * 64 + lane_];
;             const float x0 = bflo(w) - lam * (o[d0][r] * rli[r]), x1 = bfhi(w) - lam * (o[d0][r + 1] * rli[r + 1]);
;             o[d0][r] = x0; o[d0][r + 1] = x1; ss[r] += x0 * x0; ss[r + 1] += x1 * x1; }
; #pragma unroll
;     for (int r = 0; r < 16; ++r) { float s = ss[r]; s += __shfl_xor(s, 1); s += __shfl_xor(s, 2); s += __shfl_xor(s, 4); s += __shfl_xor(s, 8); s += __shfl_xor(s, 16);
;         ss[r] = (1.0f - LAM_INIT) * __builtin_amdgcn_rsqf(s * (1.0f / 128.0f) + EPS); }
	v_lshlrev_b32_e32 v34, 16, v80
	v_mul_f32_e32 v35, v42, v98
	v_fma_f32 v41, -v208, v35, v34
	v_and_b32_e32 v34, 0xffff0000, v80
	v_mul_f32_e32 v35, v43, v99
	v_fma_f32 v40, -v208, v35, v34
	v_lshlrev_b32_e32 v34, 16, v81
	v_mul_f32_e32 v35, v44, v100
	v_fma_f32 v39, -v208, v35, v34
	v_and_b32_e32 v34, 0xffff0000, v81
	v_mul_f32_e32 v35, v45, v101
	v_fma_f32 v38, -v208, v35, v34
	s_waitcnt lgkmcnt(0)
	v_lshlrev_b32_e32 v34, 16, v88
	v_mul_f32_e32 v35, v46, v102
	v_fma_f32 v37, -v208, v35, v34
	v_and_b32_e32 v34, 0xffff0000, v88
	v_mul_f32_e32 v35, v47, v87
	v_fma_f32 v36, -v208, v35, v34
	v_lshlrev_b32_e32 v34, 16, v89
	v_mul_f32_e32 v35, v48, v86
	v_fma_f32 v35, -v208, v35, v34
	v_and_b32_e32 v34, 0xffff0000, v89
	v_mul_f32_e32 v42, v49, v85
	v_fma_f32 v34, -v208, v42, v34
	ds_read2st64_b32 v[42:43], v165 offset0:24 offset1:25
	ds_read2st64_b32 v[78:79], v165 offset0:26 offset1:27
	ds_read2st64_b32 v[80:81], v165 offset0:28 offset1:29
	ds_read2st64_b32 v[88:89], v165 offset0:30 offset1:31
	v_mul_f32_e32 v3, v3, v91
	v_mul_f32_e32 v103, v73, v73
	v_fmac_f32_e32 v103, v84, v84
	s_waitcnt lgkmcnt(3)
	v_lshlrev_b32_e32 v44, 16, v42
	v_fma_f32 v49, -v208, v2, v44
	v_and_b32_e32 v2, 0xffff0000, v42
	v_fma_f32 v90, -v208, v3, v2
	v_lshlrev_b32_e32 v2, 16, v43
	v_mul_f32_e32 v3, v4, v92
	v_fma_f32 v48, -v208, v3, v2
	v_and_b32_e32 v2, 0xffff0000, v43
	v_mul_f32_e32 v3, v5, v93
	v_fma_f32 v47, -v208, v3, v2
	s_waitcnt lgkmcnt(2)
	v_lshlrev_b32_e32 v2, 16, v78
	v_mul_f32_e32 v3, v6, v94
	v_fma_f32 v46, -v208, v3, v2
	v_and_b32_e32 v2, 0xffff0000, v78
	v_mul_f32_e32 v3, v7, v95
	v_fma_f32 v45, -v208, v3, v2
	v_lshlrev_b32_e32 v2, 16, v79
	v_mul_f32_e32 v3, v8, v96
	v_fma_f32 v44, -v208, v3, v2
	v_and_b32_e32 v2, 0xffff0000, v79
	v_mul_f32_e32 v3, v9, v97
	v_fma_f32 v43, -v208, v3, v2
	s_waitcnt lgkmcnt(1)
	v_lshlrev_b32_e32 v2, 16, v80
	v_mul_f32_e32 v3, v10, v98
	v_fma_f32 v42, -v208, v3, v2
	v_and_b32_e32 v2, 0xffff0000, v80
	v_mul_f32_e32 v3, v11, v99
	v_fma_f32 v10, -v208, v3, v2
	v_lshlrev_b32_e32 v2, 16, v81
	v_mul_f32_e32 v3, v12, v100
	v_fmac_f32_e32 v103, v65, v65
	v_fma_f32 v9, -v208, v3, v2
	v_and_b32_e32 v2, 0xffff0000, v81
	v_mul_f32_e32 v3, v13, v101
	v_fmac_f32_e32 v103, v49, v49
	v_fma_f32 v8, -v208, v3, v2
	s_waitcnt lgkmcnt(0)
	v_lshlrev_b32_e32 v2, 16, v88
	v_mul_f32_e32 v3, v14, v102
	v_fma_f32 v7, -v208, v3, v2
	ds_bpermute_b32 v3, v1, v103
	v_and_b32_e32 v2, 0xffff0000, v88
	v_mul_f32_e32 v4, v15, v87
	v_fma_f32 v6, -v208, v4, v2
	v_mul_f32_e32 v104, v72, v72
	s_waitcnt lgkmcnt(0)
	v_add_f32_e32 v2, v103, v3
	ds_bpermute_b32 v3, v203, v2
	v_fmac_f32_e32 v104, v83, v83
	v_fmac_f32_e32 v104, v62, v62
	v_fmac_f32_e32 v104, v90, v90
	ds_bpermute_b32 v12, v1, v104
	s_waitcnt lgkmcnt(1)
	v_add_f32_e32 v2, v2, v3
	ds_bpermute_b32 v3, v204, v2
	v_mul_f32_e32 v105, v71, v71
	v_fmac_f32_e32 v105, v68, v68
	v_lshlrev_b32_e32 v4, 16, v89
	v_mul_f32_e32 v5, v16, v86
	v_fmac_f32_e32 v105, v61, v61
	v_fma_f32 v5, -v208, v5, v4
	v_and_b32_e32 v4, 0xffff0000, v89
	v_mul_f32_e32 v11, v17, v85
	v_fmac_f32_e32 v105, v48, v48
	v_fma_f32 v4, -v208, v11, v4
	s_waitcnt lgkmcnt(0)
	v_add_f32_e32 v2, v2, v3
	v_add_f32_e32 v11, v104, v12
	ds_bpermute_b32 v3, v205, v2
	ds_bpermute_b32 v12, v203, v11
	ds_bpermute_b32 v13, v1, v105
	v_mul_f32_e32 v106, v70, v70
	v_fmac_f32_e32 v106, v67, v67
	s_waitcnt lgkmcnt(2)
	v_add_f32_e32 v2, v2, v3
	s_waitcnt lgkmcnt(1)
	v_add_f32_e32 v11, v11, v12
	s_waitcnt lgkmcnt(0)
	v_add_f32_e32 v13, v105, v13
	ds_bpermute_b32 v3, v206, v2
	ds_bpermute_b32 v12, v204, v11
	ds_bpermute_b32 v14, v203, v13
	v_fmac_f32_e32 v106, v60, v60
	v_fmac_f32_e32 v106, v47, v47
	s_waitcnt lgkmcnt(2)
	v_add_f32_e32 v2, v2, v3
	s_waitcnt lgkmcnt(1)
	v_add_f32_e32 v3, v11, v12
	s_waitcnt lgkmcnt(0)
	v_add_f32_e32 v12, v13, v14
	ds_bpermute_b32 v11, v205, v3
	ds_bpermute_b32 v13, v204, v12
	ds_bpermute_b32 v14, v1, v106
	v_fmamk_f32 v2, v2, 0x3c000000, v209
	v_rsq_f32_e32 v2, v2
	s_waitcnt lgkmcnt(2)
	v_add_f32_e32 v3, v3, v11
	s_waitcnt lgkmcnt(1)
	v_add_f32_e32 v12, v12, v13
	s_waitcnt lgkmcnt(0)
	v_add_f32_e32 v14, v106, v14
	ds_bpermute_b32 v11, v206, v3
	ds_bpermute_b32 v13, v205, v12
	ds_bpermute_b32 v15, v203, v14
	v_mul_f32_e32 v16, 0x3f4ccccd, v2
	v_mul_f32_e32 v107, v69, v69
	s_waitcnt lgkmcnt(2)
	v_add_f32_e32 v2, v3, v11
	s_waitcnt lgkmcnt(1)
	v_add_f32_e32 v3, v12, v13
	s_waitcnt lgkmcnt(0)
	v_add_f32_e32 v12, v14, v15
	ds_bpermute_b32 v11, v206, v3
	ds_bpermute_b32 v13, v204, v12
	v_fmac_f32_e32 v107, v66, v66
	v_fmac_f32_e32 v107, v59, v59
	v_fmac_f32_e32 v107, v46, v46
	s_waitcnt lgkmcnt(1)
	v_add_f32_e32 v3, v3, v11
	ds_bpermute_b32 v11, v1, v107
	s_waitcnt lgkmcnt(1)
	v_add_f32_e32 v12, v12, v13
	ds_bpermute_b32 v13, v205, v12
	v_fmamk_f32 v2, v2, 0x3c000000, v209
	v_rsq_f32_e32 v2, v2
	s_waitcnt lgkmcnt(1)
	v_add_f32_e32 v11, v107, v11
	ds_bpermute_b32 v14, v203, v11
	s_waitcnt lgkmcnt(1)
	v_add_f32_e32 v12, v12, v13
	v_fmamk_f32 v3, v3, 0x3c000000, v209
	ds_bpermute_b32 v13, v206, v12
	v_mul_f32_e32 v108, v55, v55
	v_rsq_f32_e32 v3, v3
	v_fmac_f32_e32 v108, v32, v32
	v_fmac_f32_e32 v108, v58, v58
	v_fmac_f32_e32 v108, v45, v45
	v_mul_f32_e32 v17, 0x3f4ccccd, v2
	s_waitcnt lgkmcnt(1)
	v_add_f32_e32 v2, v11, v14
	v_mul_f32_e32 v78, 0x3f4ccccd, v3
	ds_bpermute_b32 v3, v204, v2
	s_waitcnt lgkmcnt(1)
	v_add_f32_e32 v11, v12, v13
	ds_bpermute_b32 v12, v1, v108
	v_mul_f32_e32 v109, v54, v54
	v_fmac_f32_e32 v109, v30, v30
	v_fmac_f32_e32 v109, v57, v57
	v_fmac_f32_e32 v109, v44, v44
	s_waitcnt lgkmcnt(1)
	v_add_f32_e32 v2, v2, v3
	s_waitcnt lgkmcnt(0)
;     ...
;     for (int r = 0; r < 16; ++r) { float s = ss[r]; s += __shfl_xor(s, 1); s += __shfl_xor(s, 2); s += __shfl_xor(s, 4); s += __shfl_xor(s, 8); s += __shfl_xor(s, 16);
;         ss[r] = (1.0f - LAM_INIT) * __builtin_amdgcn_rsqf(s * (1.0f / 128.0f) + EPS); }
;     const float* sg = a->in[9]; float g4[4];
; #pragma unroll
;     for (int d0 = 0; d0 < 4; ++d0) g4[d0] = sg[d0 * 32 + r32];
	v_add_f32_e32 v12, v108, v12
	ds_bpermute_b32 v3, v205, v2
	ds_bpermute_b32 v13, v203, v12
	ds_bpermute_b32 v14, v1, v109
	v_mul_f32_e32 v110, v53, v53
	v_fmac_f32_e32 v110, v28, v28
	s_waitcnt lgkmcnt(2)
	v_add_f32_e32 v2, v2, v3
	s_waitcnt lgkmcnt(1)
	v_add_f32_e32 v12, v12, v13
	s_waitcnt lgkmcnt(0)
	v_add_f32_e32 v14, v109, v14
	ds_bpermute_b32 v3, v206, v2
	ds_bpermute_b32 v13, v204, v12
	ds_bpermute_b32 v15, v203, v14
	v_fmac_f32_e32 v110, v56, v56
	v_fmac_f32_e32 v110, v43, v43
	s_waitcnt lgkmcnt(2)
	v_add_f32_e32 v2, v2, v3
	s_waitcnt lgkmcnt(1)
	v_add_f32_e32 v3, v12, v13
	s_waitcnt lgkmcnt(0)
	v_add_f32_e32 v13, v14, v15
	ds_bpermute_b32 v12, v205, v3
	ds_bpermute_b32 v14, v204, v13
	ds_bpermute_b32 v15, v1, v110
	v_fmamk_f32 v2, v2, 0x3c000000, v209
	v_rsq_f32_e32 v2, v2
	s_waitcnt lgkmcnt(2)
	v_add_f32_e32 v3, v3, v12
	s_waitcnt lgkmcnt(1)
	v_add_f32_e32 v13, v13, v14
	s_waitcnt lgkmcnt(0)
	v_add_f32_e32 v15, v110, v15
	ds_bpermute_b32 v12, v206, v3
	ds_bpermute_b32 v14, v205, v13
	ds_bpermute_b32 v79, v203, v15
	v_mul_f32_e32 v111, v52, v52
	v_fmac_f32_e32 v111, v26, v26
	v_fmac_f32_e32 v111, v41, v41
	v_fmac_f32_e32 v111, v42, v42
	v_mul_f32_e32 v80, 0x3f4ccccd, v2
	s_waitcnt lgkmcnt(2)
	v_add_f32_e32 v2, v3, v12
	s_waitcnt lgkmcnt(1)
	v_add_f32_e32 v3, v13, v14
	s_waitcnt lgkmcnt(0)
	v_add_f32_e32 v13, v15, v79
	ds_bpermute_b32 v12, v206, v3
	ds_bpermute_b32 v14, v204, v13
	ds_bpermute_b32 v15, v1, v111
	v_fmamk_f32 v2, v2, 0x3c000000, v209
	v_mul_f32_e32 v112, v51, v51
	s_waitcnt lgkmcnt(2)
	v_add_f32_e32 v3, v3, v12
	s_waitcnt lgkmcnt(1)
	v_add_f32_e32 v12, v13, v14
	s_waitcnt lgkmcnt(0)
	v_add_f32_e32 v14, v111, v15
	ds_bpermute_b32 v13, v205, v12
	ds_bpermute_b32 v15, v203, v14
	v_rsq_f32_e32 v2, v2
	v_fmac_f32_e32 v112, v24, v24
	v_fmac_f32_e32 v112, v40, v40
	s_waitcnt lgkmcnt(1)
	v_add_f32_e32 v12, v12, v13
	s_waitcnt lgkmcnt(0)
	v_add_f32_e32 v14, v14, v15
	v_fmamk_f32 v3, v3, 0x3c000000, v209
	ds_bpermute_b32 v13, v206, v12
	ds_bpermute_b32 v15, v204, v14
	v_fmac_f32_e32 v112, v10, v10
	v_rsq_f32_e32 v3, v3
	v_mul_f32_e32 v79, 0x3f4ccccd, v2
	ds_bpermute_b32 v2, v1, v112
	v_mul_f32_e32 v77, v50, v50
	v_mul_f32_e32 v81, 0x3f4ccccd, v3
	s_waitcnt lgkmcnt(2)
	v_add_f32_e32 v3, v12, v13
	s_waitcnt lgkmcnt(1)
	v_add_f32_e32 v12, v14, v15
	ds_bpermute_b32 v13, v205, v12
	s_waitcnt lgkmcnt(1)
	v_add_f32_e32 v2, v112, v2
	v_fmac_f32_e32 v77, v23, v23
	ds_bpermute_b32 v14, v203, v2
	v_fmac_f32_e32 v77, v39, v39
	v_fmac_f32_e32 v77, v9, v9
	v_fmamk_f32 v3, v3, 0x3c000000, v209
	s_waitcnt lgkmcnt(1)
	v_add_f32_e32 v12, v12, v13
	ds_bpermute_b32 v13, v1, v77
	v_rsq_f32_e32 v3, v3
	s_waitcnt lgkmcnt(1)
	v_add_f32_e32 v2, v2, v14
	ds_bpermute_b32 v14, v204, v2
	ds_bpermute_b32 v15, v206, v12
	v_mul_f32_e32 v85, 0x3f4ccccd, v3
	s_waitcnt lgkmcnt(2)
	v_add_f32_e32 v3, v77, v13
	ds_bpermute_b32 v13, v203, v3
	s_waitcnt lgkmcnt(2)
	v_add_f32_e32 v2, v2, v14
	ds_bpermute_b32 v14, v205, v2
	v_mul_f32_e32 v76, v33, v33
	v_fmac_f32_e32 v76, v22, v22
	s_waitcnt lgkmcnt(1)
	v_add_f32_e32 v3, v3, v13
	v_fmac_f32_e32 v76, v38, v38
	ds_bpermute_b32 v13, v204, v3
	v_fmac_f32_e32 v76, v8, v8
	v_add_f32_e32 v12, v12, v15
	v_fmamk_f32 v12, v12, 0x3c000000, v209
	s_waitcnt lgkmcnt(1)
	v_add_f32_e32 v2, v2, v14
	ds_bpermute_b32 v14, v1, v76
	v_rsq_f32_e32 v12, v12
	s_waitcnt lgkmcnt(1)
	v_add_f32_e32 v3, v3, v13
	ds_bpermute_b32 v13, v205, v3
	v_mul_f32_e32 v75, v31, v31
	v_mul_f32_e32 v77, 0x3f4ccccd, v12
	s_waitcnt lgkmcnt(1)
	v_add_f32_e32 v12, v76, v14
	ds_bpermute_b32 v14, v203, v12
	s_waitcnt lgkmcnt(1)
	v_add_f32_e32 v3, v3, v13
	ds_bpermute_b32 v13, v206, v3
	v_fmac_f32_e32 v75, v21, v21
	ds_bpermute_b32 v15, v206, v2
	s_waitcnt lgkmcnt(2)
	v_add_f32_e32 v12, v12, v14
	ds_bpermute_b32 v14, v204, v12
	v_fmac_f32_e32 v75, v37, v37
	v_fmac_f32_e32 v75, v7, v7
	s_waitcnt lgkmcnt(2)
	v_add_f32_e32 v3, v3, v13
	ds_bpermute_b32 v13, v1, v75
	s_load_dwordx2 s[4:5], s[26:27], 0x48
	s_waitcnt lgkmcnt(0)
	v_add_f32_e32 v2, v2, v15
	v_add_f32_e32 v12, v12, v14
	v_fmamk_f32 v2, v2, 0x3c000000, v209
	ds_bpermute_b32 v14, v205, v12
	v_and_b32_e32 v82, 31, v164
	v_rsq_f32_e32 v2, v2
	v_lshlrev_b32_e32 v15, 2, v82
	v_add_f32_e32 v13, v75, v13
	v_fmamk_f32 v3, v3, 0x3c000000, v209
	global_load_dword v76, v15, s[4:5]
	global_load_dword v88, v15, s[4:5] offset:256
	ds_bpermute_b32 v75, v203, v13
	v_rsq_f32_e32 v3, v3
	v_mul_f32_e32 v86, 0x3f4ccccd, v2
	s_waitcnt lgkmcnt(1)
	v_add_f32_e32 v2, v12, v14
	ds_bpermute_b32 v12, v206, v2
	v_mul_f32_e32 v74, v29, v29
	v_fmac_f32_e32 v74, v20, v20
	v_mul_f32_e32 v87, 0x3f4ccccd, v3
	s_waitcnt lgkmcnt(1)
	v_add_f32_e32 v3, v13, v75
	global_load_dword v75, v15, s[4:5] offset:128
	v_fmac_f32_e32 v74, v36, v36
	v_fmac_f32_e32 v74, v6, v6
	s_waitcnt lgkmcnt(0)
	v_add_f32_e32 v2, v2, v12
	ds_bpermute_b32 v12, v1, v74
	ds_bpermute_b32 v13, v204, v3
	v_fmamk_f32 v2, v2, 0x3c000000, v209
	v_mul_f32_e32 v64, v25, v25
	v_rsq_f32_e32 v2, v2
	s_waitcnt lgkmcnt(1)
	v_add_f32_e32 v12, v74, v12
	global_load_dword v74, v15, s[4:5] offset:384
	s_waitcnt lgkmcnt(0)
	v_add_f32_e32 v3, v3, v13
	ds_bpermute_b32 v13, v205, v3
	ds_bpermute_b32 v14, v203, v12
	v_mul_f32_e32 v63, v27, v27
	v_fmac_f32_e32 v64, v18, v18
	v_fmac_f32_e32 v63, v19, v19
	s_waitcnt lgkmcnt(1)
	v_add_f32_e32 v3, v3, v13
	ds_bpermute_b32 v13, v206, v3
	v_fmac_f32_e32 v64, v34, v34
	v_fmac_f32_e32 v63, v35, v35
	v_fmac_f32_e32 v64, v4, v4
	v_fmac_f32_e32 v63, v5, v5
	s_waitcnt lgkmcnt(1)
	v_add_f32_e32 v12, v12, v14
	v_mul_f32_e32 v89, 0x3f4ccccd, v2
	s_waitcnt lgkmcnt(0)
	v_add_f32_e32 v2, v3, v13
	ds_bpermute_b32 v3, v1, v64
	ds_bpermute_b32 v14, v204, v12
	ds_bpermute_b32 v15, v1, v63
	s_lshl_b32 s4, s89, 5
	s_ashr_i32 s5, s4, 31
	s_waitcnt lgkmcnt(2)
; __device__ __forceinline__ int crow(int r, int hi) { return (r & 3) + 8 * (r >> 2) + 4 * hi; }
; __device__ __forceinline__ unsigned f2bf(float f) { unsigned u = __builtin_bit_cast(unsigned, f); return (u + 0x7fffu + ((u >> 16) & 1u)) >> 16; }
;     ...
;         ss[r] = (1.0f - LAM_INIT) * __builtin_amdgcn_rsqf(s * (1.0f / 128.0f) + EPS); }
;     const float* sg = a->in[9]; float g4[4];
; #pragma unroll
;     for (int d0 = 0; d0 < 4; ++d0) g4[d0] = sg[d0 * 32 + r32];
;     att::bf16* Ow = Obase + ((size_t)b * SEQ + (size_t)qb * 256 + wave_ * 32) * 2048 + 1024 + h * 128;
; #pragma unroll
;     for (int r = 0; r < 16; ++r) { const int orow = crow(r, hi);
; #pragma unroll
;         for (int d0 = 0; d0 < 4; ++d0) Ow[(size_t)orow * 2048 + d0 * 32 + r32] = (att::bf16)f2bf(o[d0][r] * ss[r] * g4[d0]); }
	v_add_f32_e32 v3, v64, v3
	s_waitcnt lgkmcnt(1)
	v_add_f32_e32 v12, v12, v14
	s_waitcnt lgkmcnt(0)
	v_add_f32_e32 v13, v63, v15
	ds_bpermute_b32 v63, v203, v3
	ds_bpermute_b32 v15, v205, v12
	ds_bpermute_b32 v14, v203, v13
	s_add_u32 s4, s4, s88
	s_addc_u32 s5, s5, 0
	s_waitcnt lgkmcnt(2)
	v_add_f32_e32 v3, v3, v63
	s_waitcnt lgkmcnt(1)
	v_add_f32_e32 v12, v12, v15
	ds_bpermute_b32 v15, v204, v3
	s_waitcnt lgkmcnt(1)
	v_add_f32_e32 v13, v13, v14
	ds_bpermute_b32 v14, v204, v13
	ds_bpermute_b32 v63, v206, v12
	v_fmamk_f32 v2, v2, 0x3c000000, v209
	s_waitcnt lgkmcnt(2)
	v_add_f32_e32 v3, v3, v15
	ds_bpermute_b32 v15, v205, v3
	s_waitcnt lgkmcnt(2)
	v_add_f32_e32 v13, v13, v14
	ds_bpermute_b32 v14, v205, v13
	s_waitcnt lgkmcnt(2)
	v_add_f32_e32 v12, v12, v63
	v_fmamk_f32 v12, v12, 0x3c000000, v209
	s_waitcnt lgkmcnt(1)
	v_add_f32_e32 v3, v3, v15
	ds_bpermute_b32 v15, v206, v3
	s_waitcnt lgkmcnt(1)
	v_add_f32_e32 v13, v13, v14
	ds_bpermute_b32 v14, v206, v13
	v_rsq_f32_e32 v12, v12
	s_lshl_b64 s[4:5], s[4:5], 12
	s_waitcnt lgkmcnt(1)
	v_add_f32_e32 v3, v3, v15
	v_fmamk_f32 v3, v3, 0x3c000000, v209
	v_rsq_f32_e32 v2, v2
	v_rsq_f32_e32 v3, v3
	s_add_u32 s4, s44, s4
	s_addc_u32 s5, s45, s5
	s_add_u32 s4, s4, s46
	s_waitcnt lgkmcnt(0)
	v_add_f32_e32 v13, v13, v14
	v_mul_f32_e32 v64, 0x3f4ccccd, v12
	s_addc_u32 s5, s5, s47
	v_lshlrev_b32_e32 v184, 1, v82
	v_lshlrev_b32_e32 v12, 9, v164
	v_mul_f32_e32 v14, v84, v16
	v_mul_f32_e32 v63, 0x3f4ccccd, v2
	v_mul_f32_e32 v92, 0x3f4ccccd, v3
	v_lshl_add_u64 v[2:3], s[4:5], 0, v[184:185]
	v_and_b32_e32 v184, 0x4000, v12
	s_waitcnt vmcnt(3)
	v_mul_f32_e32 v14, v14, v76
	v_lshl_add_u64 v[2:3], v[2:3], 0, v[184:185]
	v_bfe_u32 v15, v14, 16, 1
	v_fmamk_f32 v13, v13, 0x3c000000, v209
	v_add3_u32 v82, v14, v15, s61
	v_add_co_u32_e32 v14, vcc, s62, v2
	v_rsq_f32_e32 v13, v13
	s_nop 0
	v_addc_co_u32_e32 v15, vcc, 0, v3, vcc
	global_store_short_d16_hi v[14:15], v82, off offset:2048
	v_mul_f32_e32 v14, v73, v16
	s_waitcnt vmcnt(2)
	v_mul_f32_e32 v14, v14, v75
	v_bfe_u32 v15, v14, 16, 1
	v_mul_f32_e32 v91, 0x3f4ccccd, v13
	v_lshl_add_u64 v[12:13], v[2:3], 0, s[42:43]
	v_add3_u32 v14, v14, v15, s61
	global_store_short_d16_hi v[12:13], v14, off offset:64
	v_mul_f32_e32 v14, v65, v16
	v_mul_f32_e32 v14, v14, v88
	v_bfe_u32 v15, v14, 16, 1
	v_add3_u32 v14, v14, v15, s61
	global_store_short_d16_hi v[12:13], v14, off offset:128
	v_mul_f32_e32 v14, v49, v16
	s_waitcnt vmcnt(3)
	v_mul_f32_e32 v14, v14, v74
	v_bfe_u32 v15, v14, 16, 1
	v_add3_u32 v14, v14, v15, s61
	global_store_short_d16_hi v[12:13], v14, off offset:192
	v_mul_f32_e32 v12, v83, v17
	v_mul_f32_e32 v12, v12, v76
	v_bfe_u32 v13, v12, 16, 1
	v_add3_u32 v14, v12, v13, s61
	v_add_co_u32_e32 v12, vcc, s63, v2
	v_fmamk_f32 v11, v11, 0x3c000000, v209
	s_nop 0
	v_addc_co_u32_e32 v13, vcc, 0, v3, vcc
	global_store_short_d16_hi v[12:13], v14, off offset:2048
	v_mul_f32_e32 v14, v72, v17
	v_mul_f32_e32 v14, v14, v75
	v_bfe_u32 v15, v14, 16, 1
	v_add3_u32 v14, v14, v15, s61
	global_store_short_d16_hi v[12:13], v14, off offset:2112
	v_mul_f32_e32 v14, v62, v17
	v_mul_f32_e32 v14, v14, v88
	v_bfe_u32 v15, v14, 16, 1
	v_add3_u32 v14, v14, v15, s61
	global_store_short_d16_hi v[12:13], v14, off offset:2176
	v_mul_f32_e32 v14, v90, v17
	v_mul_f32_e32 v14, v14, v74
	v_bfe_u32 v15, v14, 16, 1
	v_add3_u32 v14, v14, v15, s61
	global_store_short_d16_hi v[12:13], v14, off offset:2240
	v_mul_f32_e32 v12, v68, v78
	v_mul_f32_e32 v12, v12, v76
	v_bfe_u32 v13, v12, 16, 1
	v_add3_u32 v14, v12, v13, s61
	v_add_co_u32_e32 v12, vcc, s64, v2
	v_rsq_f32_e32 v11, v11
	s_nop 0
	v_addc_co_u32_e32 v13, vcc, 0, v3, vcc
	global_store_short_d16_hi v[12:13], v14, off offset:2048
	v_mul_f32_e32 v14, v71, v78
	v_mul_f32_e32 v14, v14, v75
	v_bfe_u32 v15, v14, 16, 1
	v_add3_u32 v14, v14, v15, s61
	global_store_short_d16_hi v[12:13], v14, off offset:2112
	v_mul_f32_e32 v14, v61, v78
	v_mul_f32_e32 v14, v14, v88
	v_bfe_u32 v15, v14, 16, 1
	v_add3_u32 v14, v14, v15, s61
	global_store_short_d16_hi v[12:13], v14, off offset:2176
	v_mul_f32_e32 v14, v48, v78
	v_mul_f32_e32 v14, v14, v74
	v_bfe_u32 v15, v14, 16, 1
	v_mul_f32_e32 v11, 0x3f4ccccd, v11
	v_add3_u32 v14, v14, v15, s61
	global_store_short_d16_hi v[12:13], v14, off offset:2240
	v_mul_f32_e32 v12, v67, v11
	v_mul_f32_e32 v12, v12, v76
	v_bfe_u32 v13, v12, 16, 1
	v_add3_u32 v14, v12, v13, s61
	v_add_co_u32_e32 v12, vcc, s65, v2
	v_mul_f32_e32 v10, v10, v86
	s_nop 0
	v_addc_co_u32_e32 v13, vcc, 0, v3, vcc
	global_store_short_d16_hi v[12:13], v14, off offset:2048
	v_mul_f32_e32 v14, v70, v11
	v_mul_f32_e32 v14, v14, v75
	v_bfe_u32 v15, v14, 16, 1
	v_add3_u32 v14, v14, v15, s61
	global_store_short_d16_hi v[12:13], v14, off offset:2112
	v_mul_f32_e32 v14, v60, v11
	v_mul_f32_e32 v14, v14, v88
	v_bfe_u32 v15, v14, 16, 1
	v_mul_f32_e32 v11, v47, v11
	v_add3_u32 v14, v14, v15, s61
	v_mul_f32_e32 v11, v11, v74
	global_store_short_d16_hi v[12:13], v14, off offset:2176
	v_bfe_u32 v14, v11, 16, 1
	v_add3_u32 v11, v11, v14, s61
	global_store_short_d16_hi v[12:13], v11, off offset:2240
	v_mul_f32_e32 v11, v66, v80
	v_mul_f32_e32 v11, v11, v76
	v_bfe_u32 v12, v11, 16, 1
	v_add3_u32 v11, v11, v12, s61
	v_add_co_u32_e32 v12, vcc, s66, v2
	v_mul_f32_e32 v10, v10, v74
	s_nop 0
	v_addc_co_u32_e32 v13, vcc, 0, v3, vcc
	global_store_short_d16_hi v[12:13], v11, off offset:2048
	v_mul_f32_e32 v11, v69, v80
	v_mul_f32_e32 v11, v11, v75
	v_bfe_u32 v14, v11, 16, 1
	v_add3_u32 v11, v11, v14, s61
	global_store_short_d16_hi v[12:13], v11, off offset:2112
	v_mul_f32_e32 v11, v59, v80
	v_mul_f32_e32 v11, v11, v88
	v_bfe_u32 v14, v11, 16, 1
	v_add3_u32 v11, v11, v14, s61
; __device__ __forceinline__ int crow(int r, int hi) { return (r & 3) + 8 * (r >> 2) + 4 * hi; }
; __device__ __forceinline__ unsigned f2bf(float f) { unsigned u = __builtin_bit_cast(unsigned, f); return (u + 0x7fffu + ((u >> 16) & 1u)) >> 16; }
;     ...
;     att::bf16* Ow = Obase + ((size_t)b * SEQ + (size_t)qb * 256 + wave_ * 32) * 2048 + 1024 + h * 128;
; #pragma unroll
;     for (int r = 0; r < 16; ++r) { const int orow = crow(r, hi);
; #pragma unroll
;         for (int d0 = 0; d0 < 4; ++d0) Ow[(size_t)orow * 2048 + d0 * 32 + r32] = (att::bf16)f2bf(o[d0][r] * ss[r] * g4[d0]); }
	global_store_short_d16_hi v[12:13], v11, off offset:2176
	v_mul_f32_e32 v11, v46, v80
	v_mul_f32_e32 v11, v11, v74
	v_bfe_u32 v14, v11, 16, 1
	v_add3_u32 v11, v11, v14, s61
	global_store_short_d16_hi v[12:13], v11, off offset:2240
	v_mul_f32_e32 v11, v32, v79
	v_mul_f32_e32 v11, v11, v76
	v_bfe_u32 v12, v11, 16, 1
	v_add3_u32 v11, v11, v12, s61
	v_add_co_u32_e32 v12, vcc, s67, v2
	v_mul_f32_e32 v9, v9, v87
	s_nop 0
	v_addc_co_u32_e32 v13, vcc, 0, v3, vcc
	global_store_short_d16_hi v[12:13], v11, off offset:2048
	v_mul_f32_e32 v11, v55, v79
	v_mul_f32_e32 v11, v11, v75
	v_bfe_u32 v14, v11, 16, 1
	v_add3_u32 v11, v11, v14, s61
	global_store_short_d16_hi v[12:13], v11, off offset:2112
	v_mul_f32_e32 v11, v58, v79
	v_mul_f32_e32 v11, v11, v88
	v_bfe_u32 v14, v11, 16, 1
	v_add3_u32 v11, v11, v14, s61
	global_store_short_d16_hi v[12:13], v11, off offset:2176
	v_mul_f32_e32 v11, v45, v79
	v_mul_f32_e32 v11, v11, v74
	v_bfe_u32 v14, v11, 16, 1
	v_add3_u32 v11, v11, v14, s61
	global_store_short_d16_hi v[12:13], v11, off offset:2240
	v_mul_f32_e32 v11, v30, v81
	v_mul_f32_e32 v11, v11, v76
	v_bfe_u32 v12, v11, 16, 1
	v_add3_u32 v11, v11, v12, s61
	v_add_co_u32_e32 v12, vcc, s68, v2
	v_mul_f32_e32 v9, v9, v74
	s_nop 0
	v_addc_co_u32_e32 v13, vcc, 0, v3, vcc
	global_store_short_d16_hi v[12:13], v11, off offset:2048
	v_mul_f32_e32 v11, v54, v81
	v_mul_f32_e32 v11, v11, v75
	v_bfe_u32 v14, v11, 16, 1
	v_add3_u32 v11, v11, v14, s61
	global_store_short_d16_hi v[12:13], v11, off offset:2112
	v_mul_f32_e32 v11, v57, v81
	v_mul_f32_e32 v11, v11, v88
	v_bfe_u32 v14, v11, 16, 1
	v_add3_u32 v11, v11, v14, s61
	global_store_short_d16_hi v[12:13], v11, off offset:2176
	v_mul_f32_e32 v11, v44, v81
	v_mul_f32_e32 v11, v11, v74
	v_bfe_u32 v14, v11, 16, 1
	v_add3_u32 v11, v11, v14, s61
	global_store_short_d16_hi v[12:13], v11, off offset:2240
	v_mul_f32_e32 v11, v28, v85
	v_mul_f32_e32 v11, v11, v76
	v_bfe_u32 v12, v11, 16, 1
	v_add3_u32 v11, v11, v12, s61
	v_add_co_u32_e32 v12, vcc, s69, v2
	v_mul_f32_e32 v8, v8, v89
	s_nop 0
	v_addc_co_u32_e32 v13, vcc, 0, v3, vcc
	global_store_short_d16_hi v[12:13], v11, off offset:2048
	v_mul_f32_e32 v11, v53, v85
	v_mul_f32_e32 v11, v11, v75
	v_bfe_u32 v14, v11, 16, 1
	v_add3_u32 v11, v11, v14, s61
	global_store_short_d16_hi v[12:13], v11, off offset:2112
	v_mul_f32_e32 v11, v56, v85
	v_mul_f32_e32 v11, v11, v88
	v_bfe_u32 v14, v11, 16, 1
	v_add3_u32 v11, v11, v14, s61
	global_store_short_d16_hi v[12:13], v11, off offset:2176
	v_mul_f32_e32 v11, v43, v85
	v_mul_f32_e32 v11, v11, v74
	v_bfe_u32 v14, v11, 16, 1
	v_add3_u32 v11, v11, v14, s61
	global_store_short_d16_hi v[12:13], v11, off offset:2240
	v_mul_f32_e32 v11, v26, v77
	v_mul_f32_e32 v11, v11, v76
	v_bfe_u32 v12, v11, 16, 1
	v_add3_u32 v11, v11, v12, s61
	v_add_co_u32_e32 v12, vcc, s74, v2
	v_mul_f32_e32 v8, v8, v74
	s_nop 0
	v_addc_co_u32_e32 v13, vcc, 0, v3, vcc
	global_store_short_d16_hi v[12:13], v11, off offset:2048
	v_mul_f32_e32 v11, v52, v77
	v_mul_f32_e32 v11, v11, v75
	v_bfe_u32 v14, v11, 16, 1
	v_add3_u32 v11, v11, v14, s61
	global_store_short_d16_hi v[12:13], v11, off offset:2112
	v_mul_f32_e32 v11, v41, v77
	v_mul_f32_e32 v11, v11, v88
	v_bfe_u32 v14, v11, 16, 1
	v_add3_u32 v11, v11, v14, s61
	global_store_short_d16_hi v[12:13], v11, off offset:2176
	v_mul_f32_e32 v11, v42, v77
	v_mul_f32_e32 v11, v11, v74
	v_bfe_u32 v14, v11, 16, 1
	v_add3_u32 v11, v11, v14, s61
	global_store_short_d16_hi v[12:13], v11, off offset:2240
	v_mul_f32_e32 v11, v24, v86
	v_mul_f32_e32 v11, v11, v76
	v_bfe_u32 v12, v11, 16, 1
	v_add3_u32 v11, v11, v12, s61
	v_add_co_u32_e32 v12, vcc, s75, v2
	v_mul_f32_e32 v7, v7, v63
	s_nop 0
	v_addc_co_u32_e32 v13, vcc, 0, v3, vcc
	global_store_short_d16_hi v[12:13], v11, off offset:2048
	v_mul_f32_e32 v11, v51, v86
	v_mul_f32_e32 v11, v11, v75
	v_bfe_u32 v14, v11, 16, 1
	v_add3_u32 v11, v11, v14, s61
	global_store_short_d16_hi v[12:13], v11, off offset:2112
	v_mul_f32_e32 v11, v40, v86
	v_mul_f32_e32 v11, v11, v88
	v_bfe_u32 v14, v11, 16, 1
	v_add3_u32 v11, v11, v14, s61
	global_store_short_d16_hi v[12:13], v11, off offset:2176
	v_bfe_u32 v11, v10, 16, 1
	v_add3_u32 v10, v10, v11, s61
	global_store_short_d16_hi v[12:13], v10, off offset:2240
	v_mul_f32_e32 v10, v23, v87
	v_mul_f32_e32 v10, v10, v76
; __device__ __forceinline__ int crow(int r, int hi) { return (r & 3) + 8 * (r >> 2) + 4 * hi; }
; __device__ __forceinline__ unsigned f2bf(float f) { unsigned u = __builtin_bit_cast(unsigned, f); return (u + 0x7fffu + ((u >> 16) & 1u)) >> 16; }
;     ...
;     att::bf16* Ow = Obase + ((size_t)b * SEQ + (size_t)qb * 256 + wave_ * 32) * 2048 + 1024 + h * 128;
; #pragma unroll
;     for (int r = 0; r < 16; ++r) { const int orow = crow(r, hi);
; #pragma unroll
;         for (int d0 = 0; d0 < 4; ++d0) Ow[(size_t)orow * 2048 + d0 * 32 + r32] = (att::bf16)f2bf(o[d0][r] * ss[r] * g4[d0]); }
	v_bfe_u32 v11, v10, 16, 1
	v_add3_u32 v12, v10, v11, s61
	v_add_co_u32_e32 v10, vcc, s76, v2
	v_mul_f32_e32 v7, v7, v74
	s_nop 0
	v_addc_co_u32_e32 v11, vcc, 0, v3, vcc
	global_store_short_d16_hi v[10:11], v12, off offset:2048
	v_mul_f32_e32 v12, v50, v87
	v_mul_f32_e32 v12, v12, v75
	v_bfe_u32 v13, v12, 16, 1
	v_add3_u32 v12, v12, v13, s61
	global_store_short_d16_hi v[10:11], v12, off offset:2112
	v_mul_f32_e32 v12, v39, v87
	v_mul_f32_e32 v12, v12, v88
	v_bfe_u32 v13, v12, 16, 1
	v_add3_u32 v12, v12, v13, s61
	global_store_short_d16_hi v[10:11], v12, off offset:2176
	v_bfe_u32 v12, v9, 16, 1
	v_add3_u32 v9, v9, v12, s61
	global_store_short_d16_hi v[10:11], v9, off offset:2240
	v_mul_f32_e32 v9, v22, v89
	v_mul_f32_e32 v9, v9, v76
	v_bfe_u32 v10, v9, 16, 1
	v_add3_u32 v9, v9, v10, s61
	v_add_co_u32_e32 v10, vcc, s77, v2
	v_mul_f32_e32 v6, v6, v64
	s_nop 0
	v_addc_co_u32_e32 v11, vcc, 0, v3, vcc
	global_store_short_d16_hi v[10:11], v9, off offset:2048
	v_mul_f32_e32 v9, v33, v89
	v_mul_f32_e32 v9, v9, v75
	v_bfe_u32 v12, v9, 16, 1
	v_add3_u32 v9, v9, v12, s61
	global_store_short_d16_hi v[10:11], v9, off offset:2112
	v_mul_f32_e32 v9, v38, v89
	v_mul_f32_e32 v9, v9, v88
	v_bfe_u32 v12, v9, 16, 1
	v_add3_u32 v9, v9, v12, s61
	global_store_short_d16_hi v[10:11], v9, off offset:2176
	v_bfe_u32 v9, v8, 16, 1
	v_add3_u32 v8, v8, v9, s61
	global_store_short_d16_hi v[10:11], v8, off offset:2240
	v_mul_f32_e32 v8, v21, v63
	v_mul_f32_e32 v8, v8, v76
	v_bfe_u32 v9, v8, 16, 1
	v_add3_u32 v10, v8, v9, s61
	v_add_co_u32_e32 v8, vcc, s78, v2
	v_mul_f32_e32 v6, v6, v74
	s_nop 0
	v_addc_co_u32_e32 v9, vcc, 0, v3, vcc
	global_store_short_d16_hi v[8:9], v10, off offset:2048
	v_mul_f32_e32 v10, v31, v63
	v_mul_f32_e32 v10, v10, v75
	v_bfe_u32 v11, v10, 16, 1
	v_add3_u32 v10, v10, v11, s61
	global_store_short_d16_hi v[8:9], v10, off offset:2112
	v_mul_f32_e32 v10, v37, v63
	v_mul_f32_e32 v10, v10, v88
	v_bfe_u32 v11, v10, 16, 1
	v_add3_u32 v10, v10, v11, s61
	global_store_short_d16_hi v[8:9], v10, off offset:2176
	v_bfe_u32 v10, v7, 16, 1
	v_add3_u32 v7, v7, v10, s61
	global_store_short_d16_hi v[8:9], v7, off offset:2240
	v_mul_f32_e32 v7, v20, v64
	v_mul_f32_e32 v7, v7, v76
	v_bfe_u32 v8, v7, 16, 1
	v_add3_u32 v7, v7, v8, s61
	v_add_co_u32_e32 v8, vcc, s79, v2
	v_mul_f32_e32 v5, v5, v91
	s_nop 0
	v_addc_co_u32_e32 v9, vcc, 0, v3, vcc
	global_store_short_d16_hi v[8:9], v7, off offset:2048
	v_mul_f32_e32 v7, v29, v64
	v_mul_f32_e32 v7, v7, v75
	v_bfe_u32 v10, v7, 16, 1
	v_add3_u32 v7, v7, v10, s61
	global_store_short_d16_hi v[8:9], v7, off offset:2112
	v_mul_f32_e32 v7, v36, v64
	v_mul_f32_e32 v7, v7, v88
	v_bfe_u32 v10, v7, 16, 1
	v_add3_u32 v7, v7, v10, s61
	global_store_short_d16_hi v[8:9], v7, off offset:2176
	v_bfe_u32 v7, v6, 16, 1
	v_add3_u32 v6, v6, v7, s61
	global_store_short_d16_hi v[8:9], v6, off offset:2240
	v_mul_f32_e32 v6, v19, v91
	v_mul_f32_e32 v6, v6, v76
	v_bfe_u32 v7, v6, 16, 1
	v_add3_u32 v8, v6, v7, s61
	v_add_co_u32_e32 v6, vcc, s80, v2
	v_mul_f32_e32 v5, v5, v74
	s_nop 0
	v_addc_co_u32_e32 v7, vcc, 0, v3, vcc
	global_store_short_d16_hi v[6:7], v8, off offset:2048
	v_mul_f32_e32 v8, v27, v91
	v_mul_f32_e32 v8, v8, v75
	v_bfe_u32 v9, v8, 16, 1
	v_add3_u32 v8, v8, v9, s61
	global_store_short_d16_hi v[6:7], v8, off offset:2112
	v_mul_f32_e32 v8, v35, v91
	v_mul_f32_e32 v8, v8, v88
	v_bfe_u32 v9, v8, 16, 1
	v_add3_u32 v8, v8, v9, s61
	global_store_short_d16_hi v[6:7], v8, off offset:2176
	v_bfe_u32 v8, v5, 16, 1
	v_add3_u32 v5, v5, v8, s61
	global_store_short_d16_hi v[6:7], v5, off offset:2240
	v_mul_f32_e32 v5, v18, v92
	v_mul_f32_e32 v5, v76, v5
	v_bfe_u32 v6, v5, 16, 1
	v_add_co_u32_e32 v2, vcc, s81, v2
	v_add3_u32 v5, v5, v6, s61
	s_nop 0
	v_addc_co_u32_e32 v3, vcc, 0, v3, vcc
	global_store_short_d16_hi v[2:3], v5, off offset:2048
	v_mul_f32_e32 v5, v25, v92
	v_mul_f32_e32 v5, v75, v5
	v_bfe_u32 v6, v5, 16, 1
	v_add3_u32 v5, v5, v6, s61
	global_store_short_d16_hi v[2:3], v5, off offset:2112
	v_mul_f32_e32 v5, v34, v92
	v_mul_f32_e32 v5, v88, v5
	v_bfe_u32 v6, v5, 16, 1
	v_mul_f32_e32 v4, v4, v92
	v_add3_u32 v5, v5, v6, s61
	v_mul_f32_e32 v4, v74, v4
	global_store_short_d16_hi v[2:3], v5, off offset:2176
	v_bfe_u32 v5, v4, 16, 1
	v_add3_u32 v4, v4, v5, s61
	global_store_short_d16_hi v[2:3], v4, off offset:2240

; #define ATT_SBAR() __builtin_amdgcn_sched_barrier(0)
; __device__ __forceinline__ unsigned cvtpk(float lo, float hi) { f32x2_t v = {lo, hi}; bf16x2_t b = __builtin_convertvector(v, bf16x2_t); return __builtin_bit_cast(unsigned, b); }
; __device__ __forceinline__ int v_rd_base(int lane) { return ((lane & 3) << 3) | (((lane >> 2) & 3) << 6) | (((lane >> 4) & 1) << 5) | (((lane >> 5) & 1) << 8); }
; #define ATT_WRITE_K(so) do { *(bf16x8*)(K_lds + (so) + kswz<DQK>(kr, kc * 2)) = sk0; if constexpr (DQK == 128) *(bf16x8*)(K_lds + (so) + kswz<DQK>(32 + kr, kc * 2)) = sk1; } while (0)
; #define ATT_WRITE_V(so) do { *(bf16x8*)(V_lds + (so) + vst0) = sv0; *(bf16x8*)(V_lds + (so) + vst1) = sv1; } while (0)
; #define ATT_BAR() do { ATT_SBAR(); asm volatile("s_barrier" ::: "memory"); ATT_SBAR(); } while (0)
; #define ATT_SOFTMAX(first_) do { const float pm_ = softmax_rowmax(p0, p1); \
;     if (__builtin_expect((first_) || !__all(pm_ <= THRL), 0)) { const float al_ = softmax_shift(p0, p1, negm, pm_, (first_)); ATT_RESC(al_); } \
;     softmax_exp_pack(p0, p1, pa0, pa1, pa2, pa3); } while (0)
;     ...
;   asm volatile("s_waitcnt lgkmcnt(0)" ::: "memory"); ATT_BAR();
;   if (grp == 1) ATT_BAR();
;   qkt<DQK>(p0, p1, K_lds, qr, r32, hi);
;   ATT_BAR();
;   int k1 = SHM_K, k2 = 2 * SHM_K, k0 = 0, v0 = 0, v1 = SHM_V, v2 = 2 * SHM_V;
;   const lds_cptr kq0 = (lds_cptr)K_lds, vq0 = (lds_cptr)V_lds + v_rd_base(lane);
;   bf16x8 kf[8]; s16x4 va[8], vc[8];
;     ...
;   for (int t = 0; t + 1 < NT; ++t) {
;     if constexpr (ABL & 1) { u32x4 w0 = {cvtpk(p0[0], p0[1]), cvtpk(p0[2], p0[3]), cvtpk(p0[4], p0[5]), cvtpk(p0[6], p0[7])}, w1 = {cvtpk(p0[8], p0[9]), cvtpk(p0[10], p0[11]), cvtpk(p0[12], p0[13]), cvtpk(p0[14], p0[15])};
;         u32x4 w2 = {cvtpk(p1[0], p1[1]), cvtpk(p1[2], p1[3]), cvtpk(p1[4], p1[5]), cvtpk(p1[6], p1[7])}, w3 = {cvtpk(p1[8], p1[9]), cvtpk(p1[10], p1[11]), cvtpk(p1[12], p1[13]), cvtpk(p1[14], p1[15])};
;         pa0 = *reinterpret_cast<bf16x8*>(&w0); pa1 = *reinterpret_cast<bf16x8*>(&w1); pa2 = *reinterpret_cast<bf16x8*>(&w2); pa3 = *reinterpret_cast<bf16x8*>(&w3); }
;     else { ATT_SOFTMAX(t == 0); }
;     if constexpr (!(ABL & 4)) { ATT_WRITE_K(k2); ATT_WRITE_V(v1); }
;     ATT_SBAR();
; #pragma unroll
;     for (int ks = 0; ks < 4; ++ks) ATT_VPAIR(va, v0, 0, ks);
;     asm volatile("s_waitcnt lgkmcnt(8)" ::: "memory"); ATT_BAR();
.LBB0_264:
	v_mul_u32_u24_e32 v18, 0x110, v213
	v_add3_u32 v69, 0, v184, v18
	ds_read_b128 v[18:21], v69 offset:49152
	v_mad_u32_u24 v188, v213, s54, 0
	v_add_u32_e32 v192, v188, v184
	ds_read_b128 v[34:37], v192 offset:57856
	ds_read_b128 v[70:73], v69 offset:49184
	ds_read_b128 v[74:77], v69 offset:49216
	s_and_b32 s4, s89, 0x3fffffc0
	s_lshl_b32 s4, s4, 2
	s_add_i32 s90, s4, 0
	s_add_i32 s90, s90, 0x23080
	s_waitcnt lgkmcnt(3)
	v_mfma_f32_32x32x16_bf16 v[18:33], v[18:21], v[136:139], 0
	s_mov_b32 s95, 1
	s_waitcnt lgkmcnt(2)
	v_mfma_f32_32x32x16_bf16 v[34:49], v[34:37], v[136:139], 0
	s_waitcnt lgkmcnt(1)
	v_mfma_f32_32x32x16_bf16 v[18:33], v[70:73], v[140:143], v[18:33]
	ds_read_b128 v[70:73], v69 offset:57888
	ds_read_b128 v[78:81], v69 offset:49376
	s_waitcnt lgkmcnt(1)
	v_mfma_f32_32x32x16_bf16 v[34:49], v[70:73], v[140:143], v[34:49]
	v_mfma_f32_32x32x16_bf16 v[18:33], v[74:77], v[144:147], v[18:33]
	ds_read_b128 v[70:73], v69 offset:57920
	ds_read_b128 v[74:77], v69 offset:57952
	s_waitcnt lgkmcnt(1)
	v_mfma_f32_32x32x16_bf16 v[34:49], v[70:73], v[144:147], v[34:49]
	ds_read_b128 v[70:73], v69 offset:49248
	ds_read_b128 v[82:85], v69 offset:49280
	s_waitcnt lgkmcnt(1)
	v_mfma_f32_32x32x16_bf16 v[18:33], v[70:73], v[148:151], v[18:33]
	v_mfma_f32_32x32x16_bf16 v[34:49], v[74:77], v[148:151], v[34:49]
	ds_read_b128 v[70:73], v69 offset:57984
	ds_read_b128 v[74:77], v69 offset:58016
	s_waitcnt lgkmcnt(2)
	v_mfma_f32_32x32x16_bf16 v[18:33], v[82:85], v[152:155], v[18:33]
	s_waitcnt lgkmcnt(1)
	v_mfma_f32_32x32x16_bf16 v[34:49], v[70:73], v[152:155], v[34:49]
	ds_read_b128 v[70:73], v69 offset:49312
	ds_read_b128 v[82:85], v69 offset:49344
	s_waitcnt lgkmcnt(1)
	v_mfma_f32_32x32x16_bf16 v[18:33], v[70:73], v[156:159], v[18:33]
	v_mfma_f32_32x32x16_bf16 v[34:49], v[74:77], v[156:159], v[34:49]
	ds_read_b128 v[70:73], v69 offset:58048
	ds_read_b128 v[74:77], v69 offset:58080
	v_and_b32_e32 v69, 63, v212
	s_waitcnt lgkmcnt(2)
	v_mfma_f32_32x32x16_bf16 v[18:33], v[82:85], v[160:163], v[18:33]
	s_waitcnt lgkmcnt(1)
	v_mfma_f32_32x32x16_bf16 v[34:49], v[70:73], v[160:163], v[34:49]
	v_lshlrev_b32_e32 v70, 3, v69
	v_lshlrev_b32_e32 v72, 4, v69
	v_lshlrev_b32_e32 v73, 1, v69
	v_and_b32_e32 v71, 24, v70
	v_and_b32_e32 v72, 0xc0, v72
	v_and_b32_e32 v73, 32, v73
	v_and_b32_e32 v70, 0x100, v70
	v_mfma_f32_32x32x16_bf16 v[18:33], v[78:81], v[164:167], v[18:33]
	s_waitcnt lgkmcnt(0)
	v_mfma_f32_32x32x16_bf16 v[34:49], v[74:77], v[164:167], v[34:49]
	s_barrier
	v_add3_u32 v71, 0, v71, v72
	v_add3_u32 v131, v71, v73, v70
	v_cmp_gt_u32_e64 s[4:5], 32, v69
	s_nop 8
	v_add_f32_e32 v69, 0, v34
	v_max3_f32 v70, v69, v18, v19
	v_max3_f32 v70, v70, v20, v21
	v_max3_f32 v70, v70, v22, v23
	v_max3_f32 v70, v70, v24, v25
	v_max3_f32 v70, v70, v26, v27
	v_max3_f32 v70, v70, v28, v29
	v_max3_f32 v70, v70, v30, v31
	v_max3_f32 v70, v70, v32, v33
	s_nop 4
	v_lshl_add_u32 v187, v213, 2, s90
	v_max3_f32 v69, v70, v35, v36
	v_max3_f32 v69, v69, v37, v38
	v_max3_f32 v69, v69, v39, v40
	v_max3_f32 v69, v69, v41, v42
	v_max3_f32 v69, v69, v43, v44
	v_max3_f32 v69, v69, v45, v46
	v_max3_f32 v69, v69, v47, v48
	v_max_f32 v69, v69, v49
	s_nop 0
	v_mov_b32_e32 v70, v69
	s_nop 1
	v_permlane32_swap_b32_e32 v69, v70
	v_max_f32_e32 v70, v70, v70
	v_max_f32_e32 v69, v69, v69
	v_max_f32_e32 v69, v69, v70
	v_sub_f32_e32 v18, v18, v69
	v_sub_f32_e32 v34, v34, v69
	v_sub_f32_e32 v19, v19, v69
	v_sub_f32_e32 v35, v35, v69
	v_sub_f32_e32 v20, v20, v69
	v_sub_f32_e32 v36, v36, v69
	v_sub_f32_e32 v21, v21, v69
	v_sub_f32_e32 v37, v37, v69
	v_sub_f32_e32 v22, v22, v69
	v_sub_f32_e32 v38, v38, v69
	v_sub_f32_e32 v23, v23, v69
	v_sub_f32_e32 v39, v39, v69
	v_sub_f32_e32 v24, v24, v69
	v_sub_f32_e32 v40, v40, v69
	v_sub_f32_e32 v25, v25, v69
	v_sub_f32_e32 v41, v41, v69
	v_sub_f32_e32 v26, v26, v69
	v_sub_f32_e32 v42, v42, v69
	v_sub_f32_e32 v27, v27, v69
	v_sub_f32_e32 v43, v43, v69
	v_sub_f32_e32 v28, v28, v69
	v_sub_f32_e32 v44, v44, v69
	v_sub_f32_e32 v29, v29, v69
	v_sub_f32_e32 v45, v45, v69
	v_sub_f32_e32 v30, v30, v69
	v_sub_f32_e32 v46, v46, v69
	v_sub_f32_e32 v31, v31, v69
	v_sub_f32_e32 v47, v47, v69
	v_sub_f32_e32 v32, v32, v69
	v_sub_f32_e32 v48, v48, v69
	v_sub_f32_e32 v33, v33, v69
	v_sub_f32_e32 v49, v49, v69
	v_exp_f32_e32 v18, v18
	v_exp_f32_e32 v34, v34
	v_exp_f32_e32 v19, v19
	v_exp_f32_e32 v35, v35
	v_exp_f32_e32 v20, v20
	v_exp_f32_e32 v36, v36
	v_exp_f32_e32 v21, v21
	v_exp_f32_e32 v37, v37
	v_exp_f32_e32 v22, v22
	v_exp_f32_e32 v38, v38
	v_exp_f32_e32 v23, v23
	v_exp_f32_e32 v39, v39
	v_exp_f32_e32 v24, v24
	v_exp_f32_e32 v40, v40
	v_exp_f32_e32 v25, v25
	v_exp_f32_e32 v41, v41
	v_exp_f32_e32 v26, v26
	v_exp_f32_e32 v42, v42
	v_exp_f32_e32 v27, v27
	v_exp_f32_e32 v43, v43
	v_exp_f32_e32 v28, v28
	v_exp_f32_e32 v44, v44
	v_exp_f32_e32 v29, v29
	v_exp_f32_e32 v45, v45
	v_exp_f32_e32 v30, v30
	v_exp_f32_e32 v46, v46
	v_exp_f32_e32 v31, v31
	v_exp_f32_e32 v47, v47
	v_exp_f32_e32 v32, v32
	v_exp_f32_e32 v48, v48
	v_exp_f32_e32 v33, v33
	v_exp_f32_e32 v49, v49
	v_sub_f32_e32 v82, 0, v69
	v_mov_b32_e32 v83, v82
	v_mov_b32_e32 v84, v82
	v_mov_b32_e32 v85, v82
	v_mov_b32_e32 v86, v82
	v_mov_b32_e32 v87, v82
	v_mov_b32_e32 v88, v82
	v_mov_b32_e32 v89, v82
	v_mov_b32_e32 v90, v82
	v_mov_b32_e32 v91, v82
	v_mov_b32_e32 v92, v82
	v_mov_b32_e32 v93, v82
	v_mov_b32_e32 v94, v82
	v_mov_b32_e32 v95, v82
	v_mov_b32_e32 v96, v82
	v_mov_b32_e32 v97, v82
	v_cvt_pk_bf16_f32 v98, v18, v19
	v_cvt_pk_bf16_f32 v99, v20, v21
	v_cvt_pk_bf16_f32 v100, v22, v23
	v_cvt_pk_bf16_f32 v101, v24, v25
	v_cvt_pk_bf16_f32 v102, v26, v27
	v_cvt_pk_bf16_f32 v103, v28, v29
	v_cvt_pk_bf16_f32 v104, v30, v31
	v_cvt_pk_bf16_f32 v105, v32, v33
	v_cvt_pk_bf16_f32 v106, v34, v35
	v_cvt_pk_bf16_f32 v107, v36, v37
	v_cvt_pk_bf16_f32 v108, v38, v39
	v_cvt_pk_bf16_f32 v109, v40, v41
	v_cvt_pk_bf16_f32 v110, v42, v43
	v_cvt_pk_bf16_f32 v111, v44, v45
	v_cvt_pk_bf16_f32 v112, v46, v47
	v_cvt_pk_bf16_f32 v113, v48, v49
	v_add_u32_e32 v18, 0x14800, v66
	s_waitcnt vmcnt(3)
	ds_write_b128 v18, v[50:53]
	s_waitcnt vmcnt(2)
	ds_write_b128 v18, v[54:57] offset:8704
	s_waitcnt vmcnt(1)
	ds_write_b128 v67, v[58:61] offset:16384
	s_waitcnt vmcnt(0)
	ds_write_b128 v68, v[62:65] offset:16384
	ds_read_b64_tr_b16 v[18:19], v131
	ds_read_b64_tr_b16 v[20:21], v131 offset:2048
	ds_read_b64_tr_b16 v[34:35], v131 offset:4096
	ds_read_b64_tr_b16 v[36:37], v131 offset:6144
	ds_read_b64_tr_b16 v[38:39], v131 offset:8192
	ds_read_b64_tr_b16 v[40:41], v131 offset:10240
	ds_read_b64_tr_b16 v[42:43], v131 offset:12288
	ds_read_b64_tr_b16 v[44:45], v131 offset:14336
	s_waitcnt lgkmcnt(8)
	s_barrier
; #define ATT_LOAD_K(t) do { const unsigned so_ = (unsigned)(t) * (unsigned)(KVBLK * LDK * 2); sk0 = __builtin_bit_cast(bf16x8, __builtin_amdgcn_raw_buffer_load_b128(krs, koff, so_, 0)); \
;     if constexpr (DQK == 128) sk1 = __builtin_bit_cast(bf16x8, __builtin_amdgcn_raw_buffer_load_b128(krs, koff, so_ + (unsigned)(32 * LDK * 2), 0)); } while (0)
; #define ATT_LOAD_V(t) do { const unsigned so_ = (unsigned)(t) * (unsigned)(KVBLK * LDV * 2); sv0 = __builtin_bit_cast(bf16x8, __builtin_amdgcn_raw_buffer_load_b128(vrs, voff, so_, 0)); \
;     sv1 = __builtin_bit_cast(bf16x8, __builtin_amdgcn_raw_buffer_load_b128(vrs, voff, so_ + (unsigned)(32 * LDV * 2), 0)); } while (0)
; #define ATT_BAR() do { ATT_SBAR(); asm volatile("s_barrier" ::: "memory"); ATT_SBAR(); } while (0)
;     ...
;     ATT_XSECTION(true);
;     if constexpr (!(ABL & 4)) { const int tk = (t + 3 < NT) ? t + 3 : NT - 1, tv = (t + 2 < NT) ? t + 2 : NT - 1; ATT_LOAD_K(tk); ATT_LOAD_V(tv); }
;     ATT_BAR();
	s_setprio 2
	s_waitcnt lgkmcnt(6)
	v_mfma_f32_32x32x16_bf16 v[18:33], v[98:101], v[18:21], 0
	ds_read_b64_tr_b16 v[46:47], v131 offset:512
	ds_read_b64_tr_b16 v[48:49], v131 offset:2560
	s_waitcnt lgkmcnt(6)
	v_mfma_f32_32x32x16_bf16 v[18:33], v[102:105], v[34:37], v[18:33]
	ds_read_b64_tr_b16 v[50:51], v131 offset:4608
	ds_read_b64_tr_b16 v[52:53], v131 offset:6656
	s_waitcnt lgkmcnt(6)
	v_mfma_f32_32x32x16_bf16 v[18:33], v[106:109], v[38:41], v[18:33]
	ds_read_b64_tr_b16 v[54:55], v131 offset:8704
	ds_read_b64_tr_b16 v[56:57], v131 offset:10752
	s_waitcnt lgkmcnt(6)
	v_mfma_f32_32x32x16_bf16 v[18:33], v[110:113], v[42:45], v[18:33]
	ds_read_b64_tr_b16 v[58:59], v131 offset:12800
	ds_read_b64_tr_b16 v[60:61], v131 offset:14848
	s_waitcnt lgkmcnt(6)
	v_mfma_f32_32x32x16_bf16 v[34:49], v[98:101], v[46:49], 0
	ds_read_b64_tr_b16 v[62:63], v131 offset:1024
	ds_read_b64_tr_b16 v[64:65], v131 offset:3072
	s_waitcnt lgkmcnt(6)
	v_mfma_f32_32x32x16_bf16 v[34:49], v[102:105], v[50:53], v[34:49]
	ds_read_b64_tr_b16 v[66:67], v131 offset:5120
	ds_read_b64_tr_b16 v[68:69], v131 offset:7168
	s_waitcnt lgkmcnt(6)
	v_mfma_f32_32x32x16_bf16 v[34:49], v[106:109], v[54:57], v[34:49]
	ds_read_b64_tr_b16 v[70:71], v131 offset:9216
	ds_read_b64_tr_b16 v[72:73], v131 offset:11264
	s_waitcnt lgkmcnt(6)
	v_mfma_f32_32x32x16_bf16 v[34:49], v[110:113], v[58:61], v[34:49]
	ds_read_b64_tr_b16 v[74:75], v131 offset:13312
	ds_read_b64_tr_b16 v[76:77], v131 offset:15360
	s_waitcnt lgkmcnt(6)
	v_mfma_f32_32x32x16_bf16 v[50:65], v[98:101], v[62:65], 0
	ds_read_b64_tr_b16 v[78:79], v131 offset:1536
	ds_read_b64_tr_b16 v[80:81], v131 offset:3584
	s_waitcnt lgkmcnt(6)
	v_mfma_f32_32x32x16_bf16 v[50:65], v[102:105], v[66:69], v[50:65]
	ds_read_b64_tr_b16 v[114:115], v131 offset:5632
	ds_read_b64_tr_b16 v[116:117], v131 offset:7680
	s_waitcnt lgkmcnt(6)
	v_mfma_f32_32x32x16_bf16 v[50:65], v[106:109], v[70:73], v[50:65]
	ds_read_b64_tr_b16 v[118:119], v131 offset:9728
	ds_read_b64_tr_b16 v[120:121], v131 offset:11776
	s_waitcnt lgkmcnt(6)
	v_mfma_f32_32x32x16_bf16 v[50:65], v[110:113], v[74:77], v[50:65]
	ds_read_b64_tr_b16 v[122:123], v131 offset:13824
	ds_read_b64_tr_b16 v[124:125], v131 offset:15872
	s_waitcnt lgkmcnt(6)
	v_mfma_f32_32x32x16_bf16 v[66:81], v[98:101], v[78:81], 0
	v_add_u32_e32 v193, 0xc000, v192
	ds_read_b128 v[126:129], v193 offset:17408
	s_waitcnt lgkmcnt(5)
	v_mfma_f32_32x32x16_bf16 v[66:81], v[102:105], v[114:117], v[66:81]
	ds_read_b128 v[168:171], v193 offset:26112
	s_waitcnt lgkmcnt(4)
	v_mfma_f32_32x32x16_bf16 v[66:81], v[106:109], v[118:121], v[66:81]
	ds_read_b128 v[172:175], v193 offset:17440
	s_waitcnt lgkmcnt(3)
	v_mfma_f32_32x32x16_bf16 v[66:81], v[110:113], v[122:125], v[66:81]
	ds_read_b128 v[176:179], v193 offset:26144
	v_mfma_f32_16x16x32_bf16 v[240:243], v[98:101], v[132:135], 0
	ds_read_b128 v[180:183], v193 offset:17472
	v_mfma_f32_16x16x32_bf16 v[240:243], v[102:105], v[132:135], v[240:243]
	ds_read_b128 v[194:197], v193 offset:26176
	v_mfma_f32_16x16x32_bf16 v[240:243], v[106:109], v[132:135], v[240:243]
	ds_read_b128 v[198:201], v193 offset:17504
	v_mfma_f32_16x16x32_bf16 v[240:243], v[110:113], v[132:135], v[240:243]
	ds_read_b128 v[212:215], v193 offset:26208
	s_waitcnt lgkmcnt(7)
	v_mfma_f32_32x32x16_bf16 v[98:113], v[126:129], v[136:139], v[82:97]
	ds_read_b128 v[216:219], v193 offset:17536
	v_mov_b64_e32 v[128:129], v[96:97]
	v_mov_b64_e32 v[126:127], v[94:95]
	v_mov_b64_e32 v[124:125], v[92:93]
	v_mov_b64_e32 v[122:123], v[90:91]
	v_mov_b64_e32 v[120:121], v[88:89]
	v_mov_b64_e32 v[118:119], v[86:87]
	v_mov_b64_e32 v[116:117], v[84:85]
	v_mov_b64_e32 v[114:115], v[82:83]
	ds_read_b128 v[220:223], v193 offset:26240
	s_waitcnt lgkmcnt(8)
	v_mfma_f32_32x32x16_bf16 v[114:129], v[168:171], v[136:139], v[114:129]
	s_waitcnt lgkmcnt(7)
	v_mfma_f32_32x32x16_bf16 v[98:113], v[172:175], v[140:143], v[98:113]
	ds_read_b128 v[168:171], v193 offset:17568
	s_waitcnt lgkmcnt(7)
	v_mfma_f32_32x32x16_bf16 v[114:129], v[176:179], v[140:143], v[114:129]
	ds_read_b128 v[172:175], v193 offset:26272
	s_waitcnt lgkmcnt(7)
	v_mfma_f32_32x32x16_bf16 v[98:113], v[180:183], v[144:147], v[98:113]
	ds_read_b128 v[176:179], v193 offset:17600
	s_waitcnt lgkmcnt(7)
	v_mfma_f32_32x32x16_bf16 v[114:129], v[194:197], v[144:147], v[114:129]
	ds_read_b128 v[180:183], v193 offset:26304
	s_waitcnt lgkmcnt(7)
	v_mfma_f32_32x32x16_bf16 v[98:113], v[198:201], v[148:151], v[98:113]
	ds_read_b128 v[194:197], v193 offset:17632
	s_waitcnt lgkmcnt(7)
	v_mfma_f32_32x32x16_bf16 v[114:129], v[212:215], v[148:151], v[114:129]
	ds_read_b128 v[198:201], v193 offset:26336
	s_waitcnt lgkmcnt(7)
	v_mfma_f32_32x32x16_bf16 v[98:113], v[216:219], v[152:155], v[98:113]
	s_waitcnt lgkmcnt(6)
	v_mfma_f32_32x32x16_bf16 v[114:129], v[220:223], v[152:155], v[114:129]
	s_waitcnt lgkmcnt(5)
	v_mfma_f32_32x32x16_bf16 v[98:113], v[168:171], v[156:159], v[98:113]
	s_waitcnt lgkmcnt(4)
	v_mfma_f32_32x32x16_bf16 v[114:129], v[172:175], v[156:159], v[114:129]
	s_waitcnt lgkmcnt(3)
	v_mfma_f32_32x32x16_bf16 v[98:113], v[176:179], v[160:163], v[98:113]
	s_waitcnt lgkmcnt(2)
	v_mfma_f32_32x32x16_bf16 v[114:129], v[180:183], v[160:163], v[114:129]
	s_waitcnt lgkmcnt(1)
	v_mfma_f32_32x32x16_bf16 v[98:113], v[194:197], v[164:167], v[98:113]
	s_waitcnt lgkmcnt(0)
	v_mfma_f32_32x32x16_bf16 v[114:129], v[198:201], v[164:167], v[114:129]
	s_setprio 0
	s_mov_b32 s14, s10
	s_mov_b32 s15, s11
	s_mov_b32 s96, 0x1c000
	buffer_load_dwordx4 v[224:227], v191, s[8:11], s59 offen
	buffer_load_dwordx4 v[228:231], v191, s[8:11], s96 offen
	buffer_load_dwordx4 v[232:235], v191, s[12:15], s57 offen
	buffer_load_dwordx4 v[236:239], v191, s[12:15], s58 offen
	s_barrier
	s_mov_b32 s93, 0x8000
	s_movk_i32 s15, 0x4000
	s_movk_i32 s94, 0x4400
	s_mov_b32 s92, 0
	s_mov_b32 s14, 0x8800
	s_mov_b32 s91, 0

; #define ATT_SBAR() __builtin_amdgcn_sched_barrier(0)
; __device__ __forceinline__ unsigned cvtpk(float lo, float hi) { f32x2_t v = {lo, hi}; bf16x2_t b = __builtin_convertvector(v, bf16x2_t); return __builtin_bit_cast(unsigned, b); }
; #define ATT_PK4(P, BASE, OUT) do { u32x4 w = {cvtpk(P[BASE + 0], P[BASE + 1]), cvtpk(P[BASE + 2], P[BASE + 3]), cvtpk(P[BASE + 4], P[BASE + 5]), cvtpk(P[BASE + 6], P[BASE + 7])}; \
;     OUT = *reinterpret_cast<bf16x8*>(&w); } while (0)
; #define ATT_WRITE_K(so) do { *(bf16x8*)(K_lds + (so) + kswz<DQK>(kr, kc * 2)) = sk0; if constexpr (DQK == 128) *(bf16x8*)(K_lds + (so) + kswz<DQK>(32 + kr, kc * 2)) = sk1; } while (0)
; #define ATT_WRITE_V(so) do { *(bf16x8*)(V_lds + (so) + vst0) = sv0; *(bf16x8*)(V_lds + (so) + vst1) = sv1; } while (0)
; #define ATT_BAR() do { ATT_SBAR(); asm volatile("s_barrier" ::: "memory"); ATT_SBAR(); } while (0)
; #define ATT_VPAIR(buf, so, blk, ks) do { if constexpr (!(ABL & 8) && !(ABL & 32)) { buf[2 * (ks)] = vtr(vq0 + (so) + v_rd_off(blk, ks, 0)); buf[2 * (ks) + 1] = vtr(vq0 + (so) + v_rd_off(blk, ks, 1)); } } while (0)
; __device__ __forceinline__ void softmax_exp_pack(f32x16& p0, f32x16& p1, bf16x8& pa0, bf16x8& pa1, bf16x8& pa2, bf16x8& pa3) {
; #pragma unroll
;   for (int r = 0; r < 16; ++r) { p0[r] = __builtin_amdgcn_exp2f(p0[r]); p1[r] = __builtin_amdgcn_exp2f(p1[r]); }
;     ...
;   ATT_PK4(p0, 0, pa0); ATT_PK4(p0, 8, pa1); ATT_PK4(p1, 0, pa2); ATT_PK4(p1, 8, pa3);
;     ...
;   for (int t = 0; t + 1 < NT; ++t) {
;     if constexpr (ABL & 1) { u32x4 w0 = {cvtpk(p0[0], p0[1]), cvtpk(p0[2], p0[3]), cvtpk(p0[4], p0[5]), cvtpk(p0[6], p0[7])}, w1 = {cvtpk(p0[8], p0[9]), cvtpk(p0[10], p0[11]), cvtpk(p0[12], p0[13]), cvtpk(p0[14], p0[15])};
;         u32x4 w2 = {cvtpk(p1[0], p1[1]), cvtpk(p1[2], p1[3]), cvtpk(p1[4], p1[5]), cvtpk(p1[6], p1[7])}, w3 = {cvtpk(p1[8], p1[9]), cvtpk(p1[10], p1[11]), cvtpk(p1[12], p1[13]), cvtpk(p1[14], p1[15])};
;         pa0 = *reinterpret_cast<bf16x8*>(&w0); pa1 = *reinterpret_cast<bf16x8*>(&w1); pa2 = *reinterpret_cast<bf16x8*>(&w2); pa3 = *reinterpret_cast<bf16x8*>(&w3); }
;     else { ATT_SOFTMAX(t == 0); }
;     if constexpr (!(ABL & 4)) { ATT_WRITE_K(k2); ATT_WRITE_V(v1); }
;     ATT_SBAR();
; #pragma unroll
;     for (int ks = 0; ks < 4; ++ks) ATT_VPAIR(va, v0, 0, ks);
;     asm volatile("s_waitcnt lgkmcnt(8)" ::: "memory"); ATT_BAR();
;     ATT_XSECTION(true);
.LBB0_266:
	v_exp_f32_e32 v98, v98
	v_exp_f32_e32 v114, v114
	v_exp_f32_e32 v99, v99
	v_exp_f32_e32 v115, v115
	v_exp_f32_e32 v100, v100
	v_exp_f32_e32 v101, v101
	v_exp_f32_e32 v102, v102
	v_exp_f32_e32 v103, v103
	v_exp_f32_e32 v106, v106
	v_exp_f32_e32 v107, v107
	v_exp_f32_e32 v116, v116
	v_exp_f32_e32 v117, v117
	v_exp_f32_e32 v118, v118
	v_exp_f32_e32 v119, v119
	v_exp_f32_e32 v104, v104
	v_exp_f32_e32 v120, v120
	v_exp_f32_e32 v105, v105
	v_exp_f32_e32 v121, v121
	v_exp_f32_e32 v122, v122
	v_exp_f32_e32 v123, v123
	v_exp_f32_e32 v108, v108
	v_exp_f32_e32 v124, v124
	v_exp_f32_e32 v109, v109
	v_exp_f32_e32 v125, v125
	v_exp_f32_e32 v110, v110
	v_exp_f32_e32 v126, v126
	v_exp_f32_e32 v111, v111
	v_exp_f32_e32 v127, v127
	v_exp_f32_e32 v112, v112
	v_exp_f32_e32 v128, v128
	v_exp_f32_e32 v113, v113
	v_exp_f32_e32 v129, v129
	s_add_i32 s14, s92, 0
	v_cvt_pk_bf16_f32 v98, v98, v99
	v_cvt_pk_bf16_f32 v99, v100, v101
	v_cvt_pk_bf16_f32 v100, v102, v103
	v_cvt_pk_bf16_f32 v102, v106, v107
	v_cvt_pk_bf16_f32 v106, v114, v115
	v_add_u32_e32 v114, s14, v186
	s_add_i32 s14, s93, 0
	s_waitcnt vmcnt(3)
	ds_write_b128 v114, v[224:227] offset:49152
	s_waitcnt vmcnt(2)
	ds_write_b128 v114, v[228:231] offset:57856
	v_add_u32_e32 v114, s14, v189
	v_cvt_pk_bf16_f32 v101, v104, v105
	v_cvt_pk_bf16_f32 v103, v108, v109
	v_cvt_pk_bf16_f32 v104, v110, v111
	v_cvt_pk_bf16_f32 v105, v112, v113
	v_cvt_pk_bf16_f32 v107, v116, v117
	v_cvt_pk_bf16_f32 v108, v118, v119
	v_cvt_pk_bf16_f32 v109, v120, v121
	v_cvt_pk_bf16_f32 v110, v122, v123
	v_cvt_pk_bf16_f32 v111, v124, v125
	v_cvt_pk_bf16_f32 v112, v126, v127
	v_cvt_pk_bf16_f32 v113, v128, v129
	s_waitcnt vmcnt(1)
	ds_write_b128 v114, v[232:235]
	v_add_u32_e32 v114, s14, v190
	s_waitcnt vmcnt(0)
	ds_write_b128 v114, v[236:239]
	v_add_u32_e32 v172, s97, v131
	ds_read_b64_tr_b16 v[114:115], v172
	ds_read_b64_tr_b16 v[116:117], v172 offset:2048
	ds_read_b64_tr_b16 v[118:119], v172 offset:4096
	ds_read_b64_tr_b16 v[120:121], v172 offset:6144
	ds_read_b64_tr_b16 v[122:123], v172 offset:8192
	ds_read_b64_tr_b16 v[124:125], v172 offset:10240
	ds_read_b64_tr_b16 v[126:127], v172 offset:12288
	ds_read_b64_tr_b16 v[128:129], v172 offset:14336
	s_waitcnt lgkmcnt(8)
	s_barrier
	s_setprio 2
	s_waitcnt lgkmcnt(6)
	v_mfma_f32_32x32x16_bf16 v[18:33], v[98:101], v[114:117], v[18:33]
	ds_read_b64_tr_b16 v[168:169], v172 offset:512
	ds_read_b64_tr_b16 v[170:171], v172 offset:2560
	s_waitcnt lgkmcnt(6)
	v_mfma_f32_32x32x16_bf16 v[18:33], v[102:105], v[118:121], v[18:33]
	ds_read_b64_tr_b16 v[114:115], v172 offset:4608
	ds_read_b64_tr_b16 v[116:117], v172 offset:6656
	s_waitcnt lgkmcnt(6)
	v_mfma_f32_32x32x16_bf16 v[18:33], v[106:109], v[122:125], v[18:33]
	ds_read_b64_tr_b16 v[118:119], v172 offset:8704
	ds_read_b64_tr_b16 v[120:121], v172 offset:10752
	s_waitcnt lgkmcnt(6)
	v_mfma_f32_32x32x16_bf16 v[18:33], v[110:113], v[126:129], v[18:33]
	ds_read_b64_tr_b16 v[122:123], v172 offset:12800
	ds_read_b64_tr_b16 v[124:125], v172 offset:14848
	s_waitcnt lgkmcnt(6)
	v_mfma_f32_32x32x16_bf16 v[34:49], v[98:101], v[168:171], v[34:49]
	ds_read_b64_tr_b16 v[126:127], v172 offset:1024
	ds_read_b64_tr_b16 v[128:129], v172 offset:3072
	s_waitcnt lgkmcnt(6)
	v_mfma_f32_32x32x16_bf16 v[34:49], v[102:105], v[114:117], v[34:49]
	ds_read_b64_tr_b16 v[168:169], v172 offset:5120
	ds_read_b64_tr_b16 v[170:171], v172 offset:7168
	s_waitcnt lgkmcnt(6)
	v_mfma_f32_32x32x16_bf16 v[34:49], v[106:109], v[118:121], v[34:49]
	ds_read_b64_tr_b16 v[114:115], v172 offset:9216
	ds_read_b64_tr_b16 v[116:117], v172 offset:11264
	s_waitcnt lgkmcnt(6)
	v_mfma_f32_32x32x16_bf16 v[34:49], v[110:113], v[122:125], v[34:49]
	ds_read_b64_tr_b16 v[118:119], v172 offset:13312
	ds_read_b64_tr_b16 v[120:121], v172 offset:15360
	s_waitcnt lgkmcnt(6)
	v_mfma_f32_32x32x16_bf16 v[50:65], v[98:101], v[126:129], v[50:65]
	ds_read_b64_tr_b16 v[122:123], v172 offset:1536
	ds_read_b64_tr_b16 v[124:125], v172 offset:3584
	s_waitcnt lgkmcnt(6)
	v_mfma_f32_32x32x16_bf16 v[50:65], v[102:105], v[168:171], v[50:65]
	ds_read_b64_tr_b16 v[126:127], v172 offset:5632
	ds_read_b64_tr_b16 v[128:129], v172 offset:7680
	s_waitcnt lgkmcnt(6)
	v_mfma_f32_32x32x16_bf16 v[50:65], v[106:109], v[114:117], v[50:65]
	ds_read_b64_tr_b16 v[168:169], v172 offset:9728
	ds_read_b64_tr_b16 v[170:171], v172 offset:11776
	s_waitcnt lgkmcnt(6)
	v_mfma_f32_32x32x16_bf16 v[50:65], v[110:113], v[118:121], v[50:65]
	ds_read_b64_tr_b16 v[114:115], v172 offset:13824
	ds_read_b64_tr_b16 v[116:117], v172 offset:15872
	s_waitcnt lgkmcnt(6)
	v_mfma_f32_32x32x16_bf16 v[66:81], v[98:101], v[122:125], v[66:81]
	v_add_u32_e32 v193, s36, v192
	ds_read_b128 v[118:121], v193 offset:49152
	s_waitcnt lgkmcnt(5)
	v_mfma_f32_32x32x16_bf16 v[66:81], v[102:105], v[126:129], v[66:81]
	ds_read_b128 v[172:175], v193 offset:57856
	s_waitcnt lgkmcnt(4)
	v_mfma_f32_32x32x16_bf16 v[66:81], v[106:109], v[168:171], v[66:81]
	ds_read_b128 v[176:179], v193 offset:49184
	s_waitcnt lgkmcnt(3)
	v_mfma_f32_32x32x16_bf16 v[66:81], v[110:113], v[114:117], v[66:81]
	ds_read_b128 v[168:171], v193 offset:57888
	v_mfma_f32_16x16x32_bf16 v[240:243], v[98:101], v[132:135], v[240:243]
	ds_read_b128 v[180:183], v193 offset:49216
	v_mfma_f32_16x16x32_bf16 v[240:243], v[102:105], v[132:135], v[240:243]
	ds_read_b128 v[194:197], v193 offset:57920
	v_mfma_f32_16x16x32_bf16 v[240:243], v[106:109], v[132:135], v[240:243]
	ds_read_b128 v[198:201], v193 offset:49248
	v_mfma_f32_16x16x32_bf16 v[240:243], v[110:113], v[132:135], v[240:243]
	ds_read_b128 v[212:215], v193 offset:57952
	s_waitcnt lgkmcnt(7)
	v_mfma_f32_32x32x16_bf16 v[98:113], v[118:121], v[136:139], v[82:97]
	ds_read_b128 v[216:219], v193 offset:49280
	s_waitcnt lgkmcnt(7)
	v_mfma_f32_32x32x16_bf16 v[114:129], v[172:175], v[136:139], v[82:97]
	ds_read_b128 v[220:223], v193 offset:57984
	s_waitcnt lgkmcnt(7)
	v_mfma_f32_32x32x16_bf16 v[98:113], v[176:179], v[140:143], v[98:113]
	ds_read_b128 v[172:175], v193 offset:49312
	s_waitcnt lgkmcnt(7)
	v_mfma_f32_32x32x16_bf16 v[114:129], v[168:171], v[140:143], v[114:129]
	ds_read_b128 v[176:179], v193 offset:58016
	s_waitcnt lgkmcnt(7)
	v_mfma_f32_32x32x16_bf16 v[98:113], v[180:183], v[144:147], v[98:113]
	ds_read_b128 v[168:171], v193 offset:49344
	s_waitcnt lgkmcnt(7)
	v_mfma_f32_32x32x16_bf16 v[114:129], v[194:197], v[144:147], v[114:129]
	ds_read_b128 v[180:183], v193 offset:58048
	s_waitcnt lgkmcnt(7)
	v_mfma_f32_32x32x16_bf16 v[98:113], v[198:201], v[148:151], v[98:113]
	ds_read_b128 v[194:197], v193 offset:49376
	s_waitcnt lgkmcnt(7)
	v_mfma_f32_32x32x16_bf16 v[114:129], v[212:215], v[148:151], v[114:129]
	ds_read_b128 v[198:201], v193 offset:58080
	s_waitcnt lgkmcnt(7)
	v_mfma_f32_32x32x16_bf16 v[98:113], v[216:219], v[152:155], v[98:113]
	s_min_u32 s14, s95, 0x7c
	s_lshl_b32 s14, s14, 15
	s_add_i32 s15, s14, 0x18000
	s_add_i32 s14, s14, 0x1c000
	buffer_load_dwordx4 v[224:227], v191, s[8:11], s15 offen
	s_waitcnt lgkmcnt(6)
	v_mfma_f32_32x32x16_bf16 v[114:129], v[220:223], v[152:155], v[114:129]
	buffer_load_dwordx4 v[228:231], v191, s[8:11], s14 offen
	s_waitcnt lgkmcnt(5)
	v_mfma_f32_32x32x16_bf16 v[98:113], v[172:175], v[156:159], v[98:113]
	s_add_i32 s18, s96, 0xffffc000
	s_mov_b32 s14, s10
	s_mov_b32 s15, s11
	buffer_load_dwordx4 v[232:235], v191, s[12:15], s18 offen
	s_waitcnt lgkmcnt(4)
	v_mfma_f32_32x32x16_bf16 v[114:129], v[176:179], v[156:159], v[114:129]
	buffer_load_dwordx4 v[236:239], v191, s[12:15], s96 offen
	s_waitcnt lgkmcnt(3)
	v_mfma_f32_32x32x16_bf16 v[98:113], v[168:171], v[160:163], v[98:113]
	s_waitcnt lgkmcnt(2)
	v_mfma_f32_32x32x16_bf16 v[114:129], v[180:183], v[160:163], v[114:129]
	s_waitcnt lgkmcnt(1)
	v_mfma_f32_32x32x16_bf16 v[98:113], v[194:197], v[164:167], v[98:113]
	s_waitcnt lgkmcnt(0)
	v_mfma_f32_32x32x16_bf16 v[114:129], v[198:201], v[164:167], v[114:129]
	s_setprio 0
	s_barrier
	s_add_i32 s96, s96, 0x8000
	s_add_i32 s95, s95, 1
	s_cmpk_eq_i32 s95, 0x7e
	s_cbranch_scc1 .LBB0_274
	s_mov_b32 s14, s92
	s_mov_b32 s92, s94
	s_mov_b32 s94, s36
	s_mov_b32 s15, s93
	s_mov_b32 s93, s91
	s_mov_b32 s91, s97
	s_branch .LBB0_265
.LBB0_268:
	v_mov_b32_e32 v194, v193
	s_nop 1
	v_permlane32_swap_b32_e32 v193, v194
	v_max3_f32 v193, v193, v194, 0
	v_exp_f32_e64 v194, -v193
	s_nop 4
	s_nop 0
	v_cmp_gt_f32_e32 vcc, 1.0, v194
	s_cbranch_vccz .LBB0_272
	s_and_saveexec_b64 s[14:15], s[4:5]
	ds_write_b32 v187, v194
	s_or_b64 exec, exec, s[14:15]
	s_waitcnt lgkmcnt(0)
	v_add_u32_e32 v216, s90, v184
	ds_read_b128 v[194:197], v216 offset:96
	ds_read_b128 v[198:201], v216 offset:64
	ds_read_b128 v[212:215], v216 offset:32
	ds_read_b128 v[216:219], v216
	v_and_b32_e32 v244, 63, v0
	v_lshrrev_b32_e32 v245, 4, v244
	v_and_b32_e32 v244, 1, v244
	v_lshlrev_b32_e32 v244, 6, v244
	v_lshl_add_u32 v244, v245, 4, v244
	v_add_u32_e32 v244, s90, v244
	ds_read_b128 v[244:247], v244
	s_waitcnt lgkmcnt(3)
	v_pk_mul_f32 v[30:31], v[30:31], v[194:195]
	s_waitcnt lgkmcnt(2)
	v_pk_mul_f32 v[26:27], v[26:27], v[198:199]
	s_waitcnt lgkmcnt(1)
	v_pk_mul_f32 v[22:23], v[22:23], v[212:213]
	v_pk_mul_f32 v[32:33], v[32:33], v[196:197]
	v_pk_mul_f32 v[28:29], v[28:29], v[200:201]
	v_pk_mul_f32 v[24:25], v[24:25], v[214:215]
	s_waitcnt lgkmcnt(0)
	v_pk_mul_f32 v[20:21], v[20:21], v[218:219]
	v_pk_mul_f32 v[18:19], v[18:19], v[216:217]
	v_pk_mul_f32 v[46:47], v[46:47], v[194:195]
	v_pk_mul_f32 v[42:43], v[42:43], v[198:199]
	v_pk_mul_f32 v[38:39], v[38:39], v[212:213]
	v_pk_mul_f32 v[48:49], v[48:49], v[196:197]
	v_pk_mul_f32 v[44:45], v[44:45], v[200:201]
	v_pk_mul_f32 v[40:41], v[40:41], v[214:215]
	v_pk_mul_f32 v[36:37], v[36:37], v[218:219]
	v_pk_mul_f32 v[34:35], v[34:35], v[216:217]
	v_pk_mul_f32 v[62:63], v[62:63], v[194:195]
	v_pk_mul_f32 v[58:59], v[58:59], v[198:199]
	v_pk_mul_f32 v[54:55], v[54:55], v[212:213]
	v_pk_mul_f32 v[64:65], v[64:65], v[196:197]
	v_pk_mul_f32 v[60:61], v[60:61], v[200:201]
	v_pk_mul_f32 v[56:57], v[56:57], v[214:215]
	v_pk_mul_f32 v[52:53], v[52:53], v[218:219]
	v_pk_mul_f32 v[50:51], v[50:51], v[216:217]
	v_pk_mul_f32 v[78:79], v[78:79], v[194:195]
	v_pk_mul_f32 v[74:75], v[74:75], v[198:199]
	v_pk_mul_f32 v[70:71], v[70:71], v[212:213]
	v_pk_mul_f32 v[80:81], v[80:81], v[196:197]
	v_pk_mul_f32 v[76:77], v[76:77], v[200:201]
	v_pk_mul_f32 v[72:73], v[72:73], v[214:215]
	v_pk_mul_f32 v[68:69], v[68:69], v[218:219]
	v_pk_mul_f32 v[66:67], v[66:67], v[216:217]
	s_waitcnt lgkmcnt(0)
	v_pk_mul_f32 v[240:241], v[240:241], v[244:245]
	v_pk_mul_f32 v[242:243], v[242:243], v[246:247]

; #define ATT_SBAR() __builtin_amdgcn_sched_barrier(0)
; __device__ __forceinline__ unsigned cvtpk(float lo, float hi) { f32x2_t v = {lo, hi}; bf16x2_t b = __builtin_convertvector(v, bf16x2_t); return __builtin_bit_cast(unsigned, b); }
; #define ATT_WRITE_K(so) do { *(bf16x8*)(K_lds + (so) + kswz<DQK>(kr, kc * 2)) = sk0; if constexpr (DQK == 128) *(bf16x8*)(K_lds + (so) + kswz<DQK>(32 + kr, kc * 2)) = sk1; } while (0)
; #define ATT_WRITE_V(so) do { *(bf16x8*)(V_lds + (so) + vst0) = sv0; *(bf16x8*)(V_lds + (so) + vst1) = sv1; } while (0)
; #define ATT_BAR() do { ATT_SBAR(); asm volatile("s_barrier" ::: "memory"); ATT_SBAR(); } while (0)
; #define ATT_SOFTMAX(first_) do { const float pm_ = softmax_rowmax(p0, p1); \
;     if (__builtin_expect((first_) || !__all(pm_ <= THRL), 0)) { const float al_ = softmax_shift(p0, p1, negm, pm_, (first_)); ATT_RESC(al_); } \
;     softmax_exp_pack(p0, p1, pa0, pa1, pa2, pa3); } while (0)
; #define ATT_VPAIR(buf, so, blk, ks) do { if constexpr (!(ABL & 8) && !(ABL & 32)) { buf[2 * (ks)] = vtr(vq0 + (so) + v_rd_off(blk, ks, 0)); buf[2 * (ks) + 1] = vtr(vq0 + (so) + v_rd_off(blk, ks, 1)); } } while (0)
;     ...
;   for (int t = 0; t + 1 < NT; ++t) {
;     if constexpr (ABL & 1) { u32x4 w0 = {cvtpk(p0[0], p0[1]), cvtpk(p0[2], p0[3]), cvtpk(p0[4], p0[5]), cvtpk(p0[6], p0[7])}, w1 = {cvtpk(p0[8], p0[9]), cvtpk(p0[10], p0[11]), cvtpk(p0[12], p0[13]), cvtpk(p0[14], p0[15])};
;         u32x4 w2 = {cvtpk(p1[0], p1[1]), cvtpk(p1[2], p1[3]), cvtpk(p1[4], p1[5]), cvtpk(p1[6], p1[7])}, w3 = {cvtpk(p1[8], p1[9]), cvtpk(p1[10], p1[11]), cvtpk(p1[12], p1[13]), cvtpk(p1[14], p1[15])};
;         pa0 = *reinterpret_cast<bf16x8*>(&w0); pa1 = *reinterpret_cast<bf16x8*>(&w1); pa2 = *reinterpret_cast<bf16x8*>(&w2); pa3 = *reinterpret_cast<bf16x8*>(&w3); }
;     else { ATT_SOFTMAX(t == 0); }
;     if constexpr (!(ABL & 4)) { ATT_WRITE_K(k2); ATT_WRITE_V(v1); }
;     ATT_SBAR();
; #pragma unroll
;     for (int ks = 0; ks < 4; ++ks) ATT_VPAIR(va, v0, 0, ks);
;     asm volatile("s_waitcnt lgkmcnt(8)" ::: "memory"); ATT_BAR();
;     ATT_XSECTION(true);
.LBB0_275:
	v_exp_f32_e32 v98, v98
	v_exp_f32_e32 v114, v114
	v_exp_f32_e32 v99, v99
	v_exp_f32_e32 v115, v115
	v_exp_f32_e32 v100, v100
	v_exp_f32_e32 v101, v101
	v_exp_f32_e32 v102, v102
	v_exp_f32_e32 v103, v103
	v_exp_f32_e32 v106, v106
	v_exp_f32_e32 v107, v107
	v_exp_f32_e32 v116, v116
	v_exp_f32_e32 v117, v117
	v_exp_f32_e32 v118, v118
	v_exp_f32_e32 v119, v119
	v_exp_f32_e32 v104, v104
	v_exp_f32_e32 v120, v120
	v_exp_f32_e32 v105, v105
	v_exp_f32_e32 v121, v121
	v_exp_f32_e32 v122, v122
	v_exp_f32_e32 v123, v123
	v_exp_f32_e32 v108, v108
	v_exp_f32_e32 v124, v124
	v_exp_f32_e32 v109, v109
	v_exp_f32_e32 v125, v125
	v_exp_f32_e32 v110, v110
	v_exp_f32_e32 v126, v126
	v_exp_f32_e32 v111, v111
	v_exp_f32_e32 v127, v127
	v_exp_f32_e32 v112, v112
	v_exp_f32_e32 v128, v128
	v_exp_f32_e32 v113, v113
	v_exp_f32_e32 v129, v129
	s_add_i32 s8, s94, 0
	v_cvt_pk_bf16_f32 v98, v98, v99
	v_cvt_pk_bf16_f32 v99, v100, v101
	v_cvt_pk_bf16_f32 v100, v102, v103
	v_cvt_pk_bf16_f32 v102, v106, v107
	v_cvt_pk_bf16_f32 v106, v114, v115
	v_add_u32_e32 v114, s8, v186
	s_add_i32 s8, s91, 0
	s_waitcnt vmcnt(3)
	ds_write_b128 v114, v[224:227] offset:49152
	s_waitcnt vmcnt(2)
	ds_write_b128 v114, v[228:231] offset:57856
	v_add_u32_e32 v114, s8, v189
	v_cvt_pk_bf16_f32 v101, v104, v105
	v_cvt_pk_bf16_f32 v103, v108, v109
	v_cvt_pk_bf16_f32 v104, v110, v111
	v_cvt_pk_bf16_f32 v105, v112, v113
	v_cvt_pk_bf16_f32 v107, v116, v117
	v_cvt_pk_bf16_f32 v108, v118, v119
	v_cvt_pk_bf16_f32 v109, v120, v121
	v_cvt_pk_bf16_f32 v110, v122, v123
	v_cvt_pk_bf16_f32 v111, v124, v125
	v_cvt_pk_bf16_f32 v112, v126, v127
	v_cvt_pk_bf16_f32 v113, v128, v129
	s_waitcnt vmcnt(1)
	ds_write_b128 v114, v[232:235]
	v_add_u32_e32 v114, s8, v190
	s_waitcnt vmcnt(0)
	ds_write_b128 v114, v[236:239]
	v_add_u32_e32 v172, s93, v131
	ds_read_b64_tr_b16 v[114:115], v172
	ds_read_b64_tr_b16 v[116:117], v172 offset:2048
	ds_read_b64_tr_b16 v[118:119], v172 offset:4096
	ds_read_b64_tr_b16 v[120:121], v172 offset:6144
	ds_read_b64_tr_b16 v[122:123], v172 offset:8192
	ds_read_b64_tr_b16 v[124:125], v172 offset:10240
	ds_read_b64_tr_b16 v[126:127], v172 offset:12288
	ds_read_b64_tr_b16 v[128:129], v172 offset:14336
	s_waitcnt lgkmcnt(8)
	s_barrier
	s_setprio 2
	s_waitcnt lgkmcnt(6)
	v_mfma_f32_32x32x16_bf16 v[18:33], v[98:101], v[114:117], v[18:33]
	ds_read_b64_tr_b16 v[168:169], v172 offset:512
	ds_read_b64_tr_b16 v[170:171], v172 offset:2560
	s_waitcnt lgkmcnt(6)
	v_mfma_f32_32x32x16_bf16 v[18:33], v[102:105], v[118:121], v[18:33]
	ds_read_b64_tr_b16 v[114:115], v172 offset:4608
	ds_read_b64_tr_b16 v[116:117], v172 offset:6656
	s_waitcnt lgkmcnt(6)
	v_mfma_f32_32x32x16_bf16 v[18:33], v[106:109], v[122:125], v[18:33]
	ds_read_b64_tr_b16 v[118:119], v172 offset:8704
	ds_read_b64_tr_b16 v[120:121], v172 offset:10752
	s_waitcnt lgkmcnt(6)
	v_mfma_f32_32x32x16_bf16 v[18:33], v[110:113], v[126:129], v[18:33]
	ds_read_b64_tr_b16 v[122:123], v172 offset:12800
	ds_read_b64_tr_b16 v[124:125], v172 offset:14848
	s_waitcnt lgkmcnt(6)
	v_mfma_f32_32x32x16_bf16 v[34:49], v[98:101], v[168:171], v[34:49]
	ds_read_b64_tr_b16 v[126:127], v172 offset:1024
	ds_read_b64_tr_b16 v[128:129], v172 offset:3072
	s_waitcnt lgkmcnt(6)
	v_mfma_f32_32x32x16_bf16 v[34:49], v[102:105], v[114:117], v[34:49]
	ds_read_b64_tr_b16 v[168:169], v172 offset:5120
	ds_read_b64_tr_b16 v[170:171], v172 offset:7168
	s_waitcnt lgkmcnt(6)
	v_mfma_f32_32x32x16_bf16 v[34:49], v[106:109], v[118:121], v[34:49]
	ds_read_b64_tr_b16 v[114:115], v172 offset:9216
	ds_read_b64_tr_b16 v[116:117], v172 offset:11264
	s_waitcnt lgkmcnt(6)
	v_mfma_f32_32x32x16_bf16 v[34:49], v[110:113], v[122:125], v[34:49]
	ds_read_b64_tr_b16 v[118:119], v172 offset:13312
	ds_read_b64_tr_b16 v[120:121], v172 offset:15360
	s_waitcnt lgkmcnt(6)
	v_mfma_f32_32x32x16_bf16 v[50:65], v[98:101], v[126:129], v[50:65]
	ds_read_b64_tr_b16 v[122:123], v172 offset:1536
	ds_read_b64_tr_b16 v[124:125], v172 offset:3584
	s_waitcnt lgkmcnt(6)
	v_mfma_f32_32x32x16_bf16 v[50:65], v[102:105], v[168:171], v[50:65]
	ds_read_b64_tr_b16 v[126:127], v172 offset:5632
	ds_read_b64_tr_b16 v[128:129], v172 offset:7680
	s_waitcnt lgkmcnt(6)
	v_mfma_f32_32x32x16_bf16 v[50:65], v[106:109], v[114:117], v[50:65]
	ds_read_b64_tr_b16 v[168:169], v172 offset:9728
	ds_read_b64_tr_b16 v[170:171], v172 offset:11776
	s_waitcnt lgkmcnt(6)
	v_mfma_f32_32x32x16_bf16 v[50:65], v[110:113], v[118:121], v[50:65]
	ds_read_b64_tr_b16 v[114:115], v172 offset:13824
	ds_read_b64_tr_b16 v[116:117], v172 offset:15872
	s_waitcnt lgkmcnt(6)
	v_mfma_f32_32x32x16_bf16 v[66:81], v[98:101], v[122:125], v[66:81]
	v_add3_u32 v186, v188, s92, v184
	ds_read_b128 v[118:121], v186 offset:49152
	s_waitcnt lgkmcnt(5)
	v_mfma_f32_32x32x16_bf16 v[66:81], v[102:105], v[126:129], v[66:81]
	ds_read_b128 v[122:125], v186 offset:57856
	s_waitcnt lgkmcnt(4)
	v_mfma_f32_32x32x16_bf16 v[66:81], v[106:109], v[168:171], v[66:81]
	ds_read_b128 v[126:129], v186 offset:49184
	s_waitcnt lgkmcnt(3)
	v_mfma_f32_32x32x16_bf16 v[66:81], v[110:113], v[114:117], v[66:81]
	ds_read_b128 v[168:171], v186 offset:57888
	v_mfma_f32_16x16x32_bf16 v[240:243], v[98:101], v[132:135], v[240:243]
	ds_read_b128 v[114:117], v186 offset:49216
	v_mfma_f32_16x16x32_bf16 v[240:243], v[102:105], v[132:135], v[240:243]
	ds_read_b128 v[172:175], v186 offset:57920
	v_mfma_f32_16x16x32_bf16 v[240:243], v[106:109], v[132:135], v[240:243]
	ds_read_b128 v[176:179], v186 offset:49248
	v_mfma_f32_16x16x32_bf16 v[240:243], v[110:113], v[132:135], v[240:243]
	ds_read_b128 v[180:183], v186 offset:57952
	s_waitcnt lgkmcnt(7)
; #define ATT_BAR() do { ATT_SBAR(); asm volatile("s_barrier" ::: "memory"); ATT_SBAR(); } while (0)
; #define ATT_SOFTMAX(first_) do { const float pm_ = softmax_rowmax(p0, p1); \
;     if (__builtin_expect((first_) || !__all(pm_ <= THRL), 0)) { const float al_ = softmax_shift(p0, p1, negm, pm_, (first_)); ATT_RESC(al_); } \
;     softmax_exp_pack(p0, p1, pa0, pa1, pa2, pa3); } while (0)
; #define ATT_VPAIR(buf, so, blk, ks) do { if constexpr (!(ABL & 8) && !(ABL & 32)) { buf[2 * (ks)] = vtr(vq0 + (so) + v_rd_off(blk, ks, 0)); buf[2 * (ks) + 1] = vtr(vq0 + (so) + v_rd_off(blk, ks, 1)); } } while (0)
;     ...
;   ATT_SOFTMAX(false);
; #pragma unroll
;   for (int ks = 0; ks < 4; ++ks) ATT_VPAIR(va, v0, 0, ks);
;   asm volatile("s_waitcnt lgkmcnt(0)" ::: "memory"); ATT_BAR();
;   ATT_XSECTION(false);
	v_mfma_f32_32x32x16_bf16 v[98:113], v[118:121], v[136:139], v[82:97]
	ds_read_b128 v[188:191], v186 offset:49280
	s_waitcnt lgkmcnt(7)
	v_mfma_f32_32x32x16_bf16 v[82:97], v[122:125], v[136:139], v[82:97]
	ds_read_b128 v[118:121], v186 offset:57984
	s_waitcnt lgkmcnt(7)
	v_mfma_f32_32x32x16_bf16 v[98:113], v[126:129], v[140:143], v[98:113]
	ds_read_b128 v[122:125], v186 offset:49312
	s_waitcnt lgkmcnt(7)
	v_mfma_f32_32x32x16_bf16 v[82:97], v[168:171], v[140:143], v[82:97]
	ds_read_b128 v[126:129], v186 offset:58016
	s_waitcnt lgkmcnt(7)
	v_mfma_f32_32x32x16_bf16 v[98:113], v[114:117], v[144:147], v[98:113]
	ds_read_b128 v[136:139], v186 offset:49344
	s_waitcnt lgkmcnt(7)
	v_mfma_f32_32x32x16_bf16 v[82:97], v[172:175], v[144:147], v[82:97]
	ds_read_b128 v[114:117], v186 offset:58048
	s_waitcnt lgkmcnt(7)
	v_mfma_f32_32x32x16_bf16 v[98:113], v[176:179], v[148:151], v[98:113]
	ds_read_b128 v[140:143], v186 offset:49376
	s_waitcnt lgkmcnt(7)
	v_mfma_f32_32x32x16_bf16 v[82:97], v[180:183], v[148:151], v[82:97]
	ds_read_b128 v[144:147], v186 offset:58080
	s_waitcnt lgkmcnt(7)
	v_mfma_f32_32x32x16_bf16 v[98:113], v[188:191], v[152:155], v[98:113]
	s_waitcnt lgkmcnt(6)
	v_mfma_f32_32x32x16_bf16 v[82:97], v[118:121], v[152:155], v[82:97]
	s_waitcnt lgkmcnt(5)
	v_mfma_f32_32x32x16_bf16 v[98:113], v[122:125], v[156:159], v[98:113]
	s_waitcnt lgkmcnt(4)
	v_mfma_f32_32x32x16_bf16 v[82:97], v[126:129], v[156:159], v[82:97]
	s_waitcnt lgkmcnt(3)
	v_mfma_f32_32x32x16_bf16 v[98:113], v[136:139], v[160:163], v[98:113]
	s_waitcnt lgkmcnt(2)
	v_mfma_f32_32x32x16_bf16 v[82:97], v[114:117], v[160:163], v[82:97]
	s_waitcnt lgkmcnt(1)
	v_mfma_f32_32x32x16_bf16 v[98:113], v[140:143], v[164:167], v[98:113]
	s_waitcnt lgkmcnt(0)
	v_mfma_f32_32x32x16_bf16 v[82:97], v[144:147], v[164:167], v[82:97]
	s_setprio 0
	s_barrier
	s_nop 10
	v_add_f32_e32 v114, 0, v82
	v_max3_f32 v115, v114, v98, v99
	v_max3_f32 v115, v115, v100, v101
	v_max3_f32 v115, v115, v102, v103
	v_max3_f32 v115, v115, v104, v105
	v_max3_f32 v115, v115, v106, v107
	v_max3_f32 v115, v115, v108, v109
	v_max3_f32 v115, v115, v110, v111
	v_max3_f32 v115, v115, v112, v113
	s_nop 0
	v_max3_f32 v114, v115, v83, v84
	v_max3_f32 v114, v114, v85, v86
	v_max3_f32 v114, v114, v87, v88
	v_max3_f32 v114, v114, v89, v90
	v_max3_f32 v114, v114, v91, v92
	v_max3_f32 v114, v114, v93, v94
	v_max3_f32 v114, v114, v95, v96
	v_max_f32 v114, v114, v97
	s_nop 0
	v_cmp_ge_f32_e32 vcc, s60, v114
	s_cmp_lg_u64 vcc, exec
	s_cbranch_scc1 .LBB0_314
.LBB0_276:
	v_exp_f32_e32 v98, v98
	v_exp_f32_e32 v114, v82
	v_exp_f32_e32 v82, v99
	v_exp_f32_e32 v99, v83
	v_exp_f32_e32 v83, v100
	v_exp_f32_e32 v100, v84
	v_exp_f32_e32 v84, v101
	v_exp_f32_e32 v101, v85
	v_exp_f32_e32 v85, v102
	v_exp_f32_e32 v102, v86
	v_exp_f32_e32 v86, v103
	v_exp_f32_e32 v103, v87
	v_exp_f32_e32 v87, v104
	v_exp_f32_e32 v104, v88
	v_exp_f32_e32 v88, v105
	v_exp_f32_e32 v105, v89
	v_exp_f32_e32 v89, v106
	v_exp_f32_e32 v106, v90
	v_exp_f32_e32 v90, v107
	v_exp_f32_e32 v107, v91
	v_exp_f32_e32 v91, v108
	v_exp_f32_e32 v108, v92
	v_exp_f32_e32 v92, v109
	v_exp_f32_e32 v109, v93
	v_exp_f32_e32 v93, v110
	v_exp_f32_e32 v110, v94
	v_exp_f32_e32 v94, v111
	v_exp_f32_e32 v111, v95
	v_exp_f32_e32 v95, v112
	v_exp_f32_e32 v112, v96
	v_exp_f32_e32 v96, v113
	v_exp_f32_e32 v97, v97
	v_add_u32_e32 v118, s91, v131
	v_cvt_pk_bf16_f32 v82, v98, v82
	v_cvt_pk_bf16_f32 v83, v83, v84
	v_cvt_pk_bf16_f32 v84, v85, v86
	v_cvt_pk_bf16_f32 v85, v87, v88
	v_cvt_pk_bf16_f32 v86, v89, v90
	v_cvt_pk_bf16_f32 v87, v91, v92
	v_cvt_pk_bf16_f32 v88, v93, v94
	v_cvt_pk_bf16_f32 v89, v95, v96
	v_cvt_pk_bf16_f32 v90, v114, v99
	v_cvt_pk_bf16_f32 v91, v100, v101
	v_cvt_pk_bf16_f32 v92, v102, v103
	v_cvt_pk_bf16_f32 v93, v104, v105
	v_cvt_pk_bf16_f32 v94, v106, v107
	v_cvt_pk_bf16_f32 v95, v108, v109
	v_cvt_pk_bf16_f32 v96, v110, v111
	v_cvt_pk_bf16_f32 v97, v112, v97
	ds_read_b64_tr_b16 v[98:99], v118
	ds_read_b64_tr_b16 v[100:101], v118 offset:2048
	ds_read_b64_tr_b16 v[102:103], v118 offset:4096
	ds_read_b64_tr_b16 v[104:105], v118 offset:6144
	ds_read_b64_tr_b16 v[106:107], v118 offset:8192
	ds_read_b64_tr_b16 v[108:109], v118 offset:10240
	ds_read_b64_tr_b16 v[110:111], v118 offset:12288
	ds_read_b64_tr_b16 v[112:113], v118 offset:14336
	s_waitcnt lgkmcnt(0)
	s_barrier
; __device__ __forceinline__ int crow(int r, int hi) { return (r & 3) + 8 * (r >> 2) + 4 * hi; }
; #define ATT_BAR() do { ATT_SBAR(); asm volatile("s_barrier" ::: "memory"); ATT_SBAR(); } while (0)
; __device__ __forceinline__ unsigned f2bf(float f) { unsigned u = __builtin_bit_cast(unsigned, f); return (u + 0x7fffu + ((u >> 16) & 1u)) >> 16; }
;     ...
;   ATT_XSECTION(false);
;   ATT_BAR();
;   if (grp == 0) ATT_BAR();
; #pragma unroll
;   for (int r = 0; r < 16; ++r) rli[r] = __builtin_amdgcn_rcpf(lacc[r]);
;     ...
;     att::bf16* Ow = Obase + ((size_t)b * SEQ + (size_t)qb * 256 + wave_ * 32) * 2048 + h * 128;
; #pragma unroll
;     for (int r = 0; r < 16; ++r) { const int orow = crow(r, hi);
; #pragma unroll
;         for (int d0 = 0; d0 < 4; ++d0) Ow[(size_t)orow * 2048 + d0 * 32 + r32] = (att::bf16)f2bf(o[d0][r] * rli[r]); }
	s_setprio 2
	s_waitcnt lgkmcnt(6)
	v_mfma_f32_32x32x16_bf16 v[18:33], v[82:85], v[98:101], v[18:33]
	ds_read_b64_tr_b16 v[114:115], v118 offset:512
	ds_read_b64_tr_b16 v[116:117], v118 offset:2560
	s_waitcnt lgkmcnt(6)
	v_mfma_f32_32x32x16_bf16 v[18:33], v[86:89], v[102:105], v[18:33]
	ds_read_b64_tr_b16 v[98:99], v118 offset:4608
	ds_read_b64_tr_b16 v[100:101], v118 offset:6656
	s_waitcnt lgkmcnt(6)
	v_mfma_f32_32x32x16_bf16 v[18:33], v[90:93], v[106:109], v[18:33]
	ds_read_b64_tr_b16 v[102:103], v118 offset:8704
	ds_read_b64_tr_b16 v[104:105], v118 offset:10752
	s_waitcnt lgkmcnt(6)
	v_mfma_f32_32x32x16_bf16 v[18:33], v[94:97], v[110:113], v[18:33]
	ds_read_b64_tr_b16 v[106:107], v118 offset:12800
	ds_read_b64_tr_b16 v[108:109], v118 offset:14848
	s_waitcnt lgkmcnt(6)
	v_mfma_f32_32x32x16_bf16 v[34:49], v[82:85], v[114:117], v[34:49]
	ds_read_b64_tr_b16 v[110:111], v118 offset:1024
	ds_read_b64_tr_b16 v[112:113], v118 offset:3072
	s_waitcnt lgkmcnt(6)
	v_mfma_f32_32x32x16_bf16 v[34:49], v[86:89], v[98:101], v[34:49]
	ds_read_b64_tr_b16 v[114:115], v118 offset:5120
	ds_read_b64_tr_b16 v[116:117], v118 offset:7168
	s_waitcnt lgkmcnt(6)
	v_mfma_f32_32x32x16_bf16 v[34:49], v[90:93], v[102:105], v[34:49]
	ds_read_b64_tr_b16 v[98:99], v118 offset:9216
	ds_read_b64_tr_b16 v[100:101], v118 offset:11264
	s_waitcnt lgkmcnt(6)
	v_mfma_f32_32x32x16_bf16 v[34:49], v[94:97], v[106:109], v[34:49]
	ds_read_b64_tr_b16 v[102:103], v118 offset:13312
	ds_read_b64_tr_b16 v[104:105], v118 offset:15360
	s_waitcnt lgkmcnt(6)
	v_mfma_f32_32x32x16_bf16 v[50:65], v[82:85], v[110:113], v[50:65]
	ds_read_b64_tr_b16 v[106:107], v118 offset:1536
	ds_read_b64_tr_b16 v[108:109], v118 offset:3584
	s_waitcnt lgkmcnt(6)
	v_mfma_f32_32x32x16_bf16 v[50:65], v[86:89], v[114:117], v[50:65]
	ds_read_b64_tr_b16 v[110:111], v118 offset:5632
	ds_read_b64_tr_b16 v[112:113], v118 offset:7680
	s_waitcnt lgkmcnt(6)
	v_mfma_f32_32x32x16_bf16 v[50:65], v[90:93], v[98:101], v[50:65]
	ds_read_b64_tr_b16 v[114:115], v118 offset:9728
	ds_read_b64_tr_b16 v[116:117], v118 offset:11776
	s_waitcnt lgkmcnt(6)
	v_mfma_f32_32x32x16_bf16 v[50:65], v[94:97], v[102:105], v[50:65]
	ds_read_b64_tr_b16 v[98:99], v118 offset:13824
	ds_read_b64_tr_b16 v[100:101], v118 offset:15872
	s_waitcnt lgkmcnt(6)
	v_mfma_f32_32x32x16_bf16 v[66:81], v[82:85], v[106:109], v[66:81]
	s_waitcnt lgkmcnt(4)
	v_mfma_f32_32x32x16_bf16 v[66:81], v[86:89], v[110:113], v[66:81]
	s_waitcnt lgkmcnt(2)
	v_mfma_f32_32x32x16_bf16 v[66:81], v[90:93], v[114:117], v[66:81]
	s_waitcnt lgkmcnt(0)
	v_mfma_f32_32x32x16_bf16 v[66:81], v[94:97], v[98:101], v[66:81]
	v_mfma_f32_16x16x32_bf16 v[240:243], v[82:85], v[132:135], v[240:243]
	v_mfma_f32_16x16x32_bf16 v[240:243], v[86:89], v[132:135], v[240:243]
	v_mfma_f32_16x16x32_bf16 v[240:243], v[90:93], v[132:135], v[240:243]
	v_mfma_f32_16x16x32_bf16 v[240:243], v[94:97], v[132:135], v[240:243]
	s_setprio 0
	s_barrier
	s_cmpk_gt_u32 s88, 0xff
	s_cbranch_scc1 .LBB0_278
	s_barrier
.LBB0_278:
	s_nop 7
	s_nop 1
	v_and_b32_e32 v244, 63, v0
	v_lshrrev_b32_e32 v245, 4, v244
	v_and_b32_e32 v244, 1, v244
	v_lshlrev_b32_e32 v244, 6, v244
	v_lshl_add_u32 v244, v245, 4, v244
	v_add_u32_e32 v244, s90, v244
	ds_write_b128 v244, v[240:243]
	v_add_u32_e32 v245, s90, v184
	s_waitcnt lgkmcnt(0)
	ds_read_b128 v[2:5], v245
	ds_read_b128 v[6:9], v245 offset:32
	ds_read_b128 v[10:13], v245 offset:64
	ds_read_b128 v[14:17], v245 offset:96
	s_waitcnt lgkmcnt(0)
	s_ashr_i32 s4, s89, 1
	s_andn2_b32 s4, s4, 31
	s_ashr_i32 s5, s4, 31
	s_add_u32 s4, s4, s51
	s_addc_u32 s5, s5, 0
	s_lshl_b64 s[4:5], s[4:5], 12
	s_nop 2
	v_rcp_f32_e32 v83, v2
	s_add_u32 s4, s44, s4
	s_addc_u32 s5, s45, s5
	v_and_b32_e32 v82, 31, v211
	s_add_u32 s4, s4, s46
	v_rcp_f32_e32 v85, v4
	s_addc_u32 s5, s5, s47
	v_lshlrev_b32_e32 v184, 1, v82
	v_lshlrev_b32_e32 v4, 9, v211
	v_rcp_f32_e32 v84, v3
	v_rcp_f32_e32 v87, v6
	v_lshl_add_u64 v[2:3], s[4:5], 0, v[184:185]
	v_and_b32_e32 v184, 0x4000, v4
	v_mul_f32_e32 v6, v18, v83
	v_rcp_f32_e32 v88, v7
	v_lshl_add_u64 v[2:3], v[2:3], 0, v[184:185]
	v_bfe_u32 v7, v6, 16, 1
	v_add3_u32 v18, v6, v7, s61
	v_add_co_u32_e32 v6, vcc, s63, v2
	v_rcp_f32_e32 v86, v5
	s_nop 0
	v_addc_co_u32_e32 v7, vcc, 0, v3, vcc
	global_store_short_d16_hi v[6:7], v18, off offset:-4096
	v_mul_f32_e32 v18, v34, v83
	v_bfe_u32 v34, v18, 16, 1
	v_lshl_add_u64 v[4:5], v[2:3], 0, s[38:39]
	v_add3_u32 v18, v18, v34, s61
	global_store_short_d16_hi v[4:5], v18, off offset:64
	v_mul_f32_e32 v18, v50, v83
	v_bfe_u32 v34, v18, 16, 1
	v_add3_u32 v18, v18, v34, s61
	global_store_short_d16_hi v[4:5], v18, off offset:128
	v_mul_f32_e32 v18, v66, v83
	v_bfe_u32 v34, v18, 16, 1
	v_add3_u32 v18, v18, v34, s61
	global_store_short_d16_hi v[4:5], v18, off offset:192
	v_mul_f32_e32 v4, v19, v84
	v_bfe_u32 v5, v4, 16, 1
	v_add3_u32 v4, v4, v5, s61
	global_store_short_d16_hi v[6:7], v4, off
	v_mul_f32_e32 v4, v35, v84
	v_bfe_u32 v5, v4, 16, 1
	v_add3_u32 v4, v4, v5, s61
	global_store_short_d16_hi v[6:7], v4, off offset:64
	v_mul_f32_e32 v4, v51, v84
	v_bfe_u32 v5, v4, 16, 1
	v_add3_u32 v4, v4, v5, s61
	global_store_short_d16_hi v[6:7], v4, off offset:128
	v_mul_f32_e32 v4, v67, v84
	v_bfe_u32 v5, v4, 16, 1
	v_add3_u32 v4, v4, v5, s61
	global_store_short_d16_hi v[6:7], v4, off offset:192
	v_mul_f32_e32 v4, v20, v85
	v_bfe_u32 v5, v4, 16, 1
	v_add3_u32 v18, v4, v5, s61
	v_add_co_u32_e32 v4, vcc, s64, v2
	v_rcp_f32_e32 v8, v8
	s_nop 0
	v_addc_co_u32_e32 v5, vcc, 0, v3, vcc
	v_add_co_u32_e32 v6, vcc, s65, v2
	v_rcp_f32_e32 v9, v9
	s_nop 0
	v_addc_co_u32_e32 v7, vcc, 0, v3, vcc
	global_store_short_d16_hi v[6:7], v18, off offset:-4096
	v_mul_f32_e32 v18, v36, v85
; __device__ __forceinline__ int crow(int r, int hi) { return (r & 3) + 8 * (r >> 2) + 4 * hi; }
; __device__ __forceinline__ unsigned f2bf(float f) { unsigned u = __builtin_bit_cast(unsigned, f); return (u + 0x7fffu + ((u >> 16) & 1u)) >> 16; }
;     ...
;     att::bf16* Ow = Obase + ((size_t)b * SEQ + (size_t)qb * 256 + wave_ * 32) * 2048 + h * 128;
; #pragma unroll
;     for (int r = 0; r < 16; ++r) { const int orow = crow(r, hi);
; #pragma unroll
;         for (int d0 = 0; d0 < 4; ++d0) Ow[(size_t)orow * 2048 + d0 * 32 + r32] = (att::bf16)f2bf(o[d0][r] * rli[r]); }
	v_bfe_u32 v19, v18, 16, 1
	v_add3_u32 v18, v18, v19, s61
	global_store_short_d16_hi v[4:5], v18, off offset:64
	v_mul_f32_e32 v18, v52, v85
	v_bfe_u32 v19, v18, 16, 1
	v_add3_u32 v18, v18, v19, s61
	global_store_short_d16_hi v[4:5], v18, off offset:128
	v_mul_f32_e32 v18, v68, v85
	v_bfe_u32 v19, v18, 16, 1
	v_add3_u32 v18, v18, v19, s61
	global_store_short_d16_hi v[4:5], v18, off offset:192
	v_mul_f32_e32 v4, v21, v86
	v_bfe_u32 v5, v4, 16, 1
	v_add3_u32 v4, v4, v5, s61
	global_store_short_d16_hi v[6:7], v4, off
	v_mul_f32_e32 v4, v37, v86
	v_bfe_u32 v5, v4, 16, 1
	v_add3_u32 v4, v4, v5, s61
	global_store_short_d16_hi v[6:7], v4, off offset:64
	v_mul_f32_e32 v4, v53, v86
	v_bfe_u32 v5, v4, 16, 1
	v_add3_u32 v4, v4, v5, s61
	global_store_short_d16_hi v[6:7], v4, off offset:128
	v_mul_f32_e32 v4, v69, v86
	v_bfe_u32 v5, v4, 16, 1
	v_add3_u32 v4, v4, v5, s61
	global_store_short_d16_hi v[6:7], v4, off offset:192
	v_mul_f32_e32 v4, v22, v87
	v_bfe_u32 v5, v4, 16, 1
	v_add3_u32 v18, v4, v5, s61
	v_add_co_u32_e32 v4, vcc, s66, v2
	v_rcp_f32_e32 v10, v10
	s_nop 0
	v_addc_co_u32_e32 v5, vcc, 0, v3, vcc
	v_add_co_u32_e32 v6, vcc, s67, v2
	v_rcp_f32_e32 v11, v11
	s_nop 0
	v_addc_co_u32_e32 v7, vcc, 0, v3, vcc
	global_store_short_d16_hi v[6:7], v18, off offset:-4096
	v_mul_f32_e32 v18, v38, v87
	v_bfe_u32 v19, v18, 16, 1
	v_add3_u32 v18, v18, v19, s61
	global_store_short_d16_hi v[4:5], v18, off offset:64
	v_mul_f32_e32 v18, v54, v87
	v_bfe_u32 v19, v18, 16, 1
	v_add3_u32 v18, v18, v19, s61
	global_store_short_d16_hi v[4:5], v18, off offset:128
	v_mul_f32_e32 v18, v70, v87
	v_bfe_u32 v19, v18, 16, 1
	v_add3_u32 v18, v18, v19, s61
	global_store_short_d16_hi v[4:5], v18, off offset:192
	v_mul_f32_e32 v4, v23, v88
	v_bfe_u32 v5, v4, 16, 1
	v_add3_u32 v4, v4, v5, s61
	global_store_short_d16_hi v[6:7], v4, off
	v_mul_f32_e32 v4, v39, v88
	v_bfe_u32 v5, v4, 16, 1
	v_add3_u32 v4, v4, v5, s61
	global_store_short_d16_hi v[6:7], v4, off offset:64
	v_mul_f32_e32 v4, v55, v88
	v_bfe_u32 v5, v4, 16, 1
	v_add3_u32 v4, v4, v5, s61
	global_store_short_d16_hi v[6:7], v4, off offset:128
	v_mul_f32_e32 v4, v71, v88
	v_bfe_u32 v5, v4, 16, 1
	v_add3_u32 v4, v4, v5, s61
	global_store_short_d16_hi v[6:7], v4, off offset:192
	v_mul_f32_e32 v4, v24, v8
	v_bfe_u32 v5, v4, 16, 1
	v_add3_u32 v18, v4, v5, s61
	v_add_co_u32_e32 v4, vcc, s68, v2
	v_rcp_f32_e32 v12, v12
	s_nop 0
	v_addc_co_u32_e32 v5, vcc, 0, v3, vcc
	v_add_co_u32_e32 v6, vcc, s69, v2
	v_rcp_f32_e32 v13, v13
	s_nop 0
	v_addc_co_u32_e32 v7, vcc, 0, v3, vcc
	global_store_short_d16_hi v[6:7], v18, off offset:-4096
	v_mul_f32_e32 v18, v40, v8
	v_bfe_u32 v19, v18, 16, 1
	v_add3_u32 v18, v18, v19, s61
	global_store_short_d16_hi v[4:5], v18, off offset:64
	v_mul_f32_e32 v18, v56, v8
	v_bfe_u32 v19, v18, 16, 1
	v_add3_u32 v18, v18, v19, s61
	v_mul_f32_e32 v8, v72, v8
	global_store_short_d16_hi v[4:5], v18, off offset:128
	v_bfe_u32 v18, v8, 16, 1
	v_add3_u32 v8, v8, v18, s61
	global_store_short_d16_hi v[4:5], v8, off offset:192
	v_mul_f32_e32 v4, v25, v9
	v_bfe_u32 v5, v4, 16, 1
	v_add3_u32 v4, v4, v5, s61
	global_store_short_d16_hi v[6:7], v4, off
	v_mul_f32_e32 v4, v41, v9
	v_bfe_u32 v5, v4, 16, 1
	v_add3_u32 v4, v4, v5, s61
	global_store_short_d16_hi v[6:7], v4, off offset:64
	v_mul_f32_e32 v4, v57, v9
	v_bfe_u32 v5, v4, 16, 1
	v_add3_u32 v4, v4, v5, s61
	global_store_short_d16_hi v[6:7], v4, off offset:128
	v_mul_f32_e32 v4, v73, v9
	v_bfe_u32 v5, v4, 16, 1
	v_add3_u32 v4, v4, v5, s61
	global_store_short_d16_hi v[6:7], v4, off offset:192
	v_mul_f32_e32 v4, v26, v10
	v_bfe_u32 v5, v4, 16, 1
	v_add3_u32 v8, v4, v5, s61
	v_add_co_u32_e32 v4, vcc, s74, v2
	v_rcp_f32_e32 v14, v14
	s_nop 0
	v_addc_co_u32_e32 v5, vcc, 0, v3, vcc
	v_add_co_u32_e32 v6, vcc, s75, v2
	v_rcp_f32_e32 v15, v15
	s_nop 0
	v_addc_co_u32_e32 v7, vcc, 0, v3, vcc
	global_store_short_d16_hi v[6:7], v8, off offset:-4096
	v_mul_f32_e32 v8, v42, v10
	v_bfe_u32 v9, v8, 16, 1
	v_add3_u32 v8, v8, v9, s61
	global_store_short_d16_hi v[4:5], v8, off offset:64
	v_mul_f32_e32 v8, v58, v10
	v_bfe_u32 v9, v8, 16, 1
	v_add3_u32 v8, v8, v9, s61
	global_store_short_d16_hi v[4:5], v8, off offset:128
	v_mul_f32_e32 v8, v74, v10
	v_bfe_u32 v9, v8, 16, 1
	v_add3_u32 v8, v8, v9, s61
	global_store_short_d16_hi v[4:5], v8, off offset:192
	v_mul_f32_e32 v4, v27, v11
; __device__ __forceinline__ int crow(int r, int hi) { return (r & 3) + 8 * (r >> 2) + 4 * hi; }
; __device__ __forceinline__ unsigned f2bf(float f) { unsigned u = __builtin_bit_cast(unsigned, f); return (u + 0x7fffu + ((u >> 16) & 1u)) >> 16; }
;     ...
;     att::bf16* Ow = Obase + ((size_t)b * SEQ + (size_t)qb * 256 + wave_ * 32) * 2048 + h * 128;
; #pragma unroll
;     for (int r = 0; r < 16; ++r) { const int orow = crow(r, hi);
; #pragma unroll
;         for (int d0 = 0; d0 < 4; ++d0) Ow[(size_t)orow * 2048 + d0 * 32 + r32] = (att::bf16)f2bf(o[d0][r] * rli[r]); }
	v_bfe_u32 v5, v4, 16, 1
	v_add3_u32 v4, v4, v5, s61
	global_store_short_d16_hi v[6:7], v4, off
	v_mul_f32_e32 v4, v43, v11
	v_bfe_u32 v5, v4, 16, 1
	v_add3_u32 v4, v4, v5, s61
	global_store_short_d16_hi v[6:7], v4, off offset:64
	v_mul_f32_e32 v4, v59, v11
	v_bfe_u32 v5, v4, 16, 1
	v_add3_u32 v4, v4, v5, s61
	global_store_short_d16_hi v[6:7], v4, off offset:128
	v_mul_f32_e32 v4, v75, v11
	v_bfe_u32 v5, v4, 16, 1
	v_add3_u32 v4, v4, v5, s61
	global_store_short_d16_hi v[6:7], v4, off offset:192
	v_mul_f32_e32 v4, v28, v12
	v_bfe_u32 v5, v4, 16, 1
	v_add3_u32 v8, v4, v5, s61
	v_add_co_u32_e32 v4, vcc, s76, v2
	v_rcp_f32_e32 v16, v16
	s_nop 0
	v_addc_co_u32_e32 v5, vcc, 0, v3, vcc
	v_add_co_u32_e32 v6, vcc, s77, v2
	v_rcp_f32_e32 v17, v17
	s_nop 0
	v_addc_co_u32_e32 v7, vcc, 0, v3, vcc
	global_store_short_d16_hi v[6:7], v8, off offset:-4096
	v_mul_f32_e32 v8, v44, v12
	v_bfe_u32 v9, v8, 16, 1
	v_add3_u32 v8, v8, v9, s61
	global_store_short_d16_hi v[4:5], v8, off offset:64
	v_mul_f32_e32 v8, v60, v12
	v_bfe_u32 v9, v8, 16, 1
	v_add3_u32 v8, v8, v9, s61
	global_store_short_d16_hi v[4:5], v8, off offset:128
	v_mul_f32_e32 v8, v76, v12
	v_bfe_u32 v9, v8, 16, 1
	v_add3_u32 v8, v8, v9, s61
	global_store_short_d16_hi v[4:5], v8, off offset:192
	v_mul_f32_e32 v4, v29, v13
	v_bfe_u32 v5, v4, 16, 1
	v_add3_u32 v4, v4, v5, s61
	global_store_short_d16_hi v[6:7], v4, off
	v_mul_f32_e32 v4, v45, v13
	v_bfe_u32 v5, v4, 16, 1
	v_add3_u32 v4, v4, v5, s61
	global_store_short_d16_hi v[6:7], v4, off offset:64
	v_mul_f32_e32 v4, v61, v13
	v_bfe_u32 v5, v4, 16, 1
	v_add3_u32 v4, v4, v5, s61
	global_store_short_d16_hi v[6:7], v4, off offset:128
	v_mul_f32_e32 v4, v77, v13
	v_bfe_u32 v5, v4, 16, 1
	v_add3_u32 v4, v4, v5, s61
	global_store_short_d16_hi v[6:7], v4, off offset:192
	v_mul_f32_e32 v4, v30, v14
	v_bfe_u32 v5, v4, 16, 1
	v_add3_u32 v8, v4, v5, s61
	v_add_co_u32_e32 v4, vcc, s78, v2
	s_nop 1
	v_addc_co_u32_e32 v5, vcc, 0, v3, vcc
	v_add_co_u32_e32 v6, vcc, s79, v2
	s_nop 1
	v_addc_co_u32_e32 v7, vcc, 0, v3, vcc
	global_store_short_d16_hi v[6:7], v8, off offset:-4096
	v_mul_f32_e32 v8, v46, v14
	v_bfe_u32 v9, v8, 16, 1
	v_add3_u32 v8, v8, v9, s61
	global_store_short_d16_hi v[4:5], v8, off offset:64
	v_mul_f32_e32 v8, v62, v14
	v_bfe_u32 v9, v8, 16, 1
	v_add3_u32 v8, v8, v9, s61
	global_store_short_d16_hi v[4:5], v8, off offset:128
	v_mul_f32_e32 v8, v78, v14
	v_bfe_u32 v9, v8, 16, 1
	v_add3_u32 v8, v8, v9, s61
	global_store_short_d16_hi v[4:5], v8, off offset:192
	v_mul_f32_e32 v4, v31, v15
	v_bfe_u32 v5, v4, 16, 1
	v_add3_u32 v4, v4, v5, s61
	global_store_short_d16_hi v[6:7], v4, off
	v_mul_f32_e32 v4, v47, v15
	v_bfe_u32 v5, v4, 16, 1
	v_add3_u32 v4, v4, v5, s61
	global_store_short_d16_hi v[6:7], v4, off offset:64
	v_mul_f32_e32 v4, v63, v15
	v_bfe_u32 v5, v4, 16, 1
	v_add3_u32 v4, v4, v5, s61
	global_store_short_d16_hi v[6:7], v4, off offset:128
	v_mul_f32_e32 v4, v79, v15
	v_bfe_u32 v5, v4, 16, 1
	v_add3_u32 v4, v4, v5, s61
	global_store_short_d16_hi v[6:7], v4, off offset:192
	v_mul_f32_e32 v4, v32, v16
	v_bfe_u32 v5, v4, 16, 1
	v_add3_u32 v6, v4, v5, s61
	v_add_co_u32_e32 v4, vcc, s80, v2
	s_nop 1
	v_addc_co_u32_e32 v5, vcc, 0, v3, vcc
	v_add_co_u32_e32 v2, vcc, s81, v2
	s_nop 1
	v_addc_co_u32_e32 v3, vcc, 0, v3, vcc
	global_store_short_d16_hi v[2:3], v6, off offset:-4096
	v_mul_f32_e32 v6, v48, v16
	v_bfe_u32 v7, v6, 16, 1
	v_add3_u32 v6, v6, v7, s61
	global_store_short_d16_hi v[4:5], v6, off offset:64
	v_mul_f32_e32 v6, v64, v16
	v_bfe_u32 v7, v6, 16, 1
	v_add3_u32 v6, v6, v7, s61
	global_store_short_d16_hi v[4:5], v6, off offset:128
	v_mul_f32_e32 v6, v80, v16
	v_bfe_u32 v7, v6, 16, 1
	v_add3_u32 v6, v6, v7, s61
	global_store_short_d16_hi v[4:5], v6, off offset:192
	v_mul_f32_e32 v4, v33, v17
	v_bfe_u32 v5, v4, 16, 1
	v_add3_u32 v4, v4, v5, s61
	global_store_short_d16_hi v[2:3], v4, off
	v_mul_f32_e32 v4, v49, v17
	v_bfe_u32 v5, v4, 16, 1
	v_add3_u32 v4, v4, v5, s61
	global_store_short_d16_hi v[2:3], v4, off offset:64
	v_mul_f32_e32 v4, v65, v17
	v_bfe_u32 v5, v4, 16, 1
	v_add3_u32 v4, v4, v5, s61
	global_store_short_d16_hi v[2:3], v4, off offset:128
	v_mul_f32_e32 v4, v81, v17
	v_bfe_u32 v5, v4, 16, 1
	v_add3_u32 v4, v4, v5, s61
	global_store_short_d16_hi v[2:3], v4, off offset:192
	s_cmp_lt_i32 s49, 4
	s_cbranch_scc1 .LBB0_260

; #define ATT_SBAR() __builtin_amdgcn_sched_barrier(0)
; __device__ __forceinline__ unsigned cvtpk(float lo, float hi) { f32x2_t v = {lo, hi}; bf16x2_t b = __builtin_convertvector(v, bf16x2_t); return __builtin_bit_cast(unsigned, b); }
; __device__ __forceinline__ int v_rd_base(int lane) { return ((lane & 3) << 3) | (((lane >> 2) & 3) << 6) | (((lane >> 4) & 1) << 5) | (((lane >> 5) & 1) << 8); }
; #define ATT_LOAD_K(t) do { const unsigned so_ = (unsigned)(t) * (unsigned)(KVBLK * LDK * 2); sk0 = __builtin_bit_cast(bf16x8, __builtin_amdgcn_raw_buffer_load_b128(krs, koff, so_, 0)); \
;     if constexpr (DQK == 128) sk1 = __builtin_bit_cast(bf16x8, __builtin_amdgcn_raw_buffer_load_b128(krs, koff, so_ + (unsigned)(32 * LDK * 2), 0)); } while (0)
; #define ATT_BAR() do { ATT_SBAR(); asm volatile("s_barrier" ::: "memory"); ATT_SBAR(); } while (0)
;     ...
;   if constexpr (DQK == 64) { sk0 = ek0; sv0 = ev0; sv1 = ev1; ATT_WRITE_K(0); ATT_WRITE_V(0); sk0 = ek1; ATT_WRITE_K(SHM_K); }
;   else { ATT_LOAD_K(0); ATT_LOAD_V(0); ATT_WRITE_K(0); ATT_WRITE_V(0);
;          ATT_LOAD_K(1); ATT_WRITE_K(SHM_K); }
;   ATT_LOAD_K(2); ATT_LOAD_V(1);
;   asm volatile("s_waitcnt lgkmcnt(0)" ::: "memory"); ATT_BAR();
;   if (grp == 1) ATT_BAR();
;   qkt<DQK>(p0, p1, K_lds, qr, r32, hi);
;   ATT_BAR();
;   int k1 = SHM_K, k2 = 2 * SHM_K, k0 = 0, v0 = 0, v1 = SHM_V, v2 = 2 * SHM_V;
;   const lds_cptr kq0 = (lds_cptr)K_lds, vq0 = (lds_cptr)V_lds + v_rd_base(lane);
;   bf16x8 kf[8]; s16x4 va[8], vc[8];
;     ...
;   for (int t = 0; t + 1 < NT; ++t) {
;     if constexpr (ABL & 1) { u32x4 w0 = {cvtpk(p0[0], p0[1]), cvtpk(p0[2], p0[3]), cvtpk(p0[4], p0[5]), cvtpk(p0[6], p0[7])}, w1 = {cvtpk(p0[8], p0[9]), cvtpk(p0[10], p0[11]), cvtpk(p0[12], p0[13]), cvtpk(p0[14], p0[15])};
;         u32x4 w2 = {cvtpk(p1[0], p1[1]), cvtpk(p1[2], p1[3]), cvtpk(p1[4], p1[5]), cvtpk(p1[6], p1[7])}, w3 = {cvtpk(p1[8], p1[9]), cvtpk(p1[10], p1[11]), cvtpk(p1[12], p1[13]), cvtpk(p1[14], p1[15])};
;         pa0 = *reinterpret_cast<bf16x8*>(&w0); pa1 = *reinterpret_cast<bf16x8*>(&w1); pa2 = *reinterpret_cast<bf16x8*>(&w2); pa3 = *reinterpret_cast<bf16x8*>(&w3); }
;     else { ATT_SOFTMAX(t == 0); }
;     if constexpr (!(ABL & 4)) { ATT_WRITE_K(k2); ATT_WRITE_V(v1); }
;     ATT_SBAR();
; #pragma unroll
;     for (int ks = 0; ks < 4; ++ks) ATT_VPAIR(va, v0, 0, ks);
;     asm volatile("s_waitcnt lgkmcnt(8)" ::: "memory"); ATT_BAR();
.LBB0_281:
	v_mul_u32_u24_e32 v18, 0x90, v62
	v_add3_u32 v78, 0, v184, v18
	ds_read_b128 v[18:21], v78 offset:49152
	v_mad_u32_u24 v166, v62, s82, 0
	v_add_u32_e32 v172, v166, v184
	ds_read_b128 v[34:37], v172 offset:53760
	ds_read_b128 v[66:69], v78 offset:49184
	ds_read_b128 v[70:73], v78 offset:49216
	s_and_b32 s4, s92, 0x3fffffc0
	v_and_b32_e32 v63, 63, v63
	s_lshl_b32 s4, s4, 2
	s_add_i32 s6, s4, 0
	s_waitcnt lgkmcnt(3)
	v_mfma_f32_32x32x16_bf16 v[18:33], v[18:21], v[136:139], 0
	s_add_i32 s6, s6, 0x23080
	s_mov_b32 s97, 1
	s_waitcnt lgkmcnt(2)
	v_mfma_f32_32x32x16_bf16 v[34:49], v[34:37], v[136:139], 0
	s_waitcnt lgkmcnt(1)
	v_mfma_f32_32x32x16_bf16 v[18:33], v[66:69], v[140:143], v[18:33]
	ds_read_b128 v[66:69], v78 offset:53792
	ds_read_b128 v[74:77], v78 offset:49248
	s_waitcnt lgkmcnt(1)
	v_mfma_f32_32x32x16_bf16 v[34:49], v[66:69], v[140:143], v[34:49]
	v_mfma_f32_32x32x16_bf16 v[18:33], v[70:73], v[144:147], v[18:33]
	ds_read_b128 v[66:69], v78 offset:53824
	ds_read_b128 v[70:73], v78 offset:53856
	s_waitcnt lgkmcnt(1)
	v_mfma_f32_32x32x16_bf16 v[34:49], v[66:69], v[144:147], v[34:49]
	v_lshlrev_b32_e32 v67, 3, v63
	v_lshlrev_b32_e32 v69, 4, v63
	v_add_u32_e32 v66, 0xc000, v169
	v_and_b32_e32 v68, 24, v67
	v_and_b32_e32 v69, 0xc0, v69
	v_and_b32_e32 v67, 0x100, v67
	v_mfma_f32_32x32x16_bf16 v[18:33], v[74:77], v[148:151], v[18:33]
	v_lshlrev_b32_e32 v74, 1, v63
	v_and_b32_e32 v74, 32, v74
	s_waitcnt lgkmcnt(0)
	v_mfma_f32_32x32x16_bf16 v[34:49], v[70:73], v[148:151], v[34:49]
	s_barrier
	v_cmp_gt_u32_e64 s[4:5], 32, v63
	v_lshl_add_u32 v165, v62, 2, s6
	s_nop 9
	v_add_f32_e32 v62, 0, v34
	v_max3_f32 v63, v62, v18, v19
	v_max3_f32 v63, v63, v20, v21
	v_max3_f32 v63, v63, v22, v23
	v_max3_f32 v63, v63, v24, v25
	v_max3_f32 v63, v63, v26, v27
	v_max3_f32 v63, v63, v28, v29
	v_max3_f32 v63, v63, v30, v31
	v_max3_f32 v63, v63, v32, v33
	s_nop 4
	v_add3_u32 v68, 0, v68, v69
	v_max3_f32 v62, v63, v35, v36
	v_max3_f32 v62, v62, v37, v38
	v_max3_f32 v62, v62, v39, v40
	v_max3_f32 v62, v62, v41, v42
	v_max3_f32 v62, v62, v43, v44
	v_max3_f32 v62, v62, v45, v46
	v_max3_f32 v62, v62, v47, v48
	v_max_f32 v62, v62, v49
	v_add3_u32 v131, v68, v74, v67
	v_mov_b32_e32 v63, v62
	s_nop 1
	v_permlane32_swap_b32_e32 v62, v63
	v_max_f32_e32 v63, v63, v63
	v_max_f32_e32 v62, v62, v62
	v_max_f32_e32 v62, v62, v63
	v_sub_f32_e32 v18, v18, v62
	v_sub_f32_e32 v34, v34, v62
	v_sub_f32_e32 v19, v19, v62
	v_sub_f32_e32 v35, v35, v62
	v_sub_f32_e32 v20, v20, v62
	v_sub_f32_e32 v36, v36, v62
	v_sub_f32_e32 v21, v21, v62
	v_sub_f32_e32 v37, v37, v62
	v_sub_f32_e32 v22, v22, v62
	v_sub_f32_e32 v38, v38, v62
	v_sub_f32_e32 v23, v23, v62
	v_sub_f32_e32 v39, v39, v62
	v_sub_f32_e32 v24, v24, v62
	v_sub_f32_e32 v40, v40, v62
	v_sub_f32_e32 v25, v25, v62
	v_sub_f32_e32 v41, v41, v62
	v_sub_f32_e32 v26, v26, v62
	v_sub_f32_e32 v42, v42, v62
	v_sub_f32_e32 v27, v27, v62
	v_sub_f32_e32 v43, v43, v62
	v_sub_f32_e32 v28, v28, v62
	v_sub_f32_e32 v44, v44, v62
	v_sub_f32_e32 v29, v29, v62
	v_sub_f32_e32 v45, v45, v62
	v_sub_f32_e32 v30, v30, v62
	v_sub_f32_e32 v46, v46, v62
	v_sub_f32_e32 v31, v31, v62
	v_sub_f32_e32 v47, v47, v62
	v_sub_f32_e32 v32, v32, v62
	v_sub_f32_e32 v48, v48, v62
	v_sub_f32_e32 v33, v33, v62
	v_sub_f32_e32 v49, v49, v62
	v_exp_f32_e32 v18, v18
	v_exp_f32_e32 v34, v34
	v_exp_f32_e32 v19, v19
	v_exp_f32_e32 v35, v35
	v_exp_f32_e32 v20, v20
	v_exp_f32_e32 v36, v36
	v_exp_f32_e32 v21, v21
	v_exp_f32_e32 v37, v37
	v_exp_f32_e32 v22, v22
	v_exp_f32_e32 v38, v38
	v_exp_f32_e32 v23, v23
	v_exp_f32_e32 v39, v39
	v_exp_f32_e32 v24, v24
	v_exp_f32_e32 v40, v40
	v_exp_f32_e32 v25, v25
	v_exp_f32_e32 v41, v41
	v_exp_f32_e32 v26, v26
	v_exp_f32_e32 v42, v42
	v_exp_f32_e32 v27, v27
	v_exp_f32_e32 v43, v43
	v_exp_f32_e32 v28, v28
	v_exp_f32_e32 v44, v44
	v_exp_f32_e32 v29, v29
	v_exp_f32_e32 v45, v45
	v_exp_f32_e32 v30, v30
	v_exp_f32_e32 v46, v46
	v_exp_f32_e32 v31, v31
	v_exp_f32_e32 v47, v47
	v_exp_f32_e32 v32, v32
	v_exp_f32_e32 v48, v48
	v_exp_f32_e32 v33, v33
	v_exp_f32_e32 v49, v49
	v_sub_f32_e32 v82, 0, v62
	v_mov_b32_e32 v83, v82
	v_mov_b32_e32 v84, v82
	v_mov_b32_e32 v85, v82
	v_mov_b32_e32 v86, v82
	v_mov_b32_e32 v87, v82
	v_mov_b32_e32 v88, v82
	v_mov_b32_e32 v89, v82
	v_mov_b32_e32 v90, v82
	v_mov_b32_e32 v91, v82
	v_mov_b32_e32 v92, v82
	v_mov_b32_e32 v93, v82
	v_mov_b32_e32 v94, v82
	v_mov_b32_e32 v95, v82
	v_mov_b32_e32 v96, v82
	v_mov_b32_e32 v97, v82
	v_cvt_pk_bf16_f32 v98, v18, v19
	v_cvt_pk_bf16_f32 v99, v20, v21
	v_cvt_pk_bf16_f32 v100, v22, v23
	v_cvt_pk_bf16_f32 v101, v24, v25
	v_cvt_pk_bf16_f32 v102, v26, v27
	v_cvt_pk_bf16_f32 v103, v28, v29
	v_cvt_pk_bf16_f32 v104, v30, v31
	v_cvt_pk_bf16_f32 v105, v32, v33
	v_cvt_pk_bf16_f32 v106, v34, v35
	v_cvt_pk_bf16_f32 v107, v36, v37
	v_cvt_pk_bf16_f32 v108, v38, v39
	v_cvt_pk_bf16_f32 v109, v40, v41
	v_cvt_pk_bf16_f32 v110, v42, v43
	v_cvt_pk_bf16_f32 v111, v44, v45
	v_cvt_pk_bf16_f32 v112, v46, v47
	v_cvt_pk_bf16_f32 v113, v48, v49
	s_waitcnt vmcnt(1)
	ds_write_b128 v66, v[58:61] offset:18432
	ds_write_b128 v64, v[50:53] offset:16384
	s_waitcnt vmcnt(0)
	ds_write_b128 v65, v[54:57] offset:16384
	ds_read_b64_tr_b16 v[18:19], v131
	ds_read_b64_tr_b16 v[20:21], v131 offset:2048
	ds_read_b64_tr_b16 v[34:35], v131 offset:4096
	ds_read_b64_tr_b16 v[36:37], v131 offset:6144
	ds_read_b64_tr_b16 v[38:39], v131 offset:8192
	ds_read_b64_tr_b16 v[40:41], v131 offset:10240
	ds_read_b64_tr_b16 v[42:43], v131 offset:12288
	ds_read_b64_tr_b16 v[44:45], v131 offset:14336
	s_waitcnt lgkmcnt(8)
	s_barrier
	s_setprio 2
	s_waitcnt lgkmcnt(6)
	v_mfma_f32_32x32x16_bf16 v[18:33], v[98:101], v[18:21], 0
	ds_read_b64_tr_b16 v[46:47], v131 offset:512
	ds_read_b64_tr_b16 v[48:49], v131 offset:2560
	s_waitcnt lgkmcnt(6)
	v_mfma_f32_32x32x16_bf16 v[18:33], v[102:105], v[34:37], v[18:33]
	ds_read_b64_tr_b16 v[50:51], v131 offset:4608
	ds_read_b64_tr_b16 v[52:53], v131 offset:6656
	s_waitcnt lgkmcnt(6)
	v_mfma_f32_32x32x16_bf16 v[18:33], v[106:109], v[38:41], v[18:33]
	ds_read_b64_tr_b16 v[54:55], v131 offset:8704
	ds_read_b64_tr_b16 v[56:57], v131 offset:10752
	s_waitcnt lgkmcnt(6)
	v_mfma_f32_32x32x16_bf16 v[18:33], v[110:113], v[42:45], v[18:33]
	ds_read_b64_tr_b16 v[58:59], v131 offset:12800
	ds_read_b64_tr_b16 v[60:61], v131 offset:14848
	s_waitcnt lgkmcnt(6)
	v_mfma_f32_32x32x16_bf16 v[34:49], v[98:101], v[46:49], 0
	ds_read_b64_tr_b16 v[62:63], v131 offset:1024
	ds_read_b64_tr_b16 v[64:65], v131 offset:3072
	s_waitcnt lgkmcnt(6)
	v_mfma_f32_32x32x16_bf16 v[34:49], v[102:105], v[50:53], v[34:49]
	ds_read_b64_tr_b16 v[66:67], v131 offset:5120
	ds_read_b64_tr_b16 v[68:69], v131 offset:7168
	s_waitcnt lgkmcnt(6)
	v_mfma_f32_32x32x16_bf16 v[34:49], v[106:109], v[54:57], v[34:49]
	ds_read_b64_tr_b16 v[70:71], v131 offset:9216
	ds_read_b64_tr_b16 v[72:73], v131 offset:11264
	s_waitcnt lgkmcnt(6)
	v_mfma_f32_32x32x16_bf16 v[34:49], v[110:113], v[58:61], v[34:49]
	ds_read_b64_tr_b16 v[74:75], v131 offset:13312
	ds_read_b64_tr_b16 v[76:77], v131 offset:15360
	s_waitcnt lgkmcnt(6)
	v_mfma_f32_32x32x16_bf16 v[50:65], v[98:101], v[62:65], 0
	ds_read_b64_tr_b16 v[78:79], v131 offset:1536
	ds_read_b64_tr_b16 v[80:81], v131 offset:3584
	s_waitcnt lgkmcnt(6)
	v_mfma_f32_32x32x16_bf16 v[50:65], v[102:105], v[66:69], v[50:65]
	ds_read_b64_tr_b16 v[114:115], v131 offset:5632
	ds_read_b64_tr_b16 v[116:117], v131 offset:7680
	s_waitcnt lgkmcnt(6)
	v_mfma_f32_32x32x16_bf16 v[50:65], v[106:109], v[70:73], v[50:65]
	ds_read_b64_tr_b16 v[118:119], v131 offset:9728
	ds_read_b64_tr_b16 v[120:121], v131 offset:11776
	s_waitcnt lgkmcnt(6)
	v_mfma_f32_32x32x16_bf16 v[50:65], v[110:113], v[74:77], v[50:65]
	ds_read_b64_tr_b16 v[122:123], v131 offset:13824
	ds_read_b64_tr_b16 v[124:125], v131 offset:15872
	s_waitcnt lgkmcnt(6)
	v_mfma_f32_32x32x16_bf16 v[66:81], v[98:101], v[78:81], 0
	ds_read_b128 v[126:129], v172 offset:58368
	s_waitcnt lgkmcnt(5)
	v_mfma_f32_32x32x16_bf16 v[66:81], v[102:105], v[114:117], v[66:81]
	ds_read_b128 v[152:155], v172 offset:62976
	s_waitcnt lgkmcnt(4)
	v_mfma_f32_32x32x16_bf16 v[66:81], v[106:109], v[118:121], v[66:81]
	ds_read_b128 v[156:159], v172 offset:58400
	s_waitcnt lgkmcnt(3)
	v_mfma_f32_32x32x16_bf16 v[66:81], v[110:113], v[122:125], v[66:81]
	ds_read_b128 v[160:163], v172 offset:63008
	v_mfma_f32_16x16x32_bf16 v[240:243], v[98:101], v[132:135], 0
	ds_read_b128 v[174:177], v172 offset:58432
	v_mfma_f32_16x16x32_bf16 v[240:243], v[102:105], v[132:135], v[240:243]
	ds_read_b128 v[178:181], v172 offset:63040
	v_mfma_f32_16x16x32_bf16 v[240:243], v[106:109], v[132:135], v[240:243]
	ds_read_b128 v[186:189], v172 offset:58464
	v_mfma_f32_16x16x32_bf16 v[240:243], v[110:113], v[132:135], v[240:243]
	ds_read_b128 v[190:193], v172 offset:63072
	s_waitcnt lgkmcnt(7)
	v_mfma_f32_32x32x16_bf16 v[98:113], v[126:129], v[136:139], v[82:97]
	v_mov_b64_e32 v[128:129], v[96:97]
	v_mov_b64_e32 v[126:127], v[94:95]
	v_mov_b64_e32 v[124:125], v[92:93]
	v_mov_b64_e32 v[122:123], v[90:91]
	v_mov_b64_e32 v[120:121], v[88:89]
	v_mov_b64_e32 v[118:119], v[86:87]
	v_mov_b64_e32 v[116:117], v[84:85]
	v_mov_b64_e32 v[114:115], v[82:83]
	s_waitcnt lgkmcnt(6)
	s_nop 0
	v_mfma_f32_32x32x16_bf16 v[114:129], v[152:155], v[136:139], v[114:129]
	s_waitcnt lgkmcnt(5)
	v_mfma_f32_32x32x16_bf16 v[98:113], v[156:159], v[140:143], v[98:113]
	s_waitcnt lgkmcnt(4)
	v_mfma_f32_32x32x16_bf16 v[114:129], v[160:163], v[140:143], v[114:129]
	s_waitcnt lgkmcnt(3)
	v_mfma_f32_32x32x16_bf16 v[98:113], v[174:177], v[144:147], v[98:113]
	s_waitcnt lgkmcnt(2)
	v_mfma_f32_32x32x16_bf16 v[114:129], v[178:181], v[144:147], v[114:129]
	s_waitcnt lgkmcnt(1)
	v_mfma_f32_32x32x16_bf16 v[98:113], v[186:189], v[148:151], v[98:113]
	s_waitcnt lgkmcnt(0)
	v_mfma_f32_32x32x16_bf16 v[114:129], v[190:193], v[148:151], v[114:129]
	s_setprio 0
	s_mov_b32 s14, s10
	s_mov_b32 s15, s11
	buffer_load_dwordx4 v[224:227], v170, s[8:11], s85 offen
	buffer_load_dwordx4 v[228:231], v171, s[12:15], s83 offen
	buffer_load_dwordx4 v[232:235], v171, s[12:15], s86 offen
	s_barrier
	s_mov_b32 s95, 0x8000
	s_movk_i32 s15, 0x4000
	s_movk_i32 s18, 0x2400
	s_mov_b32 s94, 0
	s_movk_i32 s14, 0x4800
	s_mov_b32 s36, 0x70000
	s_mov_b32 s93, 0
	v_add_f32_e32 v173, 0, v114
	v_max3_f32 v174, v173, v98, v99
	v_max3_f32 v174, v174, v100, v101
	v_max3_f32 v174, v174, v102, v103
	v_max3_f32 v174, v174, v104, v105
	v_max3_f32 v174, v174, v106, v107
	v_max3_f32 v174, v174, v108, v109
	v_max3_f32 v174, v174, v110, v111
	v_max3_f32 v174, v174, v112, v113
	v_max3_f32 v173, v174, v115, v116
	v_max3_f32 v173, v173, v117, v118
	v_max3_f32 v173, v173, v119, v120
	v_max3_f32 v173, v173, v121, v122
	v_max3_f32 v173, v173, v123, v124
	v_max3_f32 v173, v173, v125, v126
	v_max3_f32 v173, v173, v127, v128
	v_max_f32 v173, v173, v129

; #define ATT_SBAR() __builtin_amdgcn_sched_barrier(0)
; __device__ __forceinline__ unsigned cvtpk(float lo, float hi) { f32x2_t v = {lo, hi}; bf16x2_t b = __builtin_convertvector(v, bf16x2_t); return __builtin_bit_cast(unsigned, b); }
; #define ATT_LOAD_K(t) do { const unsigned so_ = (unsigned)(t) * (unsigned)(KVBLK * LDK * 2); sk0 = __builtin_bit_cast(bf16x8, __builtin_amdgcn_raw_buffer_load_b128(krs, koff, so_, 0)); \
;     if constexpr (DQK == 128) sk1 = __builtin_bit_cast(bf16x8, __builtin_amdgcn_raw_buffer_load_b128(krs, koff, so_ + (unsigned)(32 * LDK * 2), 0)); } while (0)
; #define ATT_LOAD_V(t) do { const unsigned so_ = (unsigned)(t) * (unsigned)(KVBLK * LDV * 2); sv0 = __builtin_bit_cast(bf16x8, __builtin_amdgcn_raw_buffer_load_b128(vrs, voff, so_, 0)); \
;     sv1 = __builtin_bit_cast(bf16x8, __builtin_amdgcn_raw_buffer_load_b128(vrs, voff, so_ + (unsigned)(32 * LDV * 2), 0)); } while (0)
; #define ATT_WRITE_K(so) do { *(bf16x8*)(K_lds + (so) + kswz<DQK>(kr, kc * 2)) = sk0; if constexpr (DQK == 128) *(bf16x8*)(K_lds + (so) + kswz<DQK>(32 + kr, kc * 2)) = sk1; } while (0)
; #define ATT_WRITE_V(so) do { *(bf16x8*)(V_lds + (so) + vst0) = sv0; *(bf16x8*)(V_lds + (so) + vst1) = sv1; } while (0)
;     ...
;   for (int t = 0; t + 1 < NT; ++t) {
;     if constexpr (ABL & 1) { u32x4 w0 = {cvtpk(p0[0], p0[1]), cvtpk(p0[2], p0[3]), cvtpk(p0[4], p0[5]), cvtpk(p0[6], p0[7])}, w1 = {cvtpk(p0[8], p0[9]), cvtpk(p0[10], p0[11]), cvtpk(p0[12], p0[13]), cvtpk(p0[14], p0[15])};
;         u32x4 w2 = {cvtpk(p1[0], p1[1]), cvtpk(p1[2], p1[3]), cvtpk(p1[4], p1[5]), cvtpk(p1[6], p1[7])}, w3 = {cvtpk(p1[8], p1[9]), cvtpk(p1[10], p1[11]), cvtpk(p1[12], p1[13]), cvtpk(p1[14], p1[15])};
;         pa0 = *reinterpret_cast<bf16x8*>(&w0); pa1 = *reinterpret_cast<bf16x8*>(&w1); pa2 = *reinterpret_cast<bf16x8*>(&w2); pa3 = *reinterpret_cast<bf16x8*>(&w3); }
;     else { ATT_SOFTMAX(t == 0); }
;     if constexpr (!(ABL & 4)) { ATT_WRITE_K(k2); ATT_WRITE_V(v1); }
;     ATT_SBAR();
; #pragma unroll
;     for (int ks = 0; ks < 4; ++ks) ATT_VPAIR(va, v0, 0, ks);
;     asm volatile("s_waitcnt lgkmcnt(8)" ::: "memory"); ATT_BAR();
;     ATT_XSECTION(true);
;     if constexpr (!(ABL & 4)) { const int tk = (t + 3 < NT) ? t + 3 : NT - 1, tv = (t + 2 < NT) ? t + 2 : NT - 1; ATT_LOAD_K(tk); ATT_LOAD_V(tv); }
;     ATT_BAR();
.LBB0_283:
	v_exp_f32_e32 v98, v98
	v_exp_f32_e32 v114, v114
	v_exp_f32_e32 v99, v99
	v_exp_f32_e32 v115, v115
	v_exp_f32_e32 v100, v100
	v_exp_f32_e32 v101, v101
	v_exp_f32_e32 v102, v102
	v_exp_f32_e32 v103, v103
	v_exp_f32_e32 v106, v106
	v_exp_f32_e32 v107, v107
	v_exp_f32_e32 v116, v116
	v_exp_f32_e32 v117, v117
	v_exp_f32_e32 v118, v118
	v_exp_f32_e32 v119, v119
	v_exp_f32_e32 v104, v104
	v_exp_f32_e32 v120, v120
	v_exp_f32_e32 v105, v105
	v_exp_f32_e32 v121, v121
	v_exp_f32_e32 v122, v122
	v_exp_f32_e32 v123, v123
	v_exp_f32_e32 v108, v108
	v_exp_f32_e32 v124, v124
	v_exp_f32_e32 v109, v109
	v_exp_f32_e32 v125, v125
	v_exp_f32_e32 v110, v110
	v_exp_f32_e32 v126, v126
	v_exp_f32_e32 v111, v111
	v_exp_f32_e32 v127, v127
	v_exp_f32_e32 v112, v112
	v_exp_f32_e32 v128, v128
	v_exp_f32_e32 v113, v113
	v_exp_f32_e32 v129, v129
	v_cvt_pk_bf16_f32 v2, v98, v99
	v_cvt_pk_bf16_f32 v3, v100, v101
	v_cvt_pk_bf16_f32 v4, v102, v103
	v_cvt_pk_bf16_f32 v6, v106, v107
	v_cvt_pk_bf16_f32 v10, v114, v115
	v_cvt_pk_bf16_f32 v5, v104, v105
	v_cvt_pk_bf16_f32 v7, v108, v109
	v_cvt_pk_bf16_f32 v8, v110, v111
	v_cvt_pk_bf16_f32 v9, v112, v113
	v_cvt_pk_bf16_f32 v11, v116, v117
	v_cvt_pk_bf16_f32 v12, v118, v119
	v_cvt_pk_bf16_f32 v13, v120, v121
	v_cvt_pk_bf16_f32 v14, v122, v123
	v_cvt_pk_bf16_f32 v15, v124, v125
	v_cvt_pk_bf16_f32 v16, v126, v127
	v_cvt_pk_bf16_f32 v17, v128, v129
	s_waitcnt vmcnt(0)
	v_add_u32_e32 v114, s94, v169
	ds_write_b128 v114, v[224:227] offset:49152
	v_add_u32_e32 v114, s95, v167
	ds_write_b128 v114, v[228:231]
	v_add_u32_e32 v114, s95, v168
	ds_write_b128 v114, v[232:235]
	v_add_u32_e32 v249, s96, v172
	ds_read_b128 v[152:155], v249 offset:49152
	ds_read_b128 v[156:159], v249 offset:53760
	ds_read_b128 v[160:163], v249 offset:49184
	ds_read_b128 v[176:179], v249 offset:53792
	s_waitcnt lgkmcnt(4)
	s_barrier
	s_setprio 2
	s_waitcnt lgkmcnt(3)
	v_mfma_f32_32x32x16_bf16 v[98:113], v[152:155], v[136:139], v[82:97]
	ds_read_b128 v[180:183], v249 offset:49216
	s_waitcnt lgkmcnt(3)
	v_mfma_f32_32x32x16_bf16 v[114:129], v[156:159], v[136:139], v[82:97]
	ds_read_b128 v[186:189], v249 offset:53824
	v_add_u32_e32 v248, s37, v131
	s_waitcnt lgkmcnt(3)
	v_mfma_f32_32x32x16_bf16 v[98:113], v[160:163], v[140:143], v[98:113]
	ds_read_b128 v[190:193], v249 offset:49248
	ds_read_b64_tr_b16 v[198:199], v248
	ds_read_b64_tr_b16 v[200:201], v248 offset:2048
	s_waitcnt lgkmcnt(5)
	v_mfma_f32_32x32x16_bf16 v[114:129], v[176:179], v[140:143], v[114:129]
	ds_read_b128 v[194:197], v249 offset:53856
	ds_read_b64_tr_b16 v[212:213], v248 offset:4096
	ds_read_b64_tr_b16 v[214:215], v248 offset:6144
	s_waitcnt lgkmcnt(7)
	v_mfma_f32_32x32x16_bf16 v[98:113], v[180:183], v[144:147], v[98:113]
	ds_read_b64_tr_b16 v[216:217], v248 offset:8192
	ds_read_b64_tr_b16 v[218:219], v248 offset:10240
	s_waitcnt lgkmcnt(8)
	v_mfma_f32_32x32x16_bf16 v[114:129], v[186:189], v[144:147], v[114:129]
	ds_read_b64_tr_b16 v[220:221], v248 offset:12288
	ds_read_b64_tr_b16 v[222:223], v248 offset:14336
	s_waitcnt lgkmcnt(9)
	v_mfma_f32_32x32x16_bf16 v[98:113], v[190:193], v[148:151], v[98:113]
	s_waitcnt lgkmcnt(6)
	v_mfma_f32_32x32x16_bf16 v[114:129], v[194:197], v[148:151], v[114:129]
	v_mfma_f32_32x32x16_bf16 v[18:33], v[2:5], v[198:201], v[18:33]
	ds_read_b64_tr_b16 v[236:237], v248 offset:512
	ds_read_b64_tr_b16 v[238:239], v248 offset:2560
	s_waitcnt lgkmcnt(6)
	v_mfma_f32_32x32x16_bf16 v[18:33], v[6:9], v[212:215], v[18:33]
	ds_read_b64_tr_b16 v[198:199], v248 offset:4608
	ds_read_b64_tr_b16 v[200:201], v248 offset:6656
	s_waitcnt lgkmcnt(6)
	v_mfma_f32_32x32x16_bf16 v[18:33], v[10:13], v[216:219], v[18:33]
	ds_read_b64_tr_b16 v[212:213], v248 offset:8704
	ds_read_b64_tr_b16 v[214:215], v248 offset:10752
	s_waitcnt lgkmcnt(6)
	v_mfma_f32_32x32x16_bf16 v[18:33], v[14:17], v[220:223], v[18:33]
	ds_read_b64_tr_b16 v[216:217], v248 offset:12800
	ds_read_b64_tr_b16 v[218:219], v248 offset:14848
	v_max3_f32 v249, v98, v99, v100
	s_waitcnt lgkmcnt(6)
	v_mfma_f32_32x32x16_bf16 v[34:49], v[2:5], v[236:239], v[34:49]
	ds_read_b64_tr_b16 v[220:221], v248 offset:1024
	ds_read_b64_tr_b16 v[222:223], v248 offset:3072
	v_max3_f32 v173, v114, v115, v116
	s_waitcnt lgkmcnt(6)
	v_mfma_f32_32x32x16_bf16 v[34:49], v[6:9], v[198:201], v[34:49]
	ds_read_b64_tr_b16 v[236:237], v248 offset:5120
	ds_read_b64_tr_b16 v[238:239], v248 offset:7168
	v_max3_f32 v249, v249, v101, v102
	s_waitcnt lgkmcnt(6)
	v_mfma_f32_32x32x16_bf16 v[34:49], v[10:13], v[212:215], v[34:49]
	ds_read_b64_tr_b16 v[198:199], v248 offset:9216
	ds_read_b64_tr_b16 v[200:201], v248 offset:11264
	v_max3_f32 v173, v173, v117, v118
	s_waitcnt lgkmcnt(6)
	v_mfma_f32_32x32x16_bf16 v[34:49], v[14:17], v[216:219], v[34:49]
	ds_read_b64_tr_b16 v[212:213], v248 offset:13312
	ds_read_b64_tr_b16 v[214:215], v248 offset:15360
	v_max3_f32 v249, v249, v103, v104
	s_waitcnt lgkmcnt(6)
	v_mfma_f32_32x32x16_bf16 v[50:65], v[2:5], v[220:223], v[50:65]
	ds_read_b64_tr_b16 v[216:217], v248 offset:1536
	ds_read_b64_tr_b16 v[218:219], v248 offset:3584
	v_max3_f32 v173, v173, v119, v120
	s_waitcnt lgkmcnt(6)
	v_mfma_f32_32x32x16_bf16 v[50:65], v[6:9], v[236:239], v[50:65]
	ds_read_b64_tr_b16 v[220:221], v248 offset:5632
	ds_read_b64_tr_b16 v[222:223], v248 offset:7680
	v_max3_f32 v249, v249, v105, v106
	s_waitcnt lgkmcnt(6)
	v_mfma_f32_32x32x16_bf16 v[50:65], v[10:13], v[198:201], v[50:65]
	ds_read_b64_tr_b16 v[236:237], v248 offset:9728
	ds_read_b64_tr_b16 v[238:239], v248 offset:11776
	v_max3_f32 v173, v173, v121, v122
	s_waitcnt lgkmcnt(6)
	v_mfma_f32_32x32x16_bf16 v[50:65], v[14:17], v[212:215], v[50:65]
	ds_read_b64_tr_b16 v[198:199], v248 offset:13824
	ds_read_b64_tr_b16 v[200:201], v248 offset:15872
	v_max3_f32 v249, v249, v107, v108
	s_waitcnt lgkmcnt(6)
	v_mfma_f32_32x32x16_bf16 v[66:81], v[2:5], v[216:219], v[66:81]
	v_max3_f32 v173, v173, v123, v124
	s_min_u32 s14, s97, 0x7c
	s_lshl_b32 s14, s14, 17
	s_add_i32 s14, s14, 0x60000
	buffer_load_dwordx4 v[224:227], v170, s[8:11], s14 offen
	s_waitcnt lgkmcnt(4)
	v_mfma_f32_32x32x16_bf16 v[66:81], v[6:9], v[220:223], v[66:81]
	v_max3_f32 v249, v249, v109, v110
	s_add_i32 s19, s36, 0xffff0000
	s_mov_b32 s14, s10
	s_mov_b32 s15, s11
	buffer_load_dwordx4 v[228:231], v171, s[12:15], s19 offen
	s_waitcnt lgkmcnt(2)
	v_mfma_f32_32x32x16_bf16 v[66:81], v[10:13], v[236:239], v[66:81]
	v_max3_f32 v173, v173, v125, v126
	buffer_load_dwordx4 v[232:235], v171, s[12:15], s36 offen
	s_waitcnt lgkmcnt(0)
	v_mfma_f32_32x32x16_bf16 v[66:81], v[14:17], v[198:201], v[66:81]
	v_max3_f32 v249, v249, v111, v112
	v_mfma_f32_16x16x32_bf16 v[240:243], v[2:5], v[132:135], v[240:243]
	v_max3_f32 v173, v173, v127, v128
	v_mfma_f32_16x16x32_bf16 v[240:243], v[6:9], v[132:135], v[240:243]
	v_max_f32 v249, v249, v113
	v_mfma_f32_16x16x32_bf16 v[240:243], v[10:13], v[132:135], v[240:243]
	v_max_f32 v173, v173, v129
	v_mfma_f32_16x16x32_bf16 v[240:243], v[14:17], v[132:135], v[240:243]
	v_max_f32 v173, v173, v249
	s_setprio 0
	s_barrier
; #define ATT_LOAD_K(t) do { const unsigned so_ = (unsigned)(t) * (unsigned)(KVBLK * LDK * 2); sk0 = __builtin_bit_cast(bf16x8, __builtin_amdgcn_raw_buffer_load_b128(krs, koff, so_, 0)); \
;     if constexpr (DQK == 128) sk1 = __builtin_bit_cast(bf16x8, __builtin_amdgcn_raw_buffer_load_b128(krs, koff, so_ + (unsigned)(32 * LDK * 2), 0)); } while (0)
; #define ATT_LOAD_V(t) do { const unsigned so_ = (unsigned)(t) * (unsigned)(KVBLK * LDV * 2); sv0 = __builtin_bit_cast(bf16x8, __builtin_amdgcn_raw_buffer_load_b128(vrs, voff, so_, 0)); \
;     sv1 = __builtin_bit_cast(bf16x8, __builtin_amdgcn_raw_buffer_load_b128(vrs, voff, so_ + (unsigned)(32 * LDV * 2), 0)); } while (0)
; #define ATT_BAR() do { ATT_SBAR(); asm volatile("s_barrier" ::: "memory"); ATT_SBAR(); } while (0)
;     ...
;     if constexpr (!(ABL & 4)) { const int tk = (t + 3 < NT) ? t + 3 : NT - 1, tv = (t + 2 < NT) ? t + 2 : NT - 1; ATT_LOAD_K(tk); ATT_LOAD_V(tv); }
;     ATT_BAR();
;     { const int tk_ = k0; k0 = k1; k1 = k2; k2 = tk_; const int tv_ = v0; v0 = v1; v1 = v2; v2 = tv_; }
	s_add_i32 s36, s36, 0x20000
	s_add_i32 s97, s97, 1
	s_cmpk_eq_i32 s97, 0x7e
	s_cbranch_scc1 .LBB0_290
	s_mov_b32 s14, s94
	s_mov_b32 s94, s18
	s_mov_b32 s18, s96
	s_mov_b32 s15, s95
	s_mov_b32 s95, s93
	s_mov_b32 s93, s37
	s_branch .LBB0_282
.LBB0_285:
	v_mov_b32_e32 v174, v173
	s_nop 1
	v_permlane32_swap_b32_e32 v173, v174
	v_max3_f32 v173, v173, v174, 0
	v_exp_f32_e64 v174, -v173
	s_nop 4
	s_nop 0
	v_cmp_gt_f32_e32 vcc, 1.0, v174
	s_cbranch_vccz .LBB0_289
	s_and_saveexec_b64 s[14:15], s[4:5]
	ds_write_b32 v165, v174
	s_or_b64 exec, exec, s[14:15]
	s_waitcnt lgkmcnt(0)
	v_add_u32_e32 v182, s6, v184
	ds_read_b128 v[174:177], v182 offset:96
	ds_read_b128 v[178:181], v182 offset:64
	ds_read_b128 v[186:189], v182 offset:32
	ds_read_b128 v[190:193], v182
	v_and_b32_e32 v244, 63, v0
	v_lshrrev_b32_e32 v245, 4, v244
	v_and_b32_e32 v244, 1, v244
	v_lshlrev_b32_e32 v244, 6, v244
	v_lshl_add_u32 v244, v245, 4, v244
	v_add_u32_e32 v244, s6, v244
	ds_read_b128 v[244:247], v244
	s_waitcnt lgkmcnt(3)
	v_pk_mul_f32 v[30:31], v[30:31], v[174:175]
	s_waitcnt lgkmcnt(2)
	v_pk_mul_f32 v[26:27], v[26:27], v[178:179]
	s_waitcnt lgkmcnt(1)
	v_pk_mul_f32 v[22:23], v[22:23], v[186:187]
	v_pk_mul_f32 v[32:33], v[32:33], v[176:177]
	v_pk_mul_f32 v[28:29], v[28:29], v[180:181]
	v_pk_mul_f32 v[24:25], v[24:25], v[188:189]
	s_waitcnt lgkmcnt(0)
	v_pk_mul_f32 v[20:21], v[20:21], v[192:193]
	v_pk_mul_f32 v[18:19], v[18:19], v[190:191]
	v_pk_mul_f32 v[46:47], v[46:47], v[174:175]
	v_pk_mul_f32 v[42:43], v[42:43], v[178:179]
	v_pk_mul_f32 v[38:39], v[38:39], v[186:187]
	v_pk_mul_f32 v[48:49], v[48:49], v[176:177]
	v_pk_mul_f32 v[44:45], v[44:45], v[180:181]
	v_pk_mul_f32 v[40:41], v[40:41], v[188:189]
	v_pk_mul_f32 v[36:37], v[36:37], v[192:193]
	v_pk_mul_f32 v[34:35], v[34:35], v[190:191]
	v_pk_mul_f32 v[62:63], v[62:63], v[174:175]
	v_pk_mul_f32 v[58:59], v[58:59], v[178:179]
	v_pk_mul_f32 v[54:55], v[54:55], v[186:187]
	v_pk_mul_f32 v[64:65], v[64:65], v[176:177]
	v_pk_mul_f32 v[60:61], v[60:61], v[180:181]
	v_pk_mul_f32 v[56:57], v[56:57], v[188:189]
	v_pk_mul_f32 v[52:53], v[52:53], v[192:193]
	v_pk_mul_f32 v[50:51], v[50:51], v[190:191]
	v_pk_mul_f32 v[78:79], v[78:79], v[174:175]
	v_pk_mul_f32 v[74:75], v[74:75], v[178:179]
	v_pk_mul_f32 v[70:71], v[70:71], v[186:187]
	v_pk_mul_f32 v[80:81], v[80:81], v[176:177]
	v_pk_mul_f32 v[76:77], v[76:77], v[180:181]
	v_pk_mul_f32 v[72:73], v[72:73], v[188:189]
	v_pk_mul_f32 v[68:69], v[68:69], v[192:193]
	v_pk_mul_f32 v[66:67], v[66:67], v[190:191]
	s_waitcnt lgkmcnt(0)
	v_pk_mul_f32 v[240:241], v[240:241], v[244:245]
	v_pk_mul_f32 v[242:243], v[242:243], v[246:247]

; #define ATT_SBAR() __builtin_amdgcn_sched_barrier(0)
; __device__ __forceinline__ unsigned cvtpk(float lo, float hi) { f32x2_t v = {lo, hi}; bf16x2_t b = __builtin_convertvector(v, bf16x2_t); return __builtin_bit_cast(unsigned, b); }
; #define ATT_LOAD_K(t) do { const unsigned so_ = (unsigned)(t) * (unsigned)(KVBLK * LDK * 2); sk0 = __builtin_bit_cast(bf16x8, __builtin_amdgcn_raw_buffer_load_b128(krs, koff, so_, 0)); \
;     if constexpr (DQK == 128) sk1 = __builtin_bit_cast(bf16x8, __builtin_amdgcn_raw_buffer_load_b128(krs, koff, so_ + (unsigned)(32 * LDK * 2), 0)); } while (0)
; #define ATT_LOAD_V(t) do { const unsigned so_ = (unsigned)(t) * (unsigned)(KVBLK * LDV * 2); sv0 = __builtin_bit_cast(bf16x8, __builtin_amdgcn_raw_buffer_load_b128(vrs, voff, so_, 0)); \
;     sv1 = __builtin_bit_cast(bf16x8, __builtin_amdgcn_raw_buffer_load_b128(vrs, voff, so_ + (unsigned)(32 * LDV * 2), 0)); } while (0)
; #define ATT_WRITE_K(so) do { *(bf16x8*)(K_lds + (so) + kswz<DQK>(kr, kc * 2)) = sk0; if constexpr (DQK == 128) *(bf16x8*)(K_lds + (so) + kswz<DQK>(32 + kr, kc * 2)) = sk1; } while (0)
;     ...
;   for (int t = 0; t + 1 < NT; ++t) {
;     if constexpr (ABL & 1) { u32x4 w0 = {cvtpk(p0[0], p0[1]), cvtpk(p0[2], p0[3]), cvtpk(p0[4], p0[5]), cvtpk(p0[6], p0[7])}, w1 = {cvtpk(p0[8], p0[9]), cvtpk(p0[10], p0[11]), cvtpk(p0[12], p0[13]), cvtpk(p0[14], p0[15])};
;         u32x4 w2 = {cvtpk(p1[0], p1[1]), cvtpk(p1[2], p1[3]), cvtpk(p1[4], p1[5]), cvtpk(p1[6], p1[7])}, w3 = {cvtpk(p1[8], p1[9]), cvtpk(p1[10], p1[11]), cvtpk(p1[12], p1[13]), cvtpk(p1[14], p1[15])};
;         pa0 = *reinterpret_cast<bf16x8*>(&w0); pa1 = *reinterpret_cast<bf16x8*>(&w1); pa2 = *reinterpret_cast<bf16x8*>(&w2); pa3 = *reinterpret_cast<bf16x8*>(&w3); }
;     else { ATT_SOFTMAX(t == 0); }
;     if constexpr (!(ABL & 4)) { ATT_WRITE_K(k2); ATT_WRITE_V(v1); }
;     ATT_SBAR();
; #pragma unroll
;     for (int ks = 0; ks < 4; ++ks) ATT_VPAIR(va, v0, 0, ks);
;     asm volatile("s_waitcnt lgkmcnt(8)" ::: "memory"); ATT_BAR();
;     ATT_XSECTION(true);
;     if constexpr (!(ABL & 4)) { const int tk = (t + 3 < NT) ? t + 3 : NT - 1, tv = (t + 2 < NT) ? t + 2 : NT - 1; ATT_LOAD_K(tk); ATT_LOAD_V(tv); }
;     ATT_BAR();
;     { const int tk_ = k0; k0 = k1; k1 = k2; k2 = tk_; const int tv_ = v0; v0 = v1; v1 = v2; v2 = tv_; }
;   }
;   ATT_SOFTMAX(false);
.LBB0_291:
	v_exp_f32_e32 v98, v98
	v_exp_f32_e32 v114, v114
	v_exp_f32_e32 v99, v99
	v_exp_f32_e32 v115, v115
	v_exp_f32_e32 v100, v100
	v_exp_f32_e32 v101, v101
	v_exp_f32_e32 v102, v102
	v_exp_f32_e32 v103, v103
	v_exp_f32_e32 v106, v106
	v_exp_f32_e32 v107, v107
	v_exp_f32_e32 v116, v116
	v_exp_f32_e32 v117, v117
	v_exp_f32_e32 v118, v118
	v_exp_f32_e32 v119, v119
	v_exp_f32_e32 v104, v104
	v_exp_f32_e32 v120, v120
	v_exp_f32_e32 v105, v105
	v_exp_f32_e32 v121, v121
	v_exp_f32_e32 v122, v122
	v_exp_f32_e32 v123, v123
	v_exp_f32_e32 v108, v108
	v_exp_f32_e32 v124, v124
	v_exp_f32_e32 v109, v109
	v_exp_f32_e32 v125, v125
	v_exp_f32_e32 v110, v110
	v_exp_f32_e32 v126, v126
	v_exp_f32_e32 v111, v111
	v_exp_f32_e32 v127, v127
	v_exp_f32_e32 v112, v112
	v_exp_f32_e32 v128, v128
	v_exp_f32_e32 v113, v113
	v_exp_f32_e32 v129, v129
	v_cvt_pk_bf16_f32 v98, v98, v99
	v_cvt_pk_bf16_f32 v99, v100, v101
	v_cvt_pk_bf16_f32 v100, v102, v103
	v_cvt_pk_bf16_f32 v102, v106, v107
	v_cvt_pk_bf16_f32 v106, v114, v115
	v_add_u32_e32 v114, s18, v169
	s_add_i32 s9, s93, 0
	s_waitcnt vmcnt(2)
	ds_write_b128 v114, v[224:227] offset:49152
	v_add_u32_e32 v114, s9, v167
	v_cvt_pk_bf16_f32 v101, v104, v105
	v_cvt_pk_bf16_f32 v103, v108, v109
	v_cvt_pk_bf16_f32 v104, v110, v111
	v_cvt_pk_bf16_f32 v105, v112, v113
	v_cvt_pk_bf16_f32 v107, v116, v117
	v_cvt_pk_bf16_f32 v108, v118, v119
	v_cvt_pk_bf16_f32 v109, v120, v121
	v_cvt_pk_bf16_f32 v110, v122, v123
	v_cvt_pk_bf16_f32 v111, v124, v125
	v_cvt_pk_bf16_f32 v112, v126, v127
	v_cvt_pk_bf16_f32 v113, v128, v129
	s_waitcnt vmcnt(1)
	ds_write_b128 v114, v[228:231]
	v_add_u32_e32 v114, s9, v168
	s_waitcnt vmcnt(0)
	ds_write_b128 v114, v[232:235]
	v_add_u32_e32 v156, s95, v131
	ds_read_b64_tr_b16 v[114:115], v156
	ds_read_b64_tr_b16 v[116:117], v156 offset:2048
	ds_read_b64_tr_b16 v[118:119], v156 offset:4096
	ds_read_b64_tr_b16 v[120:121], v156 offset:6144
	ds_read_b64_tr_b16 v[122:123], v156 offset:8192
	ds_read_b64_tr_b16 v[124:125], v156 offset:10240
	ds_read_b64_tr_b16 v[126:127], v156 offset:12288
	ds_read_b64_tr_b16 v[128:129], v156 offset:14336
	s_waitcnt lgkmcnt(8)
	s_barrier
	s_setprio 2
	s_waitcnt lgkmcnt(6)
	v_mfma_f32_32x32x16_bf16 v[18:33], v[98:101], v[114:117], v[18:33]
	ds_read_b64_tr_b16 v[152:153], v156 offset:512
	ds_read_b64_tr_b16 v[154:155], v156 offset:2560
	s_waitcnt lgkmcnt(6)
	v_mfma_f32_32x32x16_bf16 v[18:33], v[102:105], v[118:121], v[18:33]
	ds_read_b64_tr_b16 v[114:115], v156 offset:4608
	ds_read_b64_tr_b16 v[116:117], v156 offset:6656
	s_waitcnt lgkmcnt(6)
	v_mfma_f32_32x32x16_bf16 v[18:33], v[106:109], v[122:125], v[18:33]
	ds_read_b64_tr_b16 v[118:119], v156 offset:8704
	ds_read_b64_tr_b16 v[120:121], v156 offset:10752
	s_waitcnt lgkmcnt(6)
	v_mfma_f32_32x32x16_bf16 v[18:33], v[110:113], v[126:129], v[18:33]
	ds_read_b64_tr_b16 v[122:123], v156 offset:12800
	ds_read_b64_tr_b16 v[124:125], v156 offset:14848
	s_waitcnt lgkmcnt(6)
	v_mfma_f32_32x32x16_bf16 v[34:49], v[98:101], v[152:155], v[34:49]
	ds_read_b64_tr_b16 v[126:127], v156 offset:1024
	ds_read_b64_tr_b16 v[128:129], v156 offset:3072
	s_waitcnt lgkmcnt(6)
	v_mfma_f32_32x32x16_bf16 v[34:49], v[102:105], v[114:117], v[34:49]
	ds_read_b64_tr_b16 v[152:153], v156 offset:5120
	ds_read_b64_tr_b16 v[154:155], v156 offset:7168
	s_waitcnt lgkmcnt(6)
	v_mfma_f32_32x32x16_bf16 v[34:49], v[106:109], v[118:121], v[34:49]
	ds_read_b64_tr_b16 v[114:115], v156 offset:9216
	ds_read_b64_tr_b16 v[116:117], v156 offset:11264
	s_waitcnt lgkmcnt(6)
	v_mfma_f32_32x32x16_bf16 v[34:49], v[110:113], v[122:125], v[34:49]
	ds_read_b64_tr_b16 v[118:119], v156 offset:13312
	ds_read_b64_tr_b16 v[120:121], v156 offset:15360
	s_waitcnt lgkmcnt(6)
	v_mfma_f32_32x32x16_bf16 v[50:65], v[98:101], v[126:129], v[50:65]
	ds_read_b64_tr_b16 v[122:123], v156 offset:1536
	ds_read_b64_tr_b16 v[124:125], v156 offset:3584
	s_waitcnt lgkmcnt(6)
	v_mfma_f32_32x32x16_bf16 v[50:65], v[102:105], v[152:155], v[50:65]
	ds_read_b64_tr_b16 v[126:127], v156 offset:5632
	ds_read_b64_tr_b16 v[128:129], v156 offset:7680
	s_waitcnt lgkmcnt(6)
	v_mfma_f32_32x32x16_bf16 v[50:65], v[106:109], v[114:117], v[50:65]
	ds_read_b64_tr_b16 v[152:153], v156 offset:9728
	ds_read_b64_tr_b16 v[154:155], v156 offset:11776
	s_waitcnt lgkmcnt(6)
	v_mfma_f32_32x32x16_bf16 v[50:65], v[110:113], v[118:121], v[50:65]
	ds_read_b64_tr_b16 v[114:115], v156 offset:13824
	ds_read_b64_tr_b16 v[116:117], v156 offset:15872
	s_waitcnt lgkmcnt(6)
	v_mfma_f32_32x32x16_bf16 v[66:81], v[98:101], v[122:125], v[66:81]
	v_add3_u32 v166, v166, s94, v184
	ds_read_b128 v[118:121], v166 offset:49152
	s_waitcnt lgkmcnt(5)
	v_mfma_f32_32x32x16_bf16 v[66:81], v[102:105], v[126:129], v[66:81]
	ds_read_b128 v[122:125], v166 offset:53760
	s_waitcnt lgkmcnt(4)
	v_mfma_f32_32x32x16_bf16 v[66:81], v[106:109], v[152:155], v[66:81]
	ds_read_b128 v[126:129], v166 offset:49184
	s_waitcnt lgkmcnt(3)
	v_mfma_f32_32x32x16_bf16 v[66:81], v[110:113], v[114:117], v[66:81]
	ds_read_b128 v[152:155], v166 offset:53792
	v_mfma_f32_16x16x32_bf16 v[240:243], v[98:101], v[132:135], v[240:243]
	ds_read_b128 v[114:117], v166 offset:49216
	v_mfma_f32_16x16x32_bf16 v[240:243], v[102:105], v[132:135], v[240:243]
	ds_read_b128 v[156:159], v166 offset:53824
	v_mfma_f32_16x16x32_bf16 v[240:243], v[106:109], v[132:135], v[240:243]
	ds_read_b128 v[160:163], v166 offset:49248
	v_mfma_f32_16x16x32_bf16 v[240:243], v[110:113], v[132:135], v[240:243]
	ds_read_b128 v[166:169], v166 offset:53856
	s_waitcnt lgkmcnt(7)
	v_mfma_f32_32x32x16_bf16 v[98:113], v[118:121], v[136:139], v[82:97]
	s_waitcnt lgkmcnt(6)
	v_mfma_f32_32x32x16_bf16 v[82:97], v[122:125], v[136:139], v[82:97]
	s_waitcnt lgkmcnt(5)
	v_mfma_f32_32x32x16_bf16 v[98:113], v[126:129], v[140:143], v[98:113]
	s_waitcnt lgkmcnt(4)
	v_mfma_f32_32x32x16_bf16 v[82:97], v[152:155], v[140:143], v[82:97]
	s_waitcnt lgkmcnt(3)
	v_mfma_f32_32x32x16_bf16 v[98:113], v[114:117], v[144:147], v[98:113]
	s_waitcnt lgkmcnt(2)
	v_mfma_f32_32x32x16_bf16 v[82:97], v[156:159], v[144:147], v[82:97]
	s_waitcnt lgkmcnt(1)
	v_mfma_f32_32x32x16_bf16 v[98:113], v[160:163], v[148:151], v[98:113]
	s_waitcnt lgkmcnt(0)
	v_mfma_f32_32x32x16_bf16 v[82:97], v[166:169], v[148:151], v[82:97]
	s_setprio 0
	s_barrier
	s_nop 10
	v_add_f32_e32 v114, 0, v82
	v_max3_f32 v115, v114, v98, v99
	v_max3_f32 v115, v115, v100, v101
	v_max3_f32 v115, v115, v102, v103
	v_max3_f32 v115, v115, v104, v105
	v_max3_f32 v115, v115, v106, v107
	v_max3_f32 v115, v115, v108, v109
	v_max3_f32 v115, v115, v110, v111
	v_max3_f32 v115, v115, v112, v113
	s_nop 0
	v_max3_f32 v114, v115, v83, v84
	v_max3_f32 v114, v114, v85, v86
	v_max3_f32 v114, v114, v87, v88
	v_max3_f32 v114, v114, v89, v90
	v_max3_f32 v114, v114, v91, v92
	v_max3_f32 v114, v114, v93, v94
	v_max3_f32 v114, v114, v95, v96
	v_max_f32 v114, v114, v97
	s_nop 0
	v_cmp_ge_f32_e32 vcc, s60, v114
	s_cmp_lg_u64 vcc, exec
	s_cbranch_scc1 .LBB0_324
; #define ATT_BAR() do { ATT_SBAR(); asm volatile("s_barrier" ::: "memory"); ATT_SBAR(); } while (0)
; #define ATT_SOFTMAX(first_) do { const float pm_ = softmax_rowmax(p0, p1); \
;     if (__builtin_expect((first_) || !__all(pm_ <= THRL), 0)) { const float al_ = softmax_shift(p0, p1, negm, pm_, (first_)); ATT_RESC(al_); } \
;     softmax_exp_pack(p0, p1, pa0, pa1, pa2, pa3); } while (0)
; #define ATT_VPAIR(buf, so, blk, ks) do { if constexpr (!(ABL & 8) && !(ABL & 32)) { buf[2 * (ks)] = vtr(vq0 + (so) + v_rd_off(blk, ks, 0)); buf[2 * (ks) + 1] = vtr(vq0 + (so) + v_rd_off(blk, ks, 1)); } } while (0)
;     ...
;   ATT_SOFTMAX(false);
; #pragma unroll
;   for (int ks = 0; ks < 4; ++ks) ATT_VPAIR(va, v0, 0, ks);
;   asm volatile("s_waitcnt lgkmcnt(0)" ::: "memory"); ATT_BAR();
;   ATT_XSECTION(false);
;   ATT_BAR();
;   if (grp == 0) ATT_BAR();
.LBB0_292:
	v_exp_f32_e32 v98, v98
	v_exp_f32_e32 v114, v82
	v_exp_f32_e32 v82, v99
	v_exp_f32_e32 v99, v83
	v_exp_f32_e32 v83, v100
	v_exp_f32_e32 v100, v84
	v_exp_f32_e32 v84, v101
	v_exp_f32_e32 v101, v85
	v_exp_f32_e32 v85, v102
	v_exp_f32_e32 v102, v86
	v_exp_f32_e32 v86, v103
	v_exp_f32_e32 v103, v87
	v_exp_f32_e32 v87, v104
	v_exp_f32_e32 v104, v88
	v_exp_f32_e32 v88, v105
	v_exp_f32_e32 v105, v89
	v_exp_f32_e32 v89, v106
	v_exp_f32_e32 v106, v90
	v_exp_f32_e32 v90, v107
	v_exp_f32_e32 v107, v91
	v_exp_f32_e32 v91, v108
	v_exp_f32_e32 v108, v92
	v_exp_f32_e32 v92, v109
	v_exp_f32_e32 v109, v93
	v_exp_f32_e32 v93, v110
	v_exp_f32_e32 v110, v94
	v_exp_f32_e32 v94, v111
	v_exp_f32_e32 v111, v95
	v_exp_f32_e32 v95, v112
	v_exp_f32_e32 v112, v96
	v_exp_f32_e32 v96, v113
	v_exp_f32_e32 v97, v97
	v_add_u32_e32 v118, s93, v131
	v_cvt_pk_bf16_f32 v82, v98, v82
	v_cvt_pk_bf16_f32 v83, v83, v84
	v_cvt_pk_bf16_f32 v84, v85, v86
	v_cvt_pk_bf16_f32 v85, v87, v88
	v_cvt_pk_bf16_f32 v86, v89, v90
	v_cvt_pk_bf16_f32 v87, v91, v92
	v_cvt_pk_bf16_f32 v88, v93, v94
	v_cvt_pk_bf16_f32 v89, v95, v96
	v_cvt_pk_bf16_f32 v90, v114, v99
	v_cvt_pk_bf16_f32 v91, v100, v101
	v_cvt_pk_bf16_f32 v92, v102, v103
	v_cvt_pk_bf16_f32 v93, v104, v105
	v_cvt_pk_bf16_f32 v94, v106, v107
	v_cvt_pk_bf16_f32 v95, v108, v109
	v_cvt_pk_bf16_f32 v96, v110, v111
	v_cvt_pk_bf16_f32 v97, v112, v97
	ds_read_b64_tr_b16 v[98:99], v118
	ds_read_b64_tr_b16 v[100:101], v118 offset:2048
	ds_read_b64_tr_b16 v[102:103], v118 offset:4096
	ds_read_b64_tr_b16 v[104:105], v118 offset:6144
	ds_read_b64_tr_b16 v[106:107], v118 offset:8192
	ds_read_b64_tr_b16 v[108:109], v118 offset:10240
	ds_read_b64_tr_b16 v[110:111], v118 offset:12288
	ds_read_b64_tr_b16 v[112:113], v118 offset:14336
	s_waitcnt lgkmcnt(0)
	s_barrier
	s_setprio 2
	s_waitcnt lgkmcnt(6)
	v_mfma_f32_32x32x16_bf16 v[18:33], v[82:85], v[98:101], v[18:33]
	ds_read_b64_tr_b16 v[114:115], v118 offset:512
	ds_read_b64_tr_b16 v[116:117], v118 offset:2560
	s_waitcnt lgkmcnt(6)
	v_mfma_f32_32x32x16_bf16 v[18:33], v[86:89], v[102:105], v[18:33]
	ds_read_b64_tr_b16 v[98:99], v118 offset:4608
	ds_read_b64_tr_b16 v[100:101], v118 offset:6656
	s_waitcnt lgkmcnt(6)
	v_mfma_f32_32x32x16_bf16 v[18:33], v[90:93], v[106:109], v[18:33]
	ds_read_b64_tr_b16 v[102:103], v118 offset:8704
	ds_read_b64_tr_b16 v[104:105], v118 offset:10752
	s_waitcnt lgkmcnt(6)
	v_mfma_f32_32x32x16_bf16 v[18:33], v[94:97], v[110:113], v[18:33]
	ds_read_b64_tr_b16 v[106:107], v118 offset:12800
	ds_read_b64_tr_b16 v[108:109], v118 offset:14848
	s_waitcnt lgkmcnt(6)
	v_mfma_f32_32x32x16_bf16 v[34:49], v[82:85], v[114:117], v[34:49]
	ds_read_b64_tr_b16 v[110:111], v118 offset:1024
	ds_read_b64_tr_b16 v[112:113], v118 offset:3072
	s_waitcnt lgkmcnt(6)
	v_mfma_f32_32x32x16_bf16 v[34:49], v[86:89], v[98:101], v[34:49]
	ds_read_b64_tr_b16 v[114:115], v118 offset:5120
	ds_read_b64_tr_b16 v[116:117], v118 offset:7168
	s_waitcnt lgkmcnt(6)
	v_mfma_f32_32x32x16_bf16 v[34:49], v[90:93], v[102:105], v[34:49]
	ds_read_b64_tr_b16 v[98:99], v118 offset:9216
	ds_read_b64_tr_b16 v[100:101], v118 offset:11264
	s_waitcnt lgkmcnt(6)
	v_mfma_f32_32x32x16_bf16 v[34:49], v[94:97], v[106:109], v[34:49]
	ds_read_b64_tr_b16 v[102:103], v118 offset:13312
	ds_read_b64_tr_b16 v[104:105], v118 offset:15360
	s_waitcnt lgkmcnt(6)
	v_mfma_f32_32x32x16_bf16 v[50:65], v[82:85], v[110:113], v[50:65]
	ds_read_b64_tr_b16 v[106:107], v118 offset:1536
	ds_read_b64_tr_b16 v[108:109], v118 offset:3584
	s_waitcnt lgkmcnt(6)
	v_mfma_f32_32x32x16_bf16 v[50:65], v[86:89], v[114:117], v[50:65]
	ds_read_b64_tr_b16 v[110:111], v118 offset:5632
	ds_read_b64_tr_b16 v[112:113], v118 offset:7680
	s_waitcnt lgkmcnt(6)
	v_mfma_f32_32x32x16_bf16 v[50:65], v[90:93], v[98:101], v[50:65]
	ds_read_b64_tr_b16 v[114:115], v118 offset:9728
	ds_read_b64_tr_b16 v[116:117], v118 offset:11776
	s_waitcnt lgkmcnt(6)
	v_mfma_f32_32x32x16_bf16 v[50:65], v[94:97], v[102:105], v[50:65]
	ds_read_b64_tr_b16 v[98:99], v118 offset:13824
	ds_read_b64_tr_b16 v[100:101], v118 offset:15872
	s_waitcnt lgkmcnt(6)
	v_mfma_f32_32x32x16_bf16 v[66:81], v[82:85], v[106:109], v[66:81]
	s_waitcnt lgkmcnt(4)
	v_mfma_f32_32x32x16_bf16 v[66:81], v[86:89], v[110:113], v[66:81]
	s_waitcnt lgkmcnt(2)
	v_mfma_f32_32x32x16_bf16 v[66:81], v[90:93], v[114:117], v[66:81]
	s_waitcnt lgkmcnt(0)
	v_mfma_f32_32x32x16_bf16 v[66:81], v[94:97], v[98:101], v[66:81]
	v_mfma_f32_16x16x32_bf16 v[240:243], v[82:85], v[132:135], v[240:243]
	v_mfma_f32_16x16x32_bf16 v[240:243], v[86:89], v[132:135], v[240:243]
	v_mfma_f32_16x16x32_bf16 v[240:243], v[90:93], v[132:135], v[240:243]
	v_mfma_f32_16x16x32_bf16 v[240:243], v[94:97], v[132:135], v[240:243]
	s_setprio 0
	s_barrier
	s_cmpk_gt_u32 s89, 0xff
	s_cbranch_scc1 .LBB0_294
	s_barrier
; __device__ __forceinline__ unsigned cvtpk(float lo, float hi) { f32x2_t v = {lo, hi}; bf16x2_t b = __builtin_convertvector(v, bf16x2_t); return __builtin_bit_cast(unsigned, b); }
;     ...
;   if constexpr (DQK == 64) {
;     const unsigned koff_e = (unsigned)((tid >> 3) * LDK + (tid & 7) * 8) * 2u, voff_e = (unsigned)((tid >> 4) * LDV + (tid & 15) * 8) * 2u;
;     const __amdgpu_buffer_rsrc_t krs_e = __builtin_amdgcn_make_buffer_rsrc((void*)Kh, 0, 0x7fffffff, 0x00020000), vrs_e = __builtin_amdgcn_make_buffer_rsrc((void*)Vh, 0, 0x7fffffff, 0x00020000);
;     ek0 = __builtin_bit_cast(bf16x8, __builtin_amdgcn_raw_buffer_load_b128(krs_e, koff_e, 0, 0));
;     ev0 = __builtin_bit_cast(bf16x8, __builtin_amdgcn_raw_buffer_load_b128(vrs_e, voff_e, 0, 0));
;     ev1 = __builtin_bit_cast(bf16x8, __builtin_amdgcn_raw_buffer_load_b128(vrs_e, voff_e, (unsigned)(32 * LDV * 2), 0));
;     ek1 = __builtin_bit_cast(bf16x8, __builtin_amdgcn_raw_buffer_load_b128(krs_e, koff_e, (unsigned)(KVBLK * LDK * 2), 0));
;   }
;   bf16x8 qr[DQK / 16];
;   const bf16* Qw = Qb + (long)(wid * QBLK + r32) * LDQ + hi * 8;
; #pragma unroll
;   for (int d0 = 0; d0 < DQK / 16; ++d0) qr[d0] = *reinterpret_cast<const bf16x8*>(Qw + d0 * 16);
;     ...
; #pragma unroll
;     for (int d0 = 0; d0 < 4; ++d0)
; #pragma unroll
;         for (int r = 0; r < 16; r += 2) stash[(d0 * 8 + (r >> 1)) * 64 + lane_] = att::cvtpk(o[d0][r] * rli[r], o[d0][r + 1] * rli[r + 1]);
;     attn_pass<64, 1024, 1024, 1024, ABL>(Qb + 64, Kh + 64, Vh, SEQ, lds, wsf, o, rli, (const float*)(ws + WS_ROPE), nullptr, qb * 256);
.LBB0_294:
	s_nop 7
	s_nop 1
	v_and_b32_e32 v244, 63, v0
	v_lshrrev_b32_e32 v245, 4, v244
	v_and_b32_e32 v244, 1, v244
	v_lshlrev_b32_e32 v244, 6, v244
	v_lshl_add_u32 v244, v245, 4, v244
	v_add_u32_e32 v244, s6, v244
	ds_write_b128 v244, v[240:243]
	v_add_u32_e32 v245, s6, v184
	s_waitcnt lgkmcnt(0)
	ds_read_b128 v[2:5], v245
	ds_read_b128 v[6:9], v245 offset:32
	ds_read_b128 v[10:13], v245 offset:64
	ds_read_b128 v[14:17], v245 offset:96
	s_waitcnt lgkmcnt(0)
	s_nop 8
	v_rcp_f32_e32 v2, v2
	v_rcp_f32_e32 v3, v3
	v_rcp_f32_e32 v4, v4
	v_rcp_f32_e32 v5, v5
	s_ashr_i32 s89, s92, 6
	s_lshl_b32 s4, s89, 13
	v_rcp_f32_e32 v6, v6
	v_rcp_f32_e32 v7, v7
	v_and_b32_e32 v82, 63, v164
	s_add_i32 s4, s4, 0
	v_rcp_f32_e32 v8, v8
	v_rcp_f32_e32 v9, v9
	v_pk_mul_f32 v[18:19], v[18:19], v[2:3]
	v_lshl_add_u32 v82, v82, 2, s4
	v_cvt_pk_bf16_f32 v83, v18, v19
	v_pk_mul_f32 v[18:19], v[20:21], v[4:5]
	v_rcp_f32_e32 v10, v10
	v_rcp_f32_e32 v11, v11
	v_add_u32_e32 v165, 0x12c00, v82
	v_cvt_pk_bf16_f32 v18, v18, v19
	v_rcp_f32_e32 v12, v12
	v_rcp_f32_e32 v13, v13
	ds_write2st64_b32 v165, v83, v18 offset1:1
	v_pk_mul_f32 v[18:19], v[22:23], v[6:7]
	v_rcp_f32_e32 v14, v14
	v_cvt_pk_bf16_f32 v20, v18, v19
	v_pk_mul_f32 v[18:19], v[24:25], v[8:9]
	v_rcp_f32_e32 v15, v15
	v_cvt_pk_bf16_f32 v18, v18, v19
	v_rcp_f32_e32 v16, v16
	v_rcp_f32_e32 v17, v17
	ds_write2st64_b32 v165, v20, v18 offset0:2 offset1:3
	v_pk_mul_f32 v[18:19], v[26:27], v[10:11]
	s_add_u32 s8, s8, 0x80
	v_cvt_pk_bf16_f32 v20, v18, v19
	v_pk_mul_f32 v[18:19], v[28:29], v[12:13]
	s_addc_u32 s4, s91, 0
	v_cvt_pk_bf16_f32 v18, v18, v19
	ds_write2st64_b32 v165, v20, v18 offset0:4 offset1:5
	v_pk_mul_f32 v[18:19], v[30:31], v[14:15]
	s_mov_b32 s14, s10
	v_cvt_pk_bf16_f32 v20, v18, v19
	v_pk_mul_f32 v[18:19], v[32:33], v[16:17]
	s_mov_b32 s15, s11
	v_cvt_pk_bf16_f32 v18, v18, v19
	ds_write2st64_b32 v165, v20, v18 offset0:6 offset1:7
	v_pk_mul_f32 v[18:19], v[34:35], v[2:3]
	v_mov_b32_e32 v132, v130
	v_cvt_pk_bf16_f32 v20, v18, v19
	v_pk_mul_f32 v[18:19], v[36:37], v[4:5]
	v_mov_b32_e32 v133, v130
	v_cvt_pk_bf16_f32 v18, v18, v19
	ds_write2st64_b32 v165, v20, v18 offset0:8 offset1:9
	v_pk_mul_f32 v[18:19], v[38:39], v[6:7]
	v_mov_b32_e32 v131, v130
	v_cvt_pk_bf16_f32 v20, v18, v19
	v_pk_mul_f32 v[18:19], v[40:41], v[8:9]
	v_mov_b64_e32 v[134:135], v[132:133]
	v_cvt_pk_bf16_f32 v18, v18, v19
	ds_write2st64_b32 v165, v20, v18 offset0:10 offset1:11
	v_pk_mul_f32 v[18:19], v[42:43], v[10:11]
	v_mov_b64_e32 v[132:133], v[130:131]
	v_cvt_pk_bf16_f32 v20, v18, v19
	v_pk_mul_f32 v[18:19], v[44:45], v[12:13]
	s_nop 0
	v_cvt_pk_bf16_f32 v18, v18, v19
	ds_write2st64_b32 v165, v20, v18 offset0:12 offset1:13
	v_pk_mul_f32 v[18:19], v[46:47], v[14:15]
	s_nop 0
	v_cvt_pk_bf16_f32 v20, v18, v19
	v_pk_mul_f32 v[18:19], v[48:49], v[16:17]
	s_nop 0
	v_cvt_pk_bf16_f32 v18, v18, v19
	ds_write2st64_b32 v165, v20, v18 offset0:14 offset1:15
	v_pk_mul_f32 v[18:19], v[50:51], v[2:3]
	v_pk_mul_f32 v[2:3], v[66:67], v[2:3]
	v_cvt_pk_bf16_f32 v20, v18, v19
	v_pk_mul_f32 v[18:19], v[52:53], v[4:5]
	s_nop 0
	v_cvt_pk_bf16_f32 v18, v18, v19
	ds_write2st64_b32 v165, v20, v18 offset0:16 offset1:17
	v_pk_mul_f32 v[18:19], v[54:55], v[6:7]
	s_nop 0
	v_cvt_pk_bf16_f32 v20, v18, v19
	v_pk_mul_f32 v[18:19], v[56:57], v[8:9]
	s_nop 0
	v_cvt_pk_bf16_f32 v18, v18, v19
	ds_write2st64_b32 v165, v20, v18 offset0:18 offset1:19
	v_pk_mul_f32 v[18:19], v[58:59], v[10:11]
	s_nop 0
	v_cvt_pk_bf16_f32 v20, v18, v19
	v_pk_mul_f32 v[18:19], v[60:61], v[12:13]
	s_nop 0
	v_cvt_pk_bf16_f32 v18, v18, v19
	ds_write2st64_b32 v165, v20, v18 offset0:20 offset1:21
	v_pk_mul_f32 v[18:19], v[62:63], v[14:15]
	v_mov_b32_e32 v63, v0
	v_cvt_pk_bf16_f32 v20, v18, v19
	v_pk_mul_f32 v[18:19], v[64:65], v[16:17]
	s_nop 0
	v_cvt_pk_bf16_f32 v18, v18, v19
	ds_write2st64_b32 v165, v20, v18 offset0:22 offset1:23
	v_cvt_pk_bf16_f32 v18, v2, v3
	v_pk_mul_f32 v[2:3], v[68:69], v[4:5]
	v_mov_b32_e32 v5, v185
	v_cvt_pk_bf16_f32 v2, v2, v3
	ds_write2st64_b32 v165, v18, v2 offset0:24 offset1:25
	v_pk_mul_f32 v[2:3], v[70:71], v[6:7]
	s_nop 0
	v_cvt_pk_bf16_f32 v4, v2, v3
	v_pk_mul_f32 v[2:3], v[72:73], v[8:9]
	s_nop 0
	v_cvt_pk_bf16_f32 v2, v2, v3
	ds_write2st64_b32 v165, v4, v2 offset0:26 offset1:27
	v_pk_mul_f32 v[2:3], v[74:75], v[10:11]
	s_nop 0
	v_cvt_pk_bf16_f32 v4, v2, v3
	v_pk_mul_f32 v[2:3], v[76:77], v[12:13]
	s_nop 0
	v_cvt_pk_bf16_f32 v2, v2, v3
	ds_write2st64_b32 v165, v4, v2 offset0:28 offset1:29
	v_pk_mul_f32 v[2:3], v[78:79], v[14:15]
	s_nop 0
	v_cvt_pk_bf16_f32 v4, v2, v3
	v_pk_mul_f32 v[2:3], v[80:81], v[16:17]
	s_nop 0
	v_cvt_pk_bf16_f32 v2, v2, v3
	ds_write2st64_b32 v165, v4, v2 offset0:30 offset1:31
	s_nop 0
	v_readfirstlane_b32 s91, v63
	s_ashr_i32 s5, s91, 1
	v_mov_b32_e32 v2, s5
	v_bfi_b32 v2, s3, v2, v63
	v_ashrrev_i32_e32 v3, 31, v2
	v_bfe_u32 v4, v63, 5, 1
	v_lshlrev_b64 v[2:3], 11, v[2:3]
	v_and_b32_e32 v62, 31, v63
	v_lshl_add_u64 v[2:3], s[50:51], 0, v[2:3]
	v_lshlrev_b32_e32 v184, 4, v4
	s_and_b32 s9, s5, 0xffffffe0
	v_lshl_add_u64 v[54:55], v[2:3], 0, v[184:185]
	v_or_b32_e32 v2, s90, v62
	v_add_u32_e32 v2, s9, v2
	global_load_dwordx4 v[18:21], v[54:55], off offset:128
	v_ashrrev_i32_e32 v3, 31, v2
	v_lshlrev_b64 v[2:3], 8, v[2:3]
	v_and_b32_e32 v4, 32, v63
	v_lshl_add_u64 v[2:3], s[48:49], 0, v[2:3]
	v_lshl_add_u64 v[64:65], v[2:3], 0, v[4:5]
	global_load_dwordx4 v[22:25], v[64:65], off
	global_load_dwordx4 v[26:29], v[64:65], off offset:16
	global_load_dwordx4 v[30:33], v[54:55], off offset:160
	global_load_dwordx4 v[34:37], v[64:65], off offset:64
	global_load_dwordx4 v[38:41], v[64:65], off offset:80
	global_load_dwordx4 v[42:45], v[54:55], off offset:192
	global_load_dwordx4 v[46:49], v[64:65], off offset:144
	global_load_dwordx4 v[50:53], v[64:65], off offset:128
	v_lshlrev_b32_e32 v77, 3, v63
	v_lshlrev_b32_e32 v2, 4, v63
	v_ashrrev_i32_e32 v79, 4, v63
	v_and_b32_e32 v78, 0x70, v2
	v_and_b32_e32 v2, 0x78, v77
	v_lshlrev_b32_e32 v3, 11, v79
	v_ashrrev_i32_e32 v76, 3, v63
	v_lshl_or_b32 v172, v2, 1, v3
	v_lshl_or_b32 v171, v76, 11, v78
	s_and_b32 s9, s4, 0xffff
	buffer_load_dwordx4 v[6:9], v172, s[12:15], 0 offen
	buffer_load_dwordx4 v[2:5], v172, s[12:15], s57 offen
	buffer_load_dwordx4 v[14:17], v171, s[8:11], 0 offen
	buffer_load_dwordx4 v[10:13], v171, s[8:11], s11 offen
	s_nop 0
	global_load_dwordx4 v[54:57], v[54:55], off offset:224
	s_nop 0
	global_load_dwordx4 v[58:61], v[64:65], off offset:208
	s_nop 0
	global_load_dwordx4 v[64:67], v[64:65], off offset:192
	s_waitcnt vmcnt(15)
; __device__ __forceinline__ unsigned cvtpk(float lo, float hi) { f32x2_t v = {lo, hi}; bf16x2_t b = __builtin_convertvector(v, bf16x2_t); return __builtin_bit_cast(unsigned, b); }
; #define ATT_WRITE_V(so) do { *(bf16x8*)(V_lds + (so) + vst0) = sv0; *(bf16x8*)(V_lds + (so) + vst1) = sv1; } while (0)
; template <int DQK> __device__ __forceinline__ void q_prepare(bf16x8 (&qr)[DQK / 16], const float* rope, const float* gain, int s, int hi) {
;     ...
;   if constexpr (DQK == 64) {
; #pragma unroll
;     for (int d0 = 0; d0 < 4; ++d0) {
;       const f32x4q* tp = (const f32x4q*)(rope + ((size_t)s * 32 + 8 * d0 + 4 * hi) * 2);
;       const f32x4q t0 = tp[0], t1 = tp[1];
;       const float cs[4] = {t0.x, t0.z, t1.x, t1.z}, sn[4] = {t0.y, t0.w, t1.y, t1.w};
; #pragma unroll
;       for (int e = 0; e < 4; ++e) { const float x1 = v[d0][e], x2 = v[d0][4 + e]; v[d0][e] = x1 * cs[e] - x2 * sn[e]; v[d0][4 + e] = x2 * cs[e] + x1 * sn[e]; }
;     }
;   } else
; #pragma unroll
;   for (int blk = 0; blk < DQK / 64; ++blk) {
;     const int pos = (DQK == 128) ? (blk == 0 ? (s >> 6) : (s & 63)) : s;
; #pragma unroll
;     for (int dd = 0; dd < 2; ++dd) {
;       const f32x4q* tp = (const f32x4q*)(rope + ((size_t)pos * 32 + 16 * dd + 8 * hi) * 2);
;       const f32x4q t0 = tp[0], t1 = tp[1], t2 = tp[2], t3 = tp[3];
;       const float cs[8] = {t0.x, t0.z, t1.x, t1.z, t2.x, t2.z, t3.x, t3.z}, sn[8] = {t0.y, t0.w, t1.y, t1.w, t2.y, t2.w, t3.y, t3.w};
; #pragma unroll
;       for (int j = 0; j < 8; ++j) { const float x1 = v[4 * blk + dd][j], x2 = v[4 * blk + dd + 2][j];
;         v[4 * blk + dd][j] = x1 * cs[j] - x2 * sn[j]; v[4 * blk + dd + 2][j] = x2 * cs[j] + x1 * sn[j]; }
;     }
;   }
; #pragma unroll
;   for (int d0 = 0; d0 < DQK / 16; ++d0) { u32x4 w = {cvtpk(v[d0][0] * mul, v[d0][1] * mul), cvtpk(v[d0][2] * mul, v[d0][3] * mul), cvtpk(v[d0][4] * mul, v[d0][5] * mul), cvtpk(v[d0][6] * mul, v[d0][7] * mul)};
;     qr[d0] = *reinterpret_cast<bf16x8*>(&w); }
;     ...
;   if constexpr (DQK == 64) { sk0 = ek0; sv0 = ev0; sv1 = ev1; ATT_WRITE_K(0); ATT_WRITE_V(0); sk0 = ek1; ATT_WRITE_K(SHM_K); }
;   else { ATT_LOAD_K(0); ATT_LOAD_V(0); ATT_WRITE_K(0); ATT_WRITE_V(0);
;          ATT_LOAD_K(1); ATT_WRITE_K(SHM_K); }
;   ATT_LOAD_K(2); ATT_LOAD_V(1);
;   asm volatile("s_waitcnt lgkmcnt(0)" ::: "memory"); ATT_BAR();
;   if (grp == 1) ATT_BAR();
	v_lshlrev_b32_e32 v70, 16, v20
	v_and_b32_e32 v71, 0xffff0000, v20
	s_waitcnt vmcnt(14)
	v_mov_b32_e32 v72, v22
	v_mov_b32_e32 v73, v24
	v_lshlrev_b32_e32 v68, 16, v18
	v_and_b32_e32 v69, 0xffff0000, v18
	v_pk_mul_f32 v[74:75], v[72:73], v[70:71]
	v_mov_b32_e32 v24, v23
	v_pk_fma_f32 v[22:23], v[24:25], v[68:69], v[74:75]
	v_pk_mul_f32 v[24:25], v[24:25], v[70:71]
	v_pk_mul_f32 v[22:23], v[22:23], s[40:41] op_sel_hi:[1,0]
	v_pk_fma_f32 v[24:25], v[72:73], v[68:69], v[24:25] neg_lo:[0,0,1] neg_hi:[0,0,1]
	v_cvt_pk_bf16_f32 v138, v22, v23
	v_pk_mul_f32 v[24:25], v[24:25], s[40:41] op_sel_hi:[1,0]
	v_lshlrev_b32_e32 v20, 16, v21
	v_and_b32_e32 v21, 0xffff0000, v21
	s_waitcnt vmcnt(13)
	v_mov_b32_e32 v22, v26
	v_mov_b32_e32 v23, v28
	v_mov_b32_e32 v28, v27
	v_cvt_pk_bf16_f32 v136, v24, v25
	v_lshlrev_b32_e32 v18, 16, v19
	v_and_b32_e32 v19, 0xffff0000, v19
	v_pk_mul_f32 v[24:25], v[22:23], v[20:21]
	v_pk_mul_f32 v[20:21], v[28:29], v[20:21]
	v_pk_fma_f32 v[24:25], v[28:29], v[18:19], v[24:25]
	v_pk_fma_f32 v[18:19], v[22:23], v[18:19], v[20:21] neg_lo:[0,0,1] neg_hi:[0,0,1]
	s_waitcnt vmcnt(12)
	v_lshlrev_b32_e32 v20, 16, v32
	v_pk_mul_f32 v[18:19], v[18:19], s[40:41] op_sel_hi:[1,0]
	v_and_b32_e32 v21, 0xffff0000, v32
	v_cvt_pk_bf16_f32 v137, v18, v19
	v_pk_mul_f32 v[18:19], v[24:25], s[40:41] op_sel_hi:[1,0]
	s_waitcnt vmcnt(11)
	v_mov_b32_e32 v22, v34
	v_mov_b32_e32 v23, v36
	v_mov_b32_e32 v36, v35
	v_cvt_pk_bf16_f32 v139, v18, v19
	v_lshlrev_b32_e32 v18, 16, v30
	v_and_b32_e32 v19, 0xffff0000, v30
	v_pk_mul_f32 v[24:25], v[22:23], v[20:21]
	v_pk_mul_f32 v[20:21], v[36:37], v[20:21]
	v_pk_fma_f32 v[24:25], v[36:37], v[18:19], v[24:25]
	v_pk_fma_f32 v[18:19], v[22:23], v[18:19], v[20:21] neg_lo:[0,0,1] neg_hi:[0,0,1]
	v_lshlrev_b32_e32 v20, 16, v33
	v_pk_mul_f32 v[18:19], v[18:19], s[40:41] op_sel_hi:[1,0]
	v_and_b32_e32 v21, 0xffff0000, v33
	v_cvt_pk_bf16_f32 v140, v18, v19
	v_pk_mul_f32 v[18:19], v[24:25], s[40:41] op_sel_hi:[1,0]
	s_waitcnt vmcnt(10)
	v_mov_b32_e32 v22, v38
	v_mov_b32_e32 v23, v40
	v_mov_b32_e32 v40, v39
	v_cvt_pk_bf16_f32 v142, v18, v19
	v_lshlrev_b32_e32 v18, 16, v31
	v_and_b32_e32 v19, 0xffff0000, v31
	v_pk_mul_f32 v[24:25], v[22:23], v[20:21]
	v_pk_mul_f32 v[20:21], v[40:41], v[20:21]
	v_pk_fma_f32 v[24:25], v[40:41], v[18:19], v[24:25]
	v_pk_fma_f32 v[18:19], v[22:23], v[18:19], v[20:21] neg_lo:[0,0,1] neg_hi:[0,0,1]
	s_waitcnt vmcnt(9)
	v_lshlrev_b32_e32 v20, 16, v44
	v_pk_mul_f32 v[18:19], v[18:19], s[40:41] op_sel_hi:[1,0]
	v_and_b32_e32 v21, 0xffff0000, v44
	v_cvt_pk_bf16_f32 v141, v18, v19
	v_pk_mul_f32 v[18:19], v[24:25], s[40:41] op_sel_hi:[1,0]
	s_waitcnt vmcnt(7)
	v_mov_b32_e32 v22, v50
	v_mov_b32_e32 v23, v52
	v_mov_b32_e32 v52, v51
	v_cvt_pk_bf16_f32 v143, v18, v19
	v_lshlrev_b32_e32 v18, 16, v42
	v_and_b32_e32 v19, 0xffff0000, v42
	v_pk_mul_f32 v[24:25], v[22:23], v[20:21]
	v_pk_mul_f32 v[20:21], v[52:53], v[20:21]
	v_pk_fma_f32 v[24:25], v[52:53], v[18:19], v[24:25]
	v_pk_fma_f32 v[18:19], v[22:23], v[18:19], v[20:21] neg_lo:[0,0,1] neg_hi:[0,0,1]
	v_lshlrev_b32_e32 v20, 16, v45
	v_pk_mul_f32 v[18:19], v[18:19], s[40:41] op_sel_hi:[1,0]
	v_and_b32_e32 v21, 0xffff0000, v45
	v_cvt_pk_bf16_f32 v144, v18, v19
	v_pk_mul_f32 v[18:19], v[24:25], s[40:41] op_sel_hi:[1,0]
	v_mov_b32_e32 v22, v46
	v_mov_b32_e32 v23, v48
	v_mov_b32_e32 v48, v47
	v_cvt_pk_bf16_f32 v146, v18, v19
	v_lshlrev_b32_e32 v18, 16, v43
	v_and_b32_e32 v19, 0xffff0000, v43
	v_pk_mul_f32 v[24:25], v[22:23], v[20:21]
	v_pk_mul_f32 v[20:21], v[48:49], v[20:21]
	v_pk_fma_f32 v[24:25], v[48:49], v[18:19], v[24:25]
	v_pk_fma_f32 v[18:19], v[22:23], v[18:19], v[20:21] neg_lo:[0,0,1] neg_hi:[0,0,1]
	s_waitcnt vmcnt(2)
	v_lshlrev_b32_e32 v20, 16, v56
	v_pk_mul_f32 v[18:19], v[18:19], s[40:41] op_sel_hi:[1,0]
	v_and_b32_e32 v21, 0xffff0000, v56
	v_cvt_pk_bf16_f32 v145, v18, v19
	v_pk_mul_f32 v[18:19], v[24:25], s[40:41] op_sel_hi:[1,0]
	s_waitcnt vmcnt(0)
	v_mov_b32_e32 v22, v64
	v_mov_b32_e32 v23, v66
	v_mov_b32_e32 v66, v65
	v_cvt_pk_bf16_f32 v147, v18, v19
	v_lshlrev_b32_e32 v18, 16, v54
	v_and_b32_e32 v19, 0xffff0000, v54
	v_pk_mul_f32 v[24:25], v[22:23], v[20:21]
	v_pk_mul_f32 v[20:21], v[66:67], v[20:21]
	v_pk_fma_f32 v[24:25], v[66:67], v[18:19], v[24:25]
	v_pk_fma_f32 v[18:19], v[22:23], v[18:19], v[20:21] neg_lo:[0,0,1] neg_hi:[0,0,1]
	v_lshlrev_b32_e32 v20, 16, v57
	v_pk_mul_f32 v[18:19], v[18:19], s[40:41] op_sel_hi:[1,0]
	v_and_b32_e32 v21, 0xffff0000, v57
	v_cvt_pk_bf16_f32 v148, v18, v19
	v_pk_mul_f32 v[18:19], v[24:25], s[40:41] op_sel_hi:[1,0]
	v_mov_b32_e32 v22, v58
	v_mov_b32_e32 v23, v60
	v_mov_b32_e32 v60, v59
	v_cvt_pk_bf16_f32 v150, v18, v19
	v_lshlrev_b32_e32 v18, 16, v55
	v_and_b32_e32 v19, 0xffff0000, v55
	v_pk_mul_f32 v[24:25], v[22:23], v[20:21]
	v_pk_mul_f32 v[20:21], v[60:61], v[20:21]
	v_pk_fma_f32 v[24:25], v[60:61], v[18:19], v[24:25]
	v_pk_fma_f32 v[18:19], v[22:23], v[18:19], v[20:21] neg_lo:[0,0,1] neg_hi:[0,0,1]
	v_mov_b32_e32 v20, v185
	v_pk_mul_f32 v[18:19], v[18:19], s[40:41] op_sel_hi:[1,0]
	v_mov_b32_e32 v21, v185
	v_cvt_pk_bf16_f32 v149, v18, v19
	v_pk_mul_f32 v[18:19], v[24:25], s[40:41] op_sel_hi:[1,0]
	v_mov_b32_e32 v22, v185
	v_cvt_pk_bf16_f32 v151, v18, v19
	v_mov_b32_e32 v18, v185
	v_mov_b32_e32 v19, v185
	v_mov_b32_e32 v23, v185
	v_mov_b32_e32 v24, v185
	v_mov_b32_e32 v25, v185
	v_mov_b32_e32 v26, v185
	v_mov_b32_e32 v27, v185
	v_mov_b32_e32 v28, v185
	v_mov_b32_e32 v29, v185
	v_mov_b32_e32 v30, v185
	v_mov_b32_e32 v31, v185
	v_mov_b32_e32 v32, v185
	v_mov_b32_e32 v33, v185
	buffer_load_dwordx4 v[50:53], v172, s[12:15], s11 offen
	buffer_load_dwordx4 v[58:61], v171, s[8:11], s83 offen
	buffer_load_dwordx4 v[54:57], v172, s[12:15], s84 offen
	v_lshlrev_b32_e32 v36, 5, v79
	v_and_b32_e32 v37, 24, v77
	v_lshrrev_b32_e32 v34, 5, v63
	v_bfe_u32 v35, v77, 5, 2
	v_and_or_b32 v36, v36, s52, v37
	v_and_or_b32 v34, v34, s41, v35
	v_lshlrev_b32_e32 v36, 1, v36
	v_lshl_or_b32 v168, v34, 9, v36
	v_add_u32_e32 v34, 32, v79
	v_lshrrev_b32_e32 v34, 1, v34
	v_and_or_b32 v34, v34, s41, v35
	v_lshl_or_b32 v169, v34, 9, v36
	v_mul_lo_u32 v34, v76, s82
	v_add3_u32 v170, v34, v78, 0
	v_add_u32_e32 v64, 0, v168
	v_add_u32_e32 v65, 0, v169
	ds_write_b128 v170, v[14:17] offset:49152
	ds_write_b128 v64, v[6:9]
	ds_write_b128 v65, v[2:5]
	ds_write_b128 v170, v[10:13] offset:58368
	s_waitcnt lgkmcnt(0)
	s_barrier
	s_and_b32 s4, s91, 0xffffff00
	s_cmpk_lg_i32 s4, 0x100
	s_cbranch_scc1 .LBB0_296
	s_barrier
; #define ATT_PK4(P, BASE, OUT) do { u32x4 w = {cvtpk(P[BASE + 0], P[BASE + 1]), cvtpk(P[BASE + 2], P[BASE + 3]), cvtpk(P[BASE + 4], P[BASE + 5]), cvtpk(P[BASE + 6], P[BASE + 7])}; \
;     OUT = *reinterpret_cast<bf16x8*>(&w); } while (0)
; template <int DQK> __device__ __forceinline__ void qkt(f32x16& p0, f32x16& p1, const char* Ks, const bf16x8* qr, int r32, int hi) {
;   p0 = f32x16{}; p1 = f32x16{};
; #pragma unroll
;   for (int d0 = 0; d0 < DQK / 16; ++d0) { const int cb = (d0 * 16 + hi * 8) * 2;
;     const bf16x8 b0 = *reinterpret_cast<const bf16x8*>(Ks + kswz<DQK>(r32, cb));
;     const bf16x8 b1 = *reinterpret_cast<const bf16x8*>(Ks + kswz<DQK>(32 + r32, cb));
;     p0 = __builtin_amdgcn_mfma_f32_32x32x16_bf16(b0, qr[d0], p0, 0, 0, 0);
;     p1 = __builtin_amdgcn_mfma_f32_32x32x16_bf16(b1, qr[d0], p1, 0, 0, 0); }
; }
; __device__ __forceinline__ float softmax_shift(f32x16& p0, f32x16& p1, f32x16& negm, float pmax, bool first) {
;   asm volatile("s_nop 4" ::: "memory");
;   { auto rr = __builtin_amdgcn_permlane32_swap(__float_as_uint(pmax), __float_as_uint(pmax), false, false);
;     pmax = fmaxf(__uint_as_float(rr[0]), __uint_as_float(rr[1])); }
;   const float delta = first ? pmax : fmaxf(pmax, 0.f);
; #pragma unroll
;   for (int r = 0; r < 16; ++r) { p0[r] -= delta; p1[r] -= delta; negm[r] -= delta; }
;   return first ? 1.f : __builtin_amdgcn_exp2f(-delta);
; }
; __device__ __forceinline__ void softmax_exp_pack(f32x16& p0, f32x16& p1, bf16x8& pa0, bf16x8& pa1, bf16x8& pa2, bf16x8& pa3) {
; #pragma unroll
;   for (int r = 0; r < 16; ++r) { p0[r] = __builtin_amdgcn_exp2f(p0[r]); p1[r] = __builtin_amdgcn_exp2f(p1[r]); }
;     ...
;   ATT_PK4(p0, 0, pa0); ATT_PK4(p0, 8, pa1); ATT_PK4(p1, 0, pa2); ATT_PK4(p1, 8, pa3);
.LBB0_296:
	v_mul_u32_u24_e32 v2, 0x90, v62
	v_add3_u32 v78, 0, v184, v2
	ds_read_b128 v[2:5], v78 offset:49152
	v_mad_u32_u24 v167, v62, s82, 0
	v_add_u32_e32 v173, v167, v184
	ds_read_b128 v[34:37], v173 offset:53760
	ds_read_b128 v[66:69], v78 offset:49184
	ds_read_b128 v[70:73], v78 offset:49216
	v_and_b32_e32 v63, 63, v63
	s_mov_b32 s90, 1
	s_waitcnt lgkmcnt(3)
	v_mfma_f32_32x32x16_bf16 v[2:17], v[2:5], v[136:139], 0
	s_waitcnt lgkmcnt(2)
	v_mfma_f32_32x32x16_bf16 v[34:49], v[34:37], v[136:139], 0
	s_waitcnt lgkmcnt(1)
	v_mfma_f32_32x32x16_bf16 v[2:17], v[66:69], v[140:143], v[2:17]
	ds_read_b128 v[66:69], v78 offset:53792
	ds_read_b128 v[74:77], v78 offset:49248
	s_waitcnt lgkmcnt(1)
	v_mfma_f32_32x32x16_bf16 v[34:49], v[66:69], v[140:143], v[34:49]
	v_mfma_f32_32x32x16_bf16 v[2:17], v[70:73], v[144:147], v[2:17]
	ds_read_b128 v[66:69], v78 offset:53824
	ds_read_b128 v[70:73], v78 offset:53856
	s_waitcnt lgkmcnt(1)
	v_mfma_f32_32x32x16_bf16 v[34:49], v[66:69], v[144:147], v[34:49]
	v_lshlrev_b32_e32 v67, 3, v63
	v_lshlrev_b32_e32 v69, 4, v63
	v_add_u32_e32 v66, 0xc000, v170
	v_and_b32_e32 v68, 24, v67
	v_and_b32_e32 v69, 0xc0, v69
	v_and_b32_e32 v67, 0x100, v67
	v_mfma_f32_32x32x16_bf16 v[2:17], v[74:77], v[148:151], v[2:17]
	v_lshlrev_b32_e32 v74, 1, v63
	v_and_b32_e32 v74, 32, v74
	s_waitcnt lgkmcnt(0)
	v_mfma_f32_32x32x16_bf16 v[34:49], v[70:73], v[148:151], v[34:49]
	s_barrier
	v_cmp_gt_u32_e64 s[4:5], 32, v63
	v_lshl_add_u32 v166, v62, 2, s6
	s_nop 9
	v_add_f32_e32 v62, 0, v34
	v_max3_f32 v63, v62, v2, v3
	v_max3_f32 v63, v63, v4, v5
	v_max3_f32 v63, v63, v6, v7
	v_max3_f32 v63, v63, v8, v9
	v_max3_f32 v63, v63, v10, v11
	v_max3_f32 v63, v63, v12, v13
	v_max3_f32 v63, v63, v14, v15
	v_max3_f32 v63, v63, v16, v17
	s_nop 4
	v_add3_u32 v68, 0, v68, v69
	v_max3_f32 v62, v63, v35, v36
	v_max3_f32 v62, v62, v37, v38
	v_max3_f32 v62, v62, v39, v40
	v_max3_f32 v62, v62, v41, v42
	v_max3_f32 v62, v62, v43, v44
	v_max3_f32 v62, v62, v45, v46
	v_max3_f32 v62, v62, v47, v48
	v_max_f32 v62, v62, v49
	v_add3_u32 v131, v68, v74, v67
	v_mov_b32_e32 v63, v62
	s_nop 1
	v_permlane32_swap_b32_e32 v62, v63
	v_max_f32_e32 v63, v63, v63
	v_max_f32_e32 v62, v62, v62
	v_max_f32_e32 v62, v62, v63
	v_sub_f32_e32 v2, v2, v62
	v_sub_f32_e32 v34, v34, v62
	v_sub_f32_e32 v3, v3, v62
	v_sub_f32_e32 v35, v35, v62
	v_sub_f32_e32 v4, v4, v62
	v_sub_f32_e32 v36, v36, v62
	v_sub_f32_e32 v5, v5, v62
	v_sub_f32_e32 v37, v37, v62
	v_sub_f32_e32 v6, v6, v62
	v_sub_f32_e32 v38, v38, v62
	v_sub_f32_e32 v7, v7, v62
	v_sub_f32_e32 v39, v39, v62
	v_sub_f32_e32 v8, v8, v62
	v_sub_f32_e32 v40, v40, v62
	v_sub_f32_e32 v9, v9, v62
	v_sub_f32_e32 v41, v41, v62
	v_sub_f32_e32 v10, v10, v62
	v_sub_f32_e32 v42, v42, v62
	v_sub_f32_e32 v11, v11, v62
	v_sub_f32_e32 v43, v43, v62
	v_sub_f32_e32 v12, v12, v62
	v_sub_f32_e32 v44, v44, v62
	v_sub_f32_e32 v13, v13, v62
	v_sub_f32_e32 v45, v45, v62
	v_sub_f32_e32 v14, v14, v62
	v_sub_f32_e32 v46, v46, v62
	v_sub_f32_e32 v15, v15, v62
	v_sub_f32_e32 v47, v47, v62
	v_sub_f32_e32 v16, v16, v62
	v_sub_f32_e32 v48, v48, v62
	v_sub_f32_e32 v17, v17, v62
	v_sub_f32_e32 v49, v49, v62
	v_exp_f32_e32 v2, v2
	v_exp_f32_e32 v34, v34
	v_exp_f32_e32 v3, v3
	v_exp_f32_e32 v35, v35
	v_exp_f32_e32 v4, v4
	v_exp_f32_e32 v36, v36
	v_exp_f32_e32 v5, v5
	v_exp_f32_e32 v37, v37
	v_exp_f32_e32 v6, v6
	v_exp_f32_e32 v38, v38
	v_exp_f32_e32 v7, v7
	v_exp_f32_e32 v39, v39
	v_exp_f32_e32 v8, v8
	v_exp_f32_e32 v40, v40
	v_exp_f32_e32 v9, v9
	v_exp_f32_e32 v41, v41
	v_exp_f32_e32 v10, v10
	v_exp_f32_e32 v42, v42
	v_exp_f32_e32 v11, v11
	v_exp_f32_e32 v43, v43
	v_exp_f32_e32 v12, v12
	v_exp_f32_e32 v44, v44
	v_exp_f32_e32 v13, v13
	v_exp_f32_e32 v45, v45
	v_exp_f32_e32 v14, v14
	v_exp_f32_e32 v46, v46
	v_exp_f32_e32 v15, v15
	v_exp_f32_e32 v47, v47
	v_exp_f32_e32 v16, v16
	v_exp_f32_e32 v48, v48
	v_exp_f32_e32 v17, v17
	v_exp_f32_e32 v49, v49
	v_sub_f32_e32 v82, 0, v62
	v_mov_b32_e32 v83, v82
	v_mov_b32_e32 v84, v82
	v_mov_b32_e32 v85, v82
	v_mov_b32_e32 v86, v82
	v_mov_b32_e32 v87, v82
	v_mov_b32_e32 v88, v82
	v_mov_b32_e32 v89, v82
	v_mov_b32_e32 v90, v82
	v_mov_b32_e32 v91, v82
	v_mov_b32_e32 v92, v82
	v_mov_b32_e32 v93, v82
	v_mov_b32_e32 v94, v82
	v_mov_b32_e32 v95, v82
	v_mov_b32_e32 v96, v82
	v_mov_b32_e32 v97, v82
	v_cvt_pk_bf16_f32 v98, v2, v3
	v_cvt_pk_bf16_f32 v99, v4, v5
	v_cvt_pk_bf16_f32 v100, v6, v7
	v_cvt_pk_bf16_f32 v101, v8, v9
	v_cvt_pk_bf16_f32 v102, v10, v11
	v_cvt_pk_bf16_f32 v103, v12, v13
	v_cvt_pk_bf16_f32 v104, v14, v15
	v_cvt_pk_bf16_f32 v105, v16, v17
	v_cvt_pk_bf16_f32 v106, v34, v35
	v_cvt_pk_bf16_f32 v107, v36, v37
	v_cvt_pk_bf16_f32 v108, v38, v39
	v_cvt_pk_bf16_f32 v109, v40, v41
	v_cvt_pk_bf16_f32 v110, v42, v43
	v_cvt_pk_bf16_f32 v111, v44, v45
	v_cvt_pk_bf16_f32 v112, v46, v47
	v_cvt_pk_bf16_f32 v113, v48, v49
	s_waitcnt vmcnt(1)
	ds_write_b128 v66, v[58:61] offset:18432
	ds_write_b128 v64, v[50:53] offset:16384
	s_waitcnt vmcnt(0)
	ds_write_b128 v65, v[54:57] offset:16384
	ds_read_b64_tr_b16 v[2:3], v131
	ds_read_b64_tr_b16 v[4:5], v131 offset:2048
	ds_read_b64_tr_b16 v[6:7], v131 offset:4096
	ds_read_b64_tr_b16 v[8:9], v131 offset:6144
	ds_read_b64_tr_b16 v[10:11], v131 offset:8192
	ds_read_b64_tr_b16 v[12:13], v131 offset:10240
	ds_read_b64_tr_b16 v[14:15], v131 offset:12288
	ds_read_b64_tr_b16 v[16:17], v131 offset:14336
	s_waitcnt lgkmcnt(8)
	s_barrier
; #define ATT_SBAR() __builtin_amdgcn_sched_barrier(0)
; __device__ __forceinline__ unsigned cvtpk(float lo, float hi) { f32x2_t v = {lo, hi}; bf16x2_t b = __builtin_convertvector(v, bf16x2_t); return __builtin_bit_cast(unsigned, b); }
; #define ATT_LOAD_K(t) do { const unsigned so_ = (unsigned)(t) * (unsigned)(KVBLK * LDK * 2); sk0 = __builtin_bit_cast(bf16x8, __builtin_amdgcn_raw_buffer_load_b128(krs, koff, so_, 0)); \
;     if constexpr (DQK == 128) sk1 = __builtin_bit_cast(bf16x8, __builtin_amdgcn_raw_buffer_load_b128(krs, koff, so_ + (unsigned)(32 * LDK * 2), 0)); } while (0)
; #define ATT_LOAD_V(t) do { const unsigned so_ = (unsigned)(t) * (unsigned)(KVBLK * LDV * 2); sv0 = __builtin_bit_cast(bf16x8, __builtin_amdgcn_raw_buffer_load_b128(vrs, voff, so_, 0)); \
;     sv1 = __builtin_bit_cast(bf16x8, __builtin_amdgcn_raw_buffer_load_b128(vrs, voff, so_ + (unsigned)(32 * LDV * 2), 0)); } while (0)
; #define ATT_WRITE_K(so) do { *(bf16x8*)(K_lds + (so) + kswz<DQK>(kr, kc * 2)) = sk0; if constexpr (DQK == 128) *(bf16x8*)(K_lds + (so) + kswz<DQK>(32 + kr, kc * 2)) = sk1; } while (0)
; #define ATT_WRITE_V(so) do { *(bf16x8*)(V_lds + (so) + vst0) = sv0; *(bf16x8*)(V_lds + (so) + vst1) = sv1; } while (0)
;     ...
;   for (int t = 0; t + 1 < NT; ++t) {
;     if constexpr (ABL & 1) { u32x4 w0 = {cvtpk(p0[0], p0[1]), cvtpk(p0[2], p0[3]), cvtpk(p0[4], p0[5]), cvtpk(p0[6], p0[7])}, w1 = {cvtpk(p0[8], p0[9]), cvtpk(p0[10], p0[11]), cvtpk(p0[12], p0[13]), cvtpk(p0[14], p0[15])};
;         u32x4 w2 = {cvtpk(p1[0], p1[1]), cvtpk(p1[2], p1[3]), cvtpk(p1[4], p1[5]), cvtpk(p1[6], p1[7])}, w3 = {cvtpk(p1[8], p1[9]), cvtpk(p1[10], p1[11]), cvtpk(p1[12], p1[13]), cvtpk(p1[14], p1[15])};
;         pa0 = *reinterpret_cast<bf16x8*>(&w0); pa1 = *reinterpret_cast<bf16x8*>(&w1); pa2 = *reinterpret_cast<bf16x8*>(&w2); pa3 = *reinterpret_cast<bf16x8*>(&w3); }
;     else { ATT_SOFTMAX(t == 0); }
;     if constexpr (!(ABL & 4)) { ATT_WRITE_K(k2); ATT_WRITE_V(v1); }
;     ATT_SBAR();
; #pragma unroll
;     for (int ks = 0; ks < 4; ++ks) ATT_VPAIR(va, v0, 0, ks);
;     asm volatile("s_waitcnt lgkmcnt(8)" ::: "memory"); ATT_BAR();
;     ATT_XSECTION(true);
;     if constexpr (!(ABL & 4)) { const int tk = (t + 3 < NT) ? t + 3 : NT - 1, tv = (t + 2 < NT) ? t + 2 : NT - 1; ATT_LOAD_K(tk); ATT_LOAD_V(tv); }
;     ATT_BAR();
	s_setprio 2
	s_waitcnt lgkmcnt(6)
	v_mfma_f32_32x32x16_bf16 v[66:81], v[98:101], v[2:5], 0
	ds_read_b64_tr_b16 v[34:35], v131 offset:512
	ds_read_b64_tr_b16 v[36:37], v131 offset:2560
	s_waitcnt lgkmcnt(6)
	v_mfma_f32_32x32x16_bf16 v[66:81], v[102:105], v[6:9], v[66:81]
	ds_read_b64_tr_b16 v[2:3], v131 offset:4608
	ds_read_b64_tr_b16 v[4:5], v131 offset:6656
	s_waitcnt lgkmcnt(6)
	v_mfma_f32_32x32x16_bf16 v[66:81], v[106:109], v[10:13], v[66:81]
	ds_read_b64_tr_b16 v[6:7], v131 offset:8704
	ds_read_b64_tr_b16 v[8:9], v131 offset:10752
	s_waitcnt lgkmcnt(6)
	v_mfma_f32_32x32x16_bf16 v[66:81], v[110:113], v[14:17], v[66:81]
	ds_read_b64_tr_b16 v[10:11], v131 offset:12800
	ds_read_b64_tr_b16 v[12:13], v131 offset:14848
	s_waitcnt lgkmcnt(6)
	v_mfma_f32_32x32x16_bf16 v[50:65], v[98:101], v[34:37], 0
	ds_read_b64_tr_b16 v[14:15], v131 offset:1024
	ds_read_b64_tr_b16 v[16:17], v131 offset:3072
	s_waitcnt lgkmcnt(6)
	v_mfma_f32_32x32x16_bf16 v[50:65], v[102:105], v[2:5], v[50:65]
	ds_read_b64_tr_b16 v[114:115], v131 offset:5120
	ds_read_b64_tr_b16 v[116:117], v131 offset:7168
	s_waitcnt lgkmcnt(6)
	v_mfma_f32_32x32x16_bf16 v[50:65], v[106:109], v[6:9], v[50:65]
	ds_read_b64_tr_b16 v[2:3], v131 offset:9216
	ds_read_b64_tr_b16 v[4:5], v131 offset:11264
	s_waitcnt lgkmcnt(6)
	v_mfma_f32_32x32x16_bf16 v[50:65], v[110:113], v[10:13], v[50:65]
	ds_read_b64_tr_b16 v[6:7], v131 offset:13312
	ds_read_b64_tr_b16 v[8:9], v131 offset:15360
	s_waitcnt lgkmcnt(6)
	v_mfma_f32_32x32x16_bf16 v[34:49], v[98:101], v[14:17], 0
	ds_read_b64_tr_b16 v[10:11], v131 offset:1536
	ds_read_b64_tr_b16 v[12:13], v131 offset:3584
	s_waitcnt lgkmcnt(6)
	v_mfma_f32_32x32x16_bf16 v[34:49], v[102:105], v[114:117], v[34:49]
	ds_read_b64_tr_b16 v[118:119], v131 offset:5632
	ds_read_b64_tr_b16 v[120:121], v131 offset:7680
	s_waitcnt lgkmcnt(6)
	v_mfma_f32_32x32x16_bf16 v[34:49], v[106:109], v[2:5], v[34:49]
	ds_read_b64_tr_b16 v[114:115], v131 offset:9728
	ds_read_b64_tr_b16 v[116:117], v131 offset:11776
	s_waitcnt lgkmcnt(6)
	v_mfma_f32_32x32x16_bf16 v[34:49], v[110:113], v[6:9], v[34:49]
	ds_read_b64_tr_b16 v[122:123], v131 offset:13824
	ds_read_b64_tr_b16 v[124:125], v131 offset:15872
	s_waitcnt lgkmcnt(6)
	v_mfma_f32_32x32x16_bf16 v[2:17], v[98:101], v[10:13], 0
	ds_read_b128 v[126:129], v173 offset:58368
	s_waitcnt lgkmcnt(5)
	v_mfma_f32_32x32x16_bf16 v[2:17], v[102:105], v[118:121], v[2:17]
	ds_read_b128 v[152:155], v173 offset:62976
	s_waitcnt lgkmcnt(4)
	v_mfma_f32_32x32x16_bf16 v[2:17], v[106:109], v[114:117], v[2:17]
	ds_read_b128 v[156:159], v173 offset:58400
	s_waitcnt lgkmcnt(3)
	v_mfma_f32_32x32x16_bf16 v[2:17], v[110:113], v[122:125], v[2:17]
	ds_read_b128 v[160:163], v173 offset:63008
	v_mfma_f32_16x16x32_bf16 v[240:243], v[98:101], v[132:135], 0
	ds_read_b128 v[174:177], v173 offset:58432
	v_mfma_f32_16x16x32_bf16 v[240:243], v[102:105], v[132:135], v[240:243]
	ds_read_b128 v[178:181], v173 offset:63040
	v_mfma_f32_16x16x32_bf16 v[240:243], v[106:109], v[132:135], v[240:243]
	ds_read_b128 v[186:189], v173 offset:58464
	v_mfma_f32_16x16x32_bf16 v[240:243], v[110:113], v[132:135], v[240:243]
	ds_read_b128 v[190:193], v173 offset:63072
	s_waitcnt lgkmcnt(7)
	v_mfma_f32_32x32x16_bf16 v[98:113], v[126:129], v[136:139], v[82:97]
	v_mov_b64_e32 v[128:129], v[96:97]
	v_mov_b64_e32 v[126:127], v[94:95]
	v_mov_b64_e32 v[124:125], v[92:93]
	v_mov_b64_e32 v[122:123], v[90:91]
	v_mov_b64_e32 v[120:121], v[88:89]
	v_mov_b64_e32 v[118:119], v[86:87]
	v_mov_b64_e32 v[116:117], v[84:85]
	v_mov_b64_e32 v[114:115], v[82:83]
	s_waitcnt lgkmcnt(6)
	s_nop 0
	v_mfma_f32_32x32x16_bf16 v[114:129], v[152:155], v[136:139], v[114:129]
	s_waitcnt lgkmcnt(5)
	v_mfma_f32_32x32x16_bf16 v[98:113], v[156:159], v[140:143], v[98:113]
	s_waitcnt lgkmcnt(4)
	v_mfma_f32_32x32x16_bf16 v[114:129], v[160:163], v[140:143], v[114:129]
	s_waitcnt lgkmcnt(3)
	v_mfma_f32_32x32x16_bf16 v[98:113], v[174:177], v[144:147], v[98:113]
	s_waitcnt lgkmcnt(2)
	v_mfma_f32_32x32x16_bf16 v[114:129], v[178:181], v[144:147], v[114:129]
	s_waitcnt lgkmcnt(1)
	v_mfma_f32_32x32x16_bf16 v[98:113], v[186:189], v[148:151], v[98:113]
	s_waitcnt lgkmcnt(0)
	v_mfma_f32_32x32x16_bf16 v[114:129], v[190:193], v[148:151], v[114:129]
	s_setprio 0
	buffer_load_dwordx4 v[224:227], v171, s[8:11], s85 offen
	buffer_load_dwordx4 v[228:231], v172, s[12:15], s83 offen
	buffer_load_dwordx4 v[232:235], v172, s[12:15], s86 offen
	s_barrier
	s_mov_b32 s50, 0x8000
	s_movk_i32 s15, 0x4000
	s_movk_i32 s51, 0x2400
	s_mov_b32 s49, 0
	s_movk_i32 s14, 0x4800
	s_mov_b32 s36, 0x70000
	s_mov_b32 s48, 0
	s_nop 0
	v_add_f32_e32 v174, 0, v114
	v_max3_f32 v175, v174, v98, v99
	v_max3_f32 v175, v175, v100, v101
	v_max3_f32 v175, v175, v102, v103
	v_max3_f32 v175, v175, v104, v105
	v_max3_f32 v175, v175, v106, v107
	v_max3_f32 v175, v175, v108, v109
	v_max3_f32 v175, v175, v110, v111
	v_max3_f32 v175, v175, v112, v113
	v_max3_f32 v174, v175, v115, v116
	v_max3_f32 v174, v174, v117, v118
	v_max3_f32 v174, v174, v119, v120
	v_max3_f32 v174, v174, v121, v122
	v_max3_f32 v174, v174, v123, v124
	v_max3_f32 v174, v174, v125, v126
	v_max3_f32 v174, v174, v127, v128
	v_max_f32 v174, v174, v129

; #define ATT_SBAR() __builtin_amdgcn_sched_barrier(0)
; __device__ __forceinline__ unsigned cvtpk(float lo, float hi) { f32x2_t v = {lo, hi}; bf16x2_t b = __builtin_convertvector(v, bf16x2_t); return __builtin_bit_cast(unsigned, b); }
; #define ATT_LOAD_K(t) do { const unsigned so_ = (unsigned)(t) * (unsigned)(KVBLK * LDK * 2); sk0 = __builtin_bit_cast(bf16x8, __builtin_amdgcn_raw_buffer_load_b128(krs, koff, so_, 0)); \
;     if constexpr (DQK == 128) sk1 = __builtin_bit_cast(bf16x8, __builtin_amdgcn_raw_buffer_load_b128(krs, koff, so_ + (unsigned)(32 * LDK * 2), 0)); } while (0)
; #define ATT_LOAD_V(t) do { const unsigned so_ = (unsigned)(t) * (unsigned)(KVBLK * LDV * 2); sv0 = __builtin_bit_cast(bf16x8, __builtin_amdgcn_raw_buffer_load_b128(vrs, voff, so_, 0)); \
;     sv1 = __builtin_bit_cast(bf16x8, __builtin_amdgcn_raw_buffer_load_b128(vrs, voff, so_ + (unsigned)(32 * LDV * 2), 0)); } while (0)
; #define ATT_WRITE_K(so) do { *(bf16x8*)(K_lds + (so) + kswz<DQK>(kr, kc * 2)) = sk0; if constexpr (DQK == 128) *(bf16x8*)(K_lds + (so) + kswz<DQK>(32 + kr, kc * 2)) = sk1; } while (0)
;     ...
;   for (int t = 0; t + 1 < NT; ++t) {
;     if constexpr (ABL & 1) { u32x4 w0 = {cvtpk(p0[0], p0[1]), cvtpk(p0[2], p0[3]), cvtpk(p0[4], p0[5]), cvtpk(p0[6], p0[7])}, w1 = {cvtpk(p0[8], p0[9]), cvtpk(p0[10], p0[11]), cvtpk(p0[12], p0[13]), cvtpk(p0[14], p0[15])};
;         u32x4 w2 = {cvtpk(p1[0], p1[1]), cvtpk(p1[2], p1[3]), cvtpk(p1[4], p1[5]), cvtpk(p1[6], p1[7])}, w3 = {cvtpk(p1[8], p1[9]), cvtpk(p1[10], p1[11]), cvtpk(p1[12], p1[13]), cvtpk(p1[14], p1[15])};
;         pa0 = *reinterpret_cast<bf16x8*>(&w0); pa1 = *reinterpret_cast<bf16x8*>(&w1); pa2 = *reinterpret_cast<bf16x8*>(&w2); pa3 = *reinterpret_cast<bf16x8*>(&w3); }
;     else { ATT_SOFTMAX(t == 0); }
;     if constexpr (!(ABL & 4)) { ATT_WRITE_K(k2); ATT_WRITE_V(v1); }
;     ATT_SBAR();
; #pragma unroll
;     for (int ks = 0; ks < 4; ++ks) ATT_VPAIR(va, v0, 0, ks);
;     asm volatile("s_waitcnt lgkmcnt(8)" ::: "memory"); ATT_BAR();
;     ATT_XSECTION(true);
;     if constexpr (!(ABL & 4)) { const int tk = (t + 3 < NT) ? t + 3 : NT - 1, tv = (t + 2 < NT) ? t + 2 : NT - 1; ATT_LOAD_K(tk); ATT_LOAD_V(tv); }
;     ATT_BAR();
;     { const int tk_ = k0; k0 = k1; k1 = k2; k2 = tk_; const int tv_ = v0; v0 = v1; v1 = v2; v2 = tv_; }
.LBB0_298:
	v_exp_f32_e32 v98, v98
	v_exp_f32_e32 v114, v114
	v_exp_f32_e32 v99, v99
	v_exp_f32_e32 v115, v115
	v_exp_f32_e32 v100, v100
	v_exp_f32_e32 v101, v101
	v_exp_f32_e32 v102, v102
	v_exp_f32_e32 v103, v103
	v_exp_f32_e32 v106, v106
	v_exp_f32_e32 v107, v107
	v_exp_f32_e32 v116, v116
	v_exp_f32_e32 v117, v117
	v_exp_f32_e32 v118, v118
	v_exp_f32_e32 v119, v119
	v_exp_f32_e32 v104, v104
	v_exp_f32_e32 v120, v120
	v_exp_f32_e32 v105, v105
	v_exp_f32_e32 v121, v121
	v_exp_f32_e32 v122, v122
	v_exp_f32_e32 v123, v123
	v_exp_f32_e32 v108, v108
	v_exp_f32_e32 v124, v124
	v_exp_f32_e32 v109, v109
	v_exp_f32_e32 v125, v125
	v_exp_f32_e32 v110, v110
	v_exp_f32_e32 v126, v126
	v_exp_f32_e32 v111, v111
	v_exp_f32_e32 v127, v127
	v_exp_f32_e32 v112, v112
	v_exp_f32_e32 v128, v128
	v_exp_f32_e32 v113, v113
	v_exp_f32_e32 v129, v129
	v_cvt_pk_bf16_f32 v18, v98, v99
	v_cvt_pk_bf16_f32 v19, v100, v101
	v_cvt_pk_bf16_f32 v20, v102, v103
	v_cvt_pk_bf16_f32 v22, v106, v107
	v_cvt_pk_bf16_f32 v26, v114, v115
	v_cvt_pk_bf16_f32 v21, v104, v105
	v_cvt_pk_bf16_f32 v23, v108, v109
	v_cvt_pk_bf16_f32 v24, v110, v111
	v_cvt_pk_bf16_f32 v25, v112, v113
	v_cvt_pk_bf16_f32 v27, v116, v117
	v_cvt_pk_bf16_f32 v28, v118, v119
	v_cvt_pk_bf16_f32 v29, v120, v121
	v_cvt_pk_bf16_f32 v30, v122, v123
	v_cvt_pk_bf16_f32 v31, v124, v125
	v_cvt_pk_bf16_f32 v32, v126, v127
	v_cvt_pk_bf16_f32 v33, v128, v129
	s_waitcnt vmcnt(0)
	v_add_u32_e32 v114, s49, v170
	ds_write_b128 v114, v[224:227] offset:49152
	v_add_u32_e32 v114, s50, v168
	ds_write_b128 v114, v[228:231]
	v_add_u32_e32 v114, s50, v169
	ds_write_b128 v114, v[232:235]
	v_add_u32_e32 v249, s18, v173
	ds_read_b128 v[152:155], v249 offset:49152
	ds_read_b128 v[156:159], v249 offset:53760
	ds_read_b128 v[160:163], v249 offset:49184
	ds_read_b128 v[176:179], v249 offset:53792
	s_waitcnt lgkmcnt(4)
	s_barrier
	s_setprio 2
	s_waitcnt lgkmcnt(3)
	v_mfma_f32_32x32x16_bf16 v[98:113], v[152:155], v[136:139], v[82:97]
	ds_read_b128 v[180:183], v249 offset:49216
	s_waitcnt lgkmcnt(3)
	v_mfma_f32_32x32x16_bf16 v[114:129], v[156:159], v[136:139], v[82:97]
	ds_read_b128 v[186:189], v249 offset:53824
	v_add_u32_e32 v248, s37, v131
	s_waitcnt lgkmcnt(3)
	v_mfma_f32_32x32x16_bf16 v[98:113], v[160:163], v[140:143], v[98:113]
	ds_read_b128 v[190:193], v249 offset:49248
	ds_read_b64_tr_b16 v[198:199], v248
	ds_read_b64_tr_b16 v[200:201], v248 offset:2048
	s_waitcnt lgkmcnt(5)
	v_mfma_f32_32x32x16_bf16 v[114:129], v[176:179], v[140:143], v[114:129]
	ds_read_b128 v[194:197], v249 offset:53856
	ds_read_b64_tr_b16 v[212:213], v248 offset:4096
	ds_read_b64_tr_b16 v[214:215], v248 offset:6144
	s_waitcnt lgkmcnt(7)
	v_mfma_f32_32x32x16_bf16 v[98:113], v[180:183], v[144:147], v[98:113]
	ds_read_b64_tr_b16 v[216:217], v248 offset:8192
	ds_read_b64_tr_b16 v[218:219], v248 offset:10240
	s_waitcnt lgkmcnt(8)
	v_mfma_f32_32x32x16_bf16 v[114:129], v[186:189], v[144:147], v[114:129]
	ds_read_b64_tr_b16 v[220:221], v248 offset:12288
	ds_read_b64_tr_b16 v[222:223], v248 offset:14336
	s_waitcnt lgkmcnt(9)
	v_mfma_f32_32x32x16_bf16 v[98:113], v[190:193], v[148:151], v[98:113]
	s_waitcnt lgkmcnt(6)
	v_mfma_f32_32x32x16_bf16 v[114:129], v[194:197], v[148:151], v[114:129]
	v_mfma_f32_32x32x16_bf16 v[66:81], v[18:21], v[198:201], v[66:81]
	ds_read_b64_tr_b16 v[236:237], v248 offset:512
	ds_read_b64_tr_b16 v[238:239], v248 offset:2560
	s_waitcnt lgkmcnt(6)
	v_mfma_f32_32x32x16_bf16 v[66:81], v[22:25], v[212:215], v[66:81]
	ds_read_b64_tr_b16 v[198:199], v248 offset:4608
	ds_read_b64_tr_b16 v[200:201], v248 offset:6656
	s_waitcnt lgkmcnt(6)
	v_mfma_f32_32x32x16_bf16 v[66:81], v[26:29], v[216:219], v[66:81]
	ds_read_b64_tr_b16 v[212:213], v248 offset:8704
	ds_read_b64_tr_b16 v[214:215], v248 offset:10752
	s_waitcnt lgkmcnt(6)
	v_mfma_f32_32x32x16_bf16 v[66:81], v[30:33], v[220:223], v[66:81]
	ds_read_b64_tr_b16 v[216:217], v248 offset:12800
	ds_read_b64_tr_b16 v[218:219], v248 offset:14848
	v_max3_f32 v249, v98, v99, v100
	s_waitcnt lgkmcnt(6)
	v_mfma_f32_32x32x16_bf16 v[50:65], v[18:21], v[236:239], v[50:65]
	ds_read_b64_tr_b16 v[220:221], v248 offset:1024
	ds_read_b64_tr_b16 v[222:223], v248 offset:3072
	v_max3_f32 v174, v114, v115, v116
	s_waitcnt lgkmcnt(6)
	v_mfma_f32_32x32x16_bf16 v[50:65], v[22:25], v[198:201], v[50:65]
	ds_read_b64_tr_b16 v[236:237], v248 offset:5120
	ds_read_b64_tr_b16 v[238:239], v248 offset:7168
	v_max3_f32 v249, v249, v101, v102
	s_waitcnt lgkmcnt(6)
	v_mfma_f32_32x32x16_bf16 v[50:65], v[26:29], v[212:215], v[50:65]
	ds_read_b64_tr_b16 v[198:199], v248 offset:9216
	ds_read_b64_tr_b16 v[200:201], v248 offset:11264
	v_max3_f32 v174, v174, v117, v118
	s_waitcnt lgkmcnt(6)
	v_mfma_f32_32x32x16_bf16 v[50:65], v[30:33], v[216:219], v[50:65]
	ds_read_b64_tr_b16 v[212:213], v248 offset:13312
	ds_read_b64_tr_b16 v[214:215], v248 offset:15360
	v_max3_f32 v249, v249, v103, v104
	s_waitcnt lgkmcnt(6)
	v_mfma_f32_32x32x16_bf16 v[34:49], v[18:21], v[220:223], v[34:49]
	ds_read_b64_tr_b16 v[216:217], v248 offset:1536
	ds_read_b64_tr_b16 v[218:219], v248 offset:3584
	v_max3_f32 v174, v174, v119, v120
	s_waitcnt lgkmcnt(6)
	v_mfma_f32_32x32x16_bf16 v[34:49], v[22:25], v[236:239], v[34:49]
	ds_read_b64_tr_b16 v[220:221], v248 offset:5632
	ds_read_b64_tr_b16 v[222:223], v248 offset:7680
	v_max3_f32 v249, v249, v105, v106
	s_waitcnt lgkmcnt(6)
	v_mfma_f32_32x32x16_bf16 v[34:49], v[26:29], v[198:201], v[34:49]
	ds_read_b64_tr_b16 v[236:237], v248 offset:9728
	ds_read_b64_tr_b16 v[238:239], v248 offset:11776
	v_max3_f32 v174, v174, v121, v122
	s_waitcnt lgkmcnt(6)
	v_mfma_f32_32x32x16_bf16 v[34:49], v[30:33], v[212:215], v[34:49]
	ds_read_b64_tr_b16 v[198:199], v248 offset:13824
	ds_read_b64_tr_b16 v[200:201], v248 offset:15872
	v_max3_f32 v249, v249, v107, v108
	s_waitcnt lgkmcnt(6)
	v_mfma_f32_32x32x16_bf16 v[2:17], v[18:21], v[216:219], v[2:17]
	v_max3_f32 v174, v174, v123, v124
	s_min_u32 s14, s90, 0x7c
	s_lshl_b32 s14, s14, 17
	s_add_i32 s19, s14, 0x60000
	s_add_i32 s92, s36, 0xffff0000
	s_mov_b32 s14, s10
	s_mov_b32 s15, s11
	buffer_load_dwordx4 v[224:227], v171, s[8:11], s19 offen
	s_waitcnt lgkmcnt(4)
	v_mfma_f32_32x32x16_bf16 v[2:17], v[22:25], v[220:223], v[2:17]
	v_max3_f32 v249, v249, v109, v110
	buffer_load_dwordx4 v[228:231], v172, s[12:15], s92 offen
	s_waitcnt lgkmcnt(2)
	v_mfma_f32_32x32x16_bf16 v[2:17], v[26:29], v[236:239], v[2:17]
	v_max3_f32 v174, v174, v125, v126
	buffer_load_dwordx4 v[232:235], v172, s[12:15], s36 offen
	s_waitcnt lgkmcnt(0)
	v_mfma_f32_32x32x16_bf16 v[2:17], v[30:33], v[198:201], v[2:17]
	v_max3_f32 v249, v249, v111, v112
	v_mfma_f32_16x16x32_bf16 v[240:243], v[18:21], v[132:135], v[240:243]
	v_max3_f32 v174, v174, v127, v128
	v_mfma_f32_16x16x32_bf16 v[240:243], v[22:25], v[132:135], v[240:243]
	v_max_f32 v249, v249, v113
	v_mfma_f32_16x16x32_bf16 v[240:243], v[26:29], v[132:135], v[240:243]
	v_max_f32 v174, v174, v129
	v_mfma_f32_16x16x32_bf16 v[240:243], v[30:33], v[132:135], v[240:243]
	v_max_f32 v174, v174, v249
	s_setprio 0
	s_barrier
; #define ATT_LOAD_K(t) do { const unsigned so_ = (unsigned)(t) * (unsigned)(KVBLK * LDK * 2); sk0 = __builtin_bit_cast(bf16x8, __builtin_amdgcn_raw_buffer_load_b128(krs, koff, so_, 0)); \
;     if constexpr (DQK == 128) sk1 = __builtin_bit_cast(bf16x8, __builtin_amdgcn_raw_buffer_load_b128(krs, koff, so_ + (unsigned)(32 * LDK * 2), 0)); } while (0)
; #define ATT_LOAD_V(t) do { const unsigned so_ = (unsigned)(t) * (unsigned)(KVBLK * LDV * 2); sv0 = __builtin_bit_cast(bf16x8, __builtin_amdgcn_raw_buffer_load_b128(vrs, voff, so_, 0)); \
;     sv1 = __builtin_bit_cast(bf16x8, __builtin_amdgcn_raw_buffer_load_b128(vrs, voff, so_ + (unsigned)(32 * LDV * 2), 0)); } while (0)
; #define ATT_BAR() do { ATT_SBAR(); asm volatile("s_barrier" ::: "memory"); ATT_SBAR(); } while (0)
;     ...
;     if constexpr (!(ABL & 4)) { const int tk = (t + 3 < NT) ? t + 3 : NT - 1, tv = (t + 2 < NT) ? t + 2 : NT - 1; ATT_LOAD_K(tk); ATT_LOAD_V(tv); }
;     ATT_BAR();
;     { const int tk_ = k0; k0 = k1; k1 = k2; k2 = tk_; const int tv_ = v0; v0 = v1; v1 = v2; v2 = tv_; }
	s_add_i32 s36, s36, 0x20000
	s_add_i32 s90, s90, 1
	s_cmpk_eq_i32 s90, 0x7e
	s_cbranch_scc1 .LBB0_305
	s_mov_b32 s14, s49
	s_mov_b32 s49, s51
	s_mov_b32 s51, s18
	s_mov_b32 s15, s50
	s_mov_b32 s50, s48
	s_mov_b32 s48, s37
	s_branch .LBB0_297
.LBB0_300:
	v_mov_b32_e32 v175, v174
	s_nop 1
	v_permlane32_swap_b32_e32 v174, v175
	v_max3_f32 v174, v174, v175, 0
	v_exp_f32_e64 v175, -v174
	s_nop 4
	s_nop 0
	v_cmp_gt_f32_e32 vcc, 1.0, v175
	s_cbranch_vccz .LBB0_304
	s_and_saveexec_b64 s[14:15], s[4:5]
	ds_write_b32 v166, v175
	s_or_b64 exec, exec, s[14:15]
	s_waitcnt lgkmcnt(0)
	v_add_u32_e32 v175, s6, v184
	ds_read_b128 v[176:179], v175 offset:96
	ds_read_b128 v[180:183], v175 offset:64
	ds_read_b128 v[186:189], v175 offset:32
	ds_read_b128 v[190:193], v175
	v_and_b32_e32 v244, 63, v0
	v_lshrrev_b32_e32 v245, 4, v244
	v_and_b32_e32 v244, 1, v244
	v_lshlrev_b32_e32 v244, 6, v244
	v_lshl_add_u32 v244, v245, 4, v244
	v_add_u32_e32 v244, s6, v244
	ds_read_b128 v[244:247], v244
	s_waitcnt lgkmcnt(3)
	v_pk_mul_f32 v[78:79], v[78:79], v[176:177]
	s_waitcnt lgkmcnt(2)
	v_pk_mul_f32 v[74:75], v[74:75], v[180:181]
	s_waitcnt lgkmcnt(1)
	v_pk_mul_f32 v[70:71], v[70:71], v[186:187]
	v_pk_mul_f32 v[80:81], v[80:81], v[178:179]
	v_pk_mul_f32 v[76:77], v[76:77], v[182:183]
	v_pk_mul_f32 v[72:73], v[72:73], v[188:189]
	s_waitcnt lgkmcnt(0)
	v_pk_mul_f32 v[68:69], v[68:69], v[192:193]
	v_pk_mul_f32 v[66:67], v[66:67], v[190:191]
	v_pk_mul_f32 v[62:63], v[62:63], v[176:177]
	v_pk_mul_f32 v[58:59], v[58:59], v[180:181]
	v_pk_mul_f32 v[54:55], v[54:55], v[186:187]
	v_pk_mul_f32 v[64:65], v[64:65], v[178:179]
	v_pk_mul_f32 v[60:61], v[60:61], v[182:183]
	v_pk_mul_f32 v[56:57], v[56:57], v[188:189]
	v_pk_mul_f32 v[52:53], v[52:53], v[192:193]
	v_pk_mul_f32 v[50:51], v[50:51], v[190:191]
	v_pk_mul_f32 v[46:47], v[46:47], v[176:177]
	v_pk_mul_f32 v[42:43], v[42:43], v[180:181]
	v_pk_mul_f32 v[38:39], v[38:39], v[186:187]
	v_pk_mul_f32 v[48:49], v[48:49], v[178:179]
	v_pk_mul_f32 v[44:45], v[44:45], v[182:183]
	v_pk_mul_f32 v[40:41], v[40:41], v[188:189]
	v_pk_mul_f32 v[36:37], v[36:37], v[192:193]
	v_pk_mul_f32 v[34:35], v[34:35], v[190:191]
	v_pk_mul_f32 v[14:15], v[14:15], v[176:177]
	v_pk_mul_f32 v[10:11], v[10:11], v[180:181]
	v_pk_mul_f32 v[6:7], v[6:7], v[186:187]
	v_pk_mul_f32 v[16:17], v[16:17], v[178:179]
	v_pk_mul_f32 v[12:13], v[12:13], v[182:183]
	v_pk_mul_f32 v[8:9], v[8:9], v[188:189]
	v_pk_mul_f32 v[4:5], v[4:5], v[192:193]
	v_pk_mul_f32 v[2:3], v[2:3], v[190:191]
	s_waitcnt lgkmcnt(0)
	v_pk_mul_f32 v[240:241], v[240:241], v[244:245]
	v_pk_mul_f32 v[242:243], v[242:243], v[246:247]

; #define ATT_SBAR() __builtin_amdgcn_sched_barrier(0)
; __device__ __forceinline__ unsigned cvtpk(float lo, float hi) { f32x2_t v = {lo, hi}; bf16x2_t b = __builtin_convertvector(v, bf16x2_t); return __builtin_bit_cast(unsigned, b); }
; #define ATT_LOAD_K(t) do { const unsigned so_ = (unsigned)(t) * (unsigned)(KVBLK * LDK * 2); sk0 = __builtin_bit_cast(bf16x8, __builtin_amdgcn_raw_buffer_load_b128(krs, koff, so_, 0)); \
;     if constexpr (DQK == 128) sk1 = __builtin_bit_cast(bf16x8, __builtin_amdgcn_raw_buffer_load_b128(krs, koff, so_ + (unsigned)(32 * LDK * 2), 0)); } while (0)
; #define ATT_LOAD_V(t) do { const unsigned so_ = (unsigned)(t) * (unsigned)(KVBLK * LDV * 2); sv0 = __builtin_bit_cast(bf16x8, __builtin_amdgcn_raw_buffer_load_b128(vrs, voff, so_, 0)); \
;     sv1 = __builtin_bit_cast(bf16x8, __builtin_amdgcn_raw_buffer_load_b128(vrs, voff, so_ + (unsigned)(32 * LDV * 2), 0)); } while (0)
; #define ATT_WRITE_K(so) do { *(bf16x8*)(K_lds + (so) + kswz<DQK>(kr, kc * 2)) = sk0; if constexpr (DQK == 128) *(bf16x8*)(K_lds + (so) + kswz<DQK>(32 + kr, kc * 2)) = sk1; } while (0)
;     ...
;   for (int t = 0; t + 1 < NT; ++t) {
;     if constexpr (ABL & 1) { u32x4 w0 = {cvtpk(p0[0], p0[1]), cvtpk(p0[2], p0[3]), cvtpk(p0[4], p0[5]), cvtpk(p0[6], p0[7])}, w1 = {cvtpk(p0[8], p0[9]), cvtpk(p0[10], p0[11]), cvtpk(p0[12], p0[13]), cvtpk(p0[14], p0[15])};
;         u32x4 w2 = {cvtpk(p1[0], p1[1]), cvtpk(p1[2], p1[3]), cvtpk(p1[4], p1[5]), cvtpk(p1[6], p1[7])}, w3 = {cvtpk(p1[8], p1[9]), cvtpk(p1[10], p1[11]), cvtpk(p1[12], p1[13]), cvtpk(p1[14], p1[15])};
;         pa0 = *reinterpret_cast<bf16x8*>(&w0); pa1 = *reinterpret_cast<bf16x8*>(&w1); pa2 = *reinterpret_cast<bf16x8*>(&w2); pa3 = *reinterpret_cast<bf16x8*>(&w3); }
;     else { ATT_SOFTMAX(t == 0); }
;     if constexpr (!(ABL & 4)) { ATT_WRITE_K(k2); ATT_WRITE_V(v1); }
;     ATT_SBAR();
; #pragma unroll
;     for (int ks = 0; ks < 4; ++ks) ATT_VPAIR(va, v0, 0, ks);
;     asm volatile("s_waitcnt lgkmcnt(8)" ::: "memory"); ATT_BAR();
;     ATT_XSECTION(true);
;     if constexpr (!(ABL & 4)) { const int tk = (t + 3 < NT) ? t + 3 : NT - 1, tv = (t + 2 < NT) ? t + 2 : NT - 1; ATT_LOAD_K(tk); ATT_LOAD_V(tv); }
;     ATT_BAR();
;     { const int tk_ = k0; k0 = k1; k1 = k2; k2 = tk_; const int tv_ = v0; v0 = v1; v1 = v2; v2 = tv_; }
;   }
.LBB0_306:
	v_exp_f32_e32 v98, v98
	v_exp_f32_e32 v114, v114
	v_exp_f32_e32 v99, v99
	v_exp_f32_e32 v115, v115
	v_exp_f32_e32 v100, v100
	v_exp_f32_e32 v101, v101
	v_exp_f32_e32 v102, v102
	v_exp_f32_e32 v103, v103
	v_exp_f32_e32 v106, v106
	v_exp_f32_e32 v107, v107
	v_exp_f32_e32 v116, v116
	v_exp_f32_e32 v117, v117
	v_exp_f32_e32 v118, v118
	v_exp_f32_e32 v119, v119
	v_exp_f32_e32 v104, v104
	v_exp_f32_e32 v120, v120
	v_exp_f32_e32 v105, v105
	v_exp_f32_e32 v121, v121
	v_exp_f32_e32 v122, v122
	v_exp_f32_e32 v123, v123
	v_exp_f32_e32 v108, v108
	v_exp_f32_e32 v124, v124
	v_exp_f32_e32 v109, v109
	v_exp_f32_e32 v125, v125
	v_exp_f32_e32 v110, v110
	v_exp_f32_e32 v126, v126
	v_exp_f32_e32 v111, v111
	v_exp_f32_e32 v127, v127
	v_exp_f32_e32 v112, v112
	v_exp_f32_e32 v128, v128
	v_exp_f32_e32 v113, v113
	v_exp_f32_e32 v129, v129
	v_cvt_pk_bf16_f32 v98, v98, v99
	v_cvt_pk_bf16_f32 v99, v100, v101
	v_cvt_pk_bf16_f32 v100, v102, v103
	v_cvt_pk_bf16_f32 v102, v106, v107
	v_cvt_pk_bf16_f32 v106, v114, v115
	v_add_u32_e32 v114, s51, v170
	s_add_i32 s8, s48, 0
	s_waitcnt vmcnt(2)
	ds_write_b128 v114, v[224:227] offset:49152
	v_add_u32_e32 v114, s8, v168
	v_cvt_pk_bf16_f32 v101, v104, v105
	v_cvt_pk_bf16_f32 v103, v108, v109
	v_cvt_pk_bf16_f32 v104, v110, v111
	v_cvt_pk_bf16_f32 v105, v112, v113
	v_cvt_pk_bf16_f32 v107, v116, v117
	v_cvt_pk_bf16_f32 v108, v118, v119
	v_cvt_pk_bf16_f32 v109, v120, v121
	v_cvt_pk_bf16_f32 v110, v122, v123
	v_cvt_pk_bf16_f32 v111, v124, v125
	v_cvt_pk_bf16_f32 v112, v126, v127
	v_cvt_pk_bf16_f32 v113, v128, v129
	s_waitcnt vmcnt(1)
	ds_write_b128 v114, v[228:231]
	v_add_u32_e32 v114, s8, v169
	s_waitcnt vmcnt(0)
	ds_write_b128 v114, v[232:235]
	v_add_u32_e32 v156, s50, v131
	ds_read_b64_tr_b16 v[114:115], v156
	ds_read_b64_tr_b16 v[116:117], v156 offset:2048
	ds_read_b64_tr_b16 v[118:119], v156 offset:4096
	ds_read_b64_tr_b16 v[120:121], v156 offset:6144
	ds_read_b64_tr_b16 v[122:123], v156 offset:8192
	ds_read_b64_tr_b16 v[124:125], v156 offset:10240
	ds_read_b64_tr_b16 v[126:127], v156 offset:12288
	ds_read_b64_tr_b16 v[128:129], v156 offset:14336
	s_waitcnt lgkmcnt(8)
	s_barrier
	s_setprio 2
	s_waitcnt lgkmcnt(6)
	v_mfma_f32_32x32x16_bf16 v[66:81], v[98:101], v[114:117], v[66:81]
	ds_read_b64_tr_b16 v[152:153], v156 offset:512
	ds_read_b64_tr_b16 v[154:155], v156 offset:2560
	s_waitcnt lgkmcnt(6)
	v_mfma_f32_32x32x16_bf16 v[66:81], v[102:105], v[118:121], v[66:81]
	ds_read_b64_tr_b16 v[114:115], v156 offset:4608
	ds_read_b64_tr_b16 v[116:117], v156 offset:6656
	s_waitcnt lgkmcnt(6)
	v_mfma_f32_32x32x16_bf16 v[66:81], v[106:109], v[122:125], v[66:81]
	ds_read_b64_tr_b16 v[118:119], v156 offset:8704
	ds_read_b64_tr_b16 v[120:121], v156 offset:10752
	s_waitcnt lgkmcnt(6)
	v_mfma_f32_32x32x16_bf16 v[66:81], v[110:113], v[126:129], v[66:81]
	ds_read_b64_tr_b16 v[122:123], v156 offset:12800
	ds_read_b64_tr_b16 v[124:125], v156 offset:14848
	s_waitcnt lgkmcnt(6)
	v_mfma_f32_32x32x16_bf16 v[50:65], v[98:101], v[152:155], v[50:65]
	ds_read_b64_tr_b16 v[126:127], v156 offset:1024
	ds_read_b64_tr_b16 v[128:129], v156 offset:3072
	s_waitcnt lgkmcnt(6)
	v_mfma_f32_32x32x16_bf16 v[50:65], v[102:105], v[114:117], v[50:65]
	ds_read_b64_tr_b16 v[152:153], v156 offset:5120
	ds_read_b64_tr_b16 v[154:155], v156 offset:7168
	s_waitcnt lgkmcnt(6)
	v_mfma_f32_32x32x16_bf16 v[50:65], v[106:109], v[118:121], v[50:65]
	ds_read_b64_tr_b16 v[114:115], v156 offset:9216
	ds_read_b64_tr_b16 v[116:117], v156 offset:11264
	s_waitcnt lgkmcnt(6)
	v_mfma_f32_32x32x16_bf16 v[50:65], v[110:113], v[122:125], v[50:65]
	ds_read_b64_tr_b16 v[118:119], v156 offset:13312
	ds_read_b64_tr_b16 v[120:121], v156 offset:15360
	s_waitcnt lgkmcnt(6)
	v_mfma_f32_32x32x16_bf16 v[34:49], v[98:101], v[126:129], v[34:49]
	ds_read_b64_tr_b16 v[122:123], v156 offset:1536
	ds_read_b64_tr_b16 v[124:125], v156 offset:3584
	s_waitcnt lgkmcnt(6)
	v_mfma_f32_32x32x16_bf16 v[34:49], v[102:105], v[152:155], v[34:49]
	ds_read_b64_tr_b16 v[126:127], v156 offset:5632
	ds_read_b64_tr_b16 v[128:129], v156 offset:7680
	s_waitcnt lgkmcnt(6)
	v_mfma_f32_32x32x16_bf16 v[34:49], v[106:109], v[114:117], v[34:49]
	ds_read_b64_tr_b16 v[152:153], v156 offset:9728
	ds_read_b64_tr_b16 v[154:155], v156 offset:11776
	s_waitcnt lgkmcnt(6)
	v_mfma_f32_32x32x16_bf16 v[34:49], v[110:113], v[118:121], v[34:49]
	ds_read_b64_tr_b16 v[114:115], v156 offset:13824
	ds_read_b64_tr_b16 v[116:117], v156 offset:15872
	s_waitcnt lgkmcnt(6)
	v_mfma_f32_32x32x16_bf16 v[2:17], v[98:101], v[122:125], v[2:17]
	v_add3_u32 v167, v167, s49, v184
	ds_read_b128 v[118:121], v167 offset:49152
	s_waitcnt lgkmcnt(5)
	v_mfma_f32_32x32x16_bf16 v[2:17], v[102:105], v[126:129], v[2:17]
	ds_read_b128 v[122:125], v167 offset:53760
	s_waitcnt lgkmcnt(4)
	v_mfma_f32_32x32x16_bf16 v[2:17], v[106:109], v[152:155], v[2:17]
	ds_read_b128 v[126:129], v167 offset:49184
	s_waitcnt lgkmcnt(3)
	v_mfma_f32_32x32x16_bf16 v[2:17], v[110:113], v[114:117], v[2:17]
	ds_read_b128 v[152:155], v167 offset:53792
	v_mfma_f32_16x16x32_bf16 v[240:243], v[98:101], v[132:135], v[240:243]
	ds_read_b128 v[114:117], v167 offset:49216
	v_mfma_f32_16x16x32_bf16 v[240:243], v[102:105], v[132:135], v[240:243]
	ds_read_b128 v[156:159], v167 offset:53824
	v_mfma_f32_16x16x32_bf16 v[240:243], v[106:109], v[132:135], v[240:243]
	ds_read_b128 v[160:163], v167 offset:49248
	v_mfma_f32_16x16x32_bf16 v[240:243], v[110:113], v[132:135], v[240:243]
	ds_read_b128 v[168:171], v167 offset:53856
	s_waitcnt lgkmcnt(7)
	v_mfma_f32_32x32x16_bf16 v[98:113], v[118:121], v[136:139], v[82:97]
	s_waitcnt lgkmcnt(6)
	v_mfma_f32_32x32x16_bf16 v[82:97], v[122:125], v[136:139], v[82:97]
	s_waitcnt lgkmcnt(5)
	v_mfma_f32_32x32x16_bf16 v[98:113], v[126:129], v[140:143], v[98:113]
	s_waitcnt lgkmcnt(4)
	v_mfma_f32_32x32x16_bf16 v[82:97], v[152:155], v[140:143], v[82:97]
	s_waitcnt lgkmcnt(3)
	v_mfma_f32_32x32x16_bf16 v[98:113], v[114:117], v[144:147], v[98:113]
	s_waitcnt lgkmcnt(2)
	v_mfma_f32_32x32x16_bf16 v[82:97], v[156:159], v[144:147], v[82:97]
	s_waitcnt lgkmcnt(1)
	v_mfma_f32_32x32x16_bf16 v[98:113], v[160:163], v[148:151], v[98:113]
	s_waitcnt lgkmcnt(0)
	v_mfma_f32_32x32x16_bf16 v[82:97], v[168:171], v[148:151], v[82:97]
	s_setprio 0
	s_barrier
	s_nop 10
	v_add_f32_e32 v114, 0, v82
	v_max3_f32 v115, v114, v98, v99
	v_max3_f32 v115, v115, v100, v101
	v_max3_f32 v115, v115, v102, v103
	v_max3_f32 v115, v115, v104, v105
	v_max3_f32 v115, v115, v106, v107
	v_max3_f32 v115, v115, v108, v109
	v_max3_f32 v115, v115, v110, v111
	v_max3_f32 v115, v115, v112, v113
	s_nop 0
	v_max3_f32 v114, v115, v83, v84
	v_max3_f32 v114, v114, v85, v86
	v_max3_f32 v114, v114, v87, v88
	v_max3_f32 v114, v114, v89, v90
	v_max3_f32 v114, v114, v91, v92
	v_max3_f32 v114, v114, v93, v94
	v_max3_f32 v114, v114, v95, v96
	v_max_f32 v114, v114, v97
	s_nop 0
	v_cmp_ge_f32_e32 vcc, s60, v114
	s_cmp_lg_u64 vcc, exec
	s_cbranch_scc1 .LBB0_334
; #define ATT_BAR() do { ATT_SBAR(); asm volatile("s_barrier" ::: "memory"); ATT_SBAR(); } while (0)
; #define ATT_SOFTMAX(first_) do { const float pm_ = softmax_rowmax(p0, p1); \
;     if (__builtin_expect((first_) || !__all(pm_ <= THRL), 0)) { const float al_ = softmax_shift(p0, p1, negm, pm_, (first_)); ATT_RESC(al_); } \
;     softmax_exp_pack(p0, p1, pa0, pa1, pa2, pa3); } while (0)
; #define ATT_VPAIR(buf, so, blk, ks) do { if constexpr (!(ABL & 8) && !(ABL & 32)) { buf[2 * (ks)] = vtr(vq0 + (so) + v_rd_off(blk, ks, 0)); buf[2 * (ks) + 1] = vtr(vq0 + (so) + v_rd_off(blk, ks, 1)); } } while (0)
;     ...
;   ATT_SOFTMAX(false);
; #pragma unroll
;   for (int ks = 0; ks < 4; ++ks) ATT_VPAIR(va, v0, 0, ks);
;   asm volatile("s_waitcnt lgkmcnt(0)" ::: "memory"); ATT_BAR();
;   ATT_XSECTION(false);
;   ATT_BAR();
;   if (grp == 0) ATT_BAR();
.LBB0_307:
	v_exp_f32_e32 v98, v98
	v_exp_f32_e32 v114, v82
	v_exp_f32_e32 v82, v99
	v_exp_f32_e32 v99, v83
	v_exp_f32_e32 v83, v100
	v_exp_f32_e32 v100, v84
	v_exp_f32_e32 v84, v101
	v_exp_f32_e32 v101, v85
	v_exp_f32_e32 v85, v102
	v_exp_f32_e32 v102, v86
	v_exp_f32_e32 v86, v103
	v_exp_f32_e32 v103, v87
	v_exp_f32_e32 v87, v104
	v_exp_f32_e32 v104, v88
	v_exp_f32_e32 v88, v105
	v_exp_f32_e32 v105, v89
	v_exp_f32_e32 v89, v106
	v_exp_f32_e32 v106, v90
	v_exp_f32_e32 v90, v107
	v_exp_f32_e32 v107, v91
	v_exp_f32_e32 v91, v108
	v_exp_f32_e32 v108, v92
	v_exp_f32_e32 v92, v109
	v_exp_f32_e32 v109, v93
	v_exp_f32_e32 v93, v110
	v_exp_f32_e32 v110, v94
	v_exp_f32_e32 v94, v111
	v_exp_f32_e32 v111, v95
	v_exp_f32_e32 v95, v112
	v_exp_f32_e32 v112, v96
	v_exp_f32_e32 v96, v113
	v_exp_f32_e32 v97, v97
	v_add_u32_e32 v118, s48, v131
	v_cvt_pk_bf16_f32 v82, v98, v82
	v_cvt_pk_bf16_f32 v83, v83, v84
	v_cvt_pk_bf16_f32 v84, v85, v86
	v_cvt_pk_bf16_f32 v85, v87, v88
	v_cvt_pk_bf16_f32 v86, v89, v90
	v_cvt_pk_bf16_f32 v87, v91, v92
	v_cvt_pk_bf16_f32 v88, v93, v94
	v_cvt_pk_bf16_f32 v89, v95, v96
	v_cvt_pk_bf16_f32 v90, v114, v99
	v_cvt_pk_bf16_f32 v91, v100, v101
	v_cvt_pk_bf16_f32 v92, v102, v103
	v_cvt_pk_bf16_f32 v93, v104, v105
	v_cvt_pk_bf16_f32 v94, v106, v107
	v_cvt_pk_bf16_f32 v95, v108, v109
	v_cvt_pk_bf16_f32 v96, v110, v111
	v_cvt_pk_bf16_f32 v97, v112, v97
	ds_read_b64_tr_b16 v[98:99], v118
	ds_read_b64_tr_b16 v[100:101], v118 offset:2048
	ds_read_b64_tr_b16 v[102:103], v118 offset:4096
	ds_read_b64_tr_b16 v[104:105], v118 offset:6144
	ds_read_b64_tr_b16 v[106:107], v118 offset:8192
	ds_read_b64_tr_b16 v[108:109], v118 offset:10240
	ds_read_b64_tr_b16 v[110:111], v118 offset:12288
	ds_read_b64_tr_b16 v[112:113], v118 offset:14336
	s_waitcnt lgkmcnt(0)
	s_barrier
	s_setprio 2
	s_waitcnt lgkmcnt(6)
	v_mfma_f32_32x32x16_bf16 v[66:81], v[82:85], v[98:101], v[66:81]
	ds_read_b64_tr_b16 v[114:115], v118 offset:512
	ds_read_b64_tr_b16 v[116:117], v118 offset:2560
	s_waitcnt lgkmcnt(6)
	v_mfma_f32_32x32x16_bf16 v[66:81], v[86:89], v[102:105], v[66:81]
	ds_read_b64_tr_b16 v[98:99], v118 offset:4608
	ds_read_b64_tr_b16 v[100:101], v118 offset:6656
	s_waitcnt lgkmcnt(6)
	v_mfma_f32_32x32x16_bf16 v[66:81], v[90:93], v[106:109], v[66:81]
	ds_read_b64_tr_b16 v[102:103], v118 offset:8704
	ds_read_b64_tr_b16 v[104:105], v118 offset:10752
	s_waitcnt lgkmcnt(6)
	v_mfma_f32_32x32x16_bf16 v[66:81], v[94:97], v[110:113], v[66:81]
	ds_read_b64_tr_b16 v[106:107], v118 offset:12800
	ds_read_b64_tr_b16 v[108:109], v118 offset:14848
	s_waitcnt lgkmcnt(6)
	v_mfma_f32_32x32x16_bf16 v[50:65], v[82:85], v[114:117], v[50:65]
	ds_read_b64_tr_b16 v[110:111], v118 offset:1024
	ds_read_b64_tr_b16 v[112:113], v118 offset:3072
	s_waitcnt lgkmcnt(6)
	v_mfma_f32_32x32x16_bf16 v[50:65], v[86:89], v[98:101], v[50:65]
	ds_read_b64_tr_b16 v[114:115], v118 offset:5120
	ds_read_b64_tr_b16 v[116:117], v118 offset:7168
	s_waitcnt lgkmcnt(6)
	v_mfma_f32_32x32x16_bf16 v[50:65], v[90:93], v[102:105], v[50:65]
	ds_read_b64_tr_b16 v[98:99], v118 offset:9216
	ds_read_b64_tr_b16 v[100:101], v118 offset:11264
	s_waitcnt lgkmcnt(6)
	v_mfma_f32_32x32x16_bf16 v[50:65], v[94:97], v[106:109], v[50:65]
	ds_read_b64_tr_b16 v[102:103], v118 offset:13312
	ds_read_b64_tr_b16 v[104:105], v118 offset:15360
	s_waitcnt lgkmcnt(6)
	v_mfma_f32_32x32x16_bf16 v[34:49], v[82:85], v[110:113], v[34:49]
	ds_read_b64_tr_b16 v[106:107], v118 offset:1536
	ds_read_b64_tr_b16 v[108:109], v118 offset:3584
	s_waitcnt lgkmcnt(6)
	v_mfma_f32_32x32x16_bf16 v[34:49], v[86:89], v[114:117], v[34:49]
	ds_read_b64_tr_b16 v[110:111], v118 offset:5632
	ds_read_b64_tr_b16 v[112:113], v118 offset:7680
	s_waitcnt lgkmcnt(6)
	v_mfma_f32_32x32x16_bf16 v[34:49], v[90:93], v[98:101], v[34:49]
	ds_read_b64_tr_b16 v[114:115], v118 offset:9728
	ds_read_b64_tr_b16 v[116:117], v118 offset:11776
	s_waitcnt lgkmcnt(6)
	v_mfma_f32_32x32x16_bf16 v[34:49], v[94:97], v[102:105], v[34:49]
	ds_read_b64_tr_b16 v[98:99], v118 offset:13824
	ds_read_b64_tr_b16 v[100:101], v118 offset:15872
	s_waitcnt lgkmcnt(6)
	v_mfma_f32_32x32x16_bf16 v[2:17], v[82:85], v[106:109], v[2:17]
	s_waitcnt lgkmcnt(4)
	v_mfma_f32_32x32x16_bf16 v[2:17], v[86:89], v[110:113], v[2:17]
	s_waitcnt lgkmcnt(2)
	v_mfma_f32_32x32x16_bf16 v[2:17], v[90:93], v[114:117], v[2:17]
	s_waitcnt lgkmcnt(0)
	v_mfma_f32_32x32x16_bf16 v[2:17], v[94:97], v[98:101], v[2:17]
	v_mfma_f32_16x16x32_bf16 v[240:243], v[82:85], v[132:135], v[240:243]
	v_mfma_f32_16x16x32_bf16 v[240:243], v[86:89], v[132:135], v[240:243]
	v_mfma_f32_16x16x32_bf16 v[240:243], v[90:93], v[132:135], v[240:243]
	v_mfma_f32_16x16x32_bf16 v[240:243], v[94:97], v[132:135], v[240:243]
	s_setprio 0
	s_barrier
	s_cmpk_gt_u32 s91, 0xff
	s_cbranch_scc1 .LBB0_259
	s_barrier
	s_branch .LBB0_259
; __device__ __forceinline__ float softmax_shift(f32x16& p0, f32x16& p1, f32x16& negm, float pmax, bool first) {
;   asm volatile("s_nop 4" ::: "memory");
;   { auto rr = __builtin_amdgcn_permlane32_swap(__float_as_uint(pmax), __float_as_uint(pmax), false, false);
;     pmax = fmaxf(__uint_as_float(rr[0]), __uint_as_float(rr[1])); }
;   const float delta = first ? pmax : fmaxf(pmax, 0.f);
; #pragma unroll
;   for (int r = 0; r < 16; ++r) { p0[r] -= delta; p1[r] -= delta; negm[r] -= delta; }
;   return first ? 1.f : __builtin_amdgcn_exp2f(-delta);
; }
.LBB0_309:
	v_mov_b32_e32 v192, v191
	s_nop 1
	v_permlane32_swap_b32_e32 v191, v192
	v_max3_f32 v191, v191, v192, 0
	v_exp_f32_e64 v192, -v191
	s_nop 4
	s_nop 0
	v_cmp_gt_f32_e32 vcc, 1.0, v192
	s_cbranch_vccz .LBB0_313
	s_and_saveexec_b64 s[8:9], s[4:5]
	ds_write_b32 v187, v192
	s_or_b64 exec, exec, s[8:9]
	s_waitcnt lgkmcnt(0)
	v_add_u32_e32 v200, s90, v184
	ds_read_b128 v[192:195], v200 offset:96
	ds_read_b128 v[196:199], v200 offset:64
	ds_read_b128 v[212:215], v200 offset:32
	ds_read_b128 v[216:219], v200
	v_and_b32_e32 v244, 63, v0
	v_lshrrev_b32_e32 v245, 4, v244
	v_and_b32_e32 v244, 1, v244
	v_lshlrev_b32_e32 v244, 6, v244
	v_lshl_add_u32 v244, v245, 4, v244
	v_add_u32_e32 v244, s90, v244
	ds_read_b128 v[244:247], v244
	s_waitcnt lgkmcnt(3)
	v_pk_mul_f32 v[30:31], v[30:31], v[192:193]
	s_waitcnt lgkmcnt(2)
	v_pk_mul_f32 v[26:27], v[26:27], v[196:197]
	s_waitcnt lgkmcnt(1)
	v_pk_mul_f32 v[22:23], v[22:23], v[212:213]
	v_pk_mul_f32 v[32:33], v[32:33], v[194:195]
	v_pk_mul_f32 v[28:29], v[28:29], v[198:199]
	v_pk_mul_f32 v[24:25], v[24:25], v[214:215]
	s_waitcnt lgkmcnt(0)
	v_pk_mul_f32 v[20:21], v[20:21], v[218:219]
	v_pk_mul_f32 v[18:19], v[18:19], v[216:217]
	v_pk_mul_f32 v[46:47], v[46:47], v[192:193]
	v_pk_mul_f32 v[42:43], v[42:43], v[196:197]
	v_pk_mul_f32 v[38:39], v[38:39], v[212:213]
	v_pk_mul_f32 v[48:49], v[48:49], v[194:195]
	v_pk_mul_f32 v[44:45], v[44:45], v[198:199]
	v_pk_mul_f32 v[40:41], v[40:41], v[214:215]
	v_pk_mul_f32 v[36:37], v[36:37], v[218:219]
	v_pk_mul_f32 v[34:35], v[34:35], v[216:217]
	v_pk_mul_f32 v[62:63], v[62:63], v[192:193]
	v_pk_mul_f32 v[58:59], v[58:59], v[196:197]
	v_pk_mul_f32 v[54:55], v[54:55], v[212:213]
	v_pk_mul_f32 v[64:65], v[64:65], v[194:195]
	v_pk_mul_f32 v[60:61], v[60:61], v[198:199]
	v_pk_mul_f32 v[56:57], v[56:57], v[214:215]
	v_pk_mul_f32 v[52:53], v[52:53], v[218:219]
	v_pk_mul_f32 v[50:51], v[50:51], v[216:217]
	v_pk_mul_f32 v[78:79], v[78:79], v[192:193]
	v_pk_mul_f32 v[74:75], v[74:75], v[196:197]
	v_pk_mul_f32 v[70:71], v[70:71], v[212:213]
	v_pk_mul_f32 v[80:81], v[80:81], v[194:195]
	v_pk_mul_f32 v[76:77], v[76:77], v[198:199]
	v_pk_mul_f32 v[72:73], v[72:73], v[214:215]
	v_pk_mul_f32 v[68:69], v[68:69], v[218:219]
	v_pk_mul_f32 v[66:67], v[66:67], v[216:217]
	s_waitcnt lgkmcnt(0)
	v_pk_mul_f32 v[240:241], v[240:241], v[244:245]
	v_pk_mul_f32 v[242:243], v[242:243], v[246:247]

; __device__ __forceinline__ float softmax_shift(f32x16& p0, f32x16& p1, f32x16& negm, float pmax, bool first) {
;   asm volatile("s_nop 4" ::: "memory");
;   { auto rr = __builtin_amdgcn_permlane32_swap(__float_as_uint(pmax), __float_as_uint(pmax), false, false);
;     pmax = fmaxf(__uint_as_float(rr[0]), __uint_as_float(rr[1])); }
;   const float delta = first ? pmax : fmaxf(pmax, 0.f);
; #pragma unroll
;   for (int r = 0; r < 16; ++r) { p0[r] -= delta; p1[r] -= delta; negm[r] -= delta; }
;   return first ? 1.f : __builtin_amdgcn_exp2f(-delta);
; }
.LBB0_314:
	v_mov_b32_e32 v115, v114
	s_nop 1
	v_permlane32_swap_b32_e32 v114, v115
	v_max3_f32 v114, v114, v115, 0
	v_exp_f32_e64 v115, -v114
	s_nop 4
	s_nop 0
	v_cmp_gt_f32_e32 vcc, 1.0, v115
	s_cbranch_vccz .LBB0_318
	s_and_saveexec_b64 s[8:9], s[4:5]
	ds_write_b32 v187, v115
	s_or_b64 exec, exec, s[8:9]
	s_waitcnt lgkmcnt(0)
	v_add_u32_e32 v115, s90, v184
	ds_read_b128 v[116:119], v115 offset:96
	ds_read_b128 v[120:123], v115 offset:64
	ds_read_b128 v[124:127], v115 offset:32
	ds_read_b128 v[136:139], v115
	v_and_b32_e32 v244, 63, v0
	v_lshrrev_b32_e32 v245, 4, v244
	v_and_b32_e32 v244, 1, v244
	v_lshlrev_b32_e32 v244, 6, v244
	v_lshl_add_u32 v244, v245, 4, v244
	v_add_u32_e32 v244, s90, v244
	ds_read_b128 v[244:247], v244
	s_waitcnt lgkmcnt(3)
	v_pk_mul_f32 v[30:31], v[30:31], v[116:117]
	s_waitcnt lgkmcnt(2)
	v_pk_mul_f32 v[26:27], v[26:27], v[120:121]
	s_waitcnt lgkmcnt(1)
	v_pk_mul_f32 v[22:23], v[22:23], v[124:125]
	v_pk_mul_f32 v[32:33], v[32:33], v[118:119]
	v_pk_mul_f32 v[28:29], v[28:29], v[122:123]
	v_pk_mul_f32 v[24:25], v[24:25], v[126:127]
	s_waitcnt lgkmcnt(0)
	v_pk_mul_f32 v[20:21], v[20:21], v[138:139]
	v_pk_mul_f32 v[18:19], v[18:19], v[136:137]
	v_pk_mul_f32 v[46:47], v[46:47], v[116:117]
	v_pk_mul_f32 v[42:43], v[42:43], v[120:121]
	v_pk_mul_f32 v[38:39], v[38:39], v[124:125]
	v_pk_mul_f32 v[48:49], v[48:49], v[118:119]
	v_pk_mul_f32 v[44:45], v[44:45], v[122:123]
	v_pk_mul_f32 v[40:41], v[40:41], v[126:127]
	v_pk_mul_f32 v[36:37], v[36:37], v[138:139]
	v_pk_mul_f32 v[34:35], v[34:35], v[136:137]
	v_pk_mul_f32 v[62:63], v[62:63], v[116:117]
	v_pk_mul_f32 v[58:59], v[58:59], v[120:121]
	v_pk_mul_f32 v[54:55], v[54:55], v[124:125]
	v_pk_mul_f32 v[64:65], v[64:65], v[118:119]
	v_pk_mul_f32 v[60:61], v[60:61], v[122:123]
	v_pk_mul_f32 v[56:57], v[56:57], v[126:127]
	v_pk_mul_f32 v[52:53], v[52:53], v[138:139]
	v_pk_mul_f32 v[50:51], v[50:51], v[136:137]
	v_pk_mul_f32 v[78:79], v[78:79], v[116:117]
	v_pk_mul_f32 v[74:75], v[74:75], v[120:121]
	v_pk_mul_f32 v[70:71], v[70:71], v[124:125]
	v_pk_mul_f32 v[80:81], v[80:81], v[118:119]
	v_pk_mul_f32 v[76:77], v[76:77], v[122:123]
	v_pk_mul_f32 v[72:73], v[72:73], v[126:127]
	v_pk_mul_f32 v[68:69], v[68:69], v[138:139]
	v_pk_mul_f32 v[66:67], v[66:67], v[136:137]
	s_waitcnt lgkmcnt(0)
	v_pk_mul_f32 v[240:241], v[240:241], v[244:245]
	v_pk_mul_f32 v[242:243], v[242:243], v[246:247]

; __device__ __forceinline__ float softmax_shift(f32x16& p0, f32x16& p1, f32x16& negm, float pmax, bool first) {
;   asm volatile("s_nop 4" ::: "memory");
;   { auto rr = __builtin_amdgcn_permlane32_swap(__float_as_uint(pmax), __float_as_uint(pmax), false, false);
;     pmax = fmaxf(__uint_as_float(rr[0]), __uint_as_float(rr[1])); }
;   const float delta = first ? pmax : fmaxf(pmax, 0.f);
; #pragma unroll
;   for (int r = 0; r < 16; ++r) { p0[r] -= delta; p1[r] -= delta; negm[r] -= delta; }
;   return first ? 1.f : __builtin_amdgcn_exp2f(-delta);
; }
.LBB0_319:
	v_mov_b32_e32 v171, v170
	s_nop 1
	v_permlane32_swap_b32_e32 v170, v171
	v_max3_f32 v170, v170, v171, 0
	v_exp_f32_e64 v171, -v170
	s_nop 4
	s_nop 0
	v_cmp_gt_f32_e32 vcc, 1.0, v171
	s_cbranch_vccz .LBB0_323
	s_and_saveexec_b64 s[14:15], s[4:5]
	ds_write_b32 v165, v171
	s_or_b64 exec, exec, s[14:15]
	s_waitcnt lgkmcnt(0)
	v_add_u32_e32 v171, s6, v184
	ds_read_b128 v[172:175], v171 offset:96
	ds_read_b128 v[176:179], v171 offset:64
	ds_read_b128 v[180:183], v171 offset:32
	ds_read_b128 v[186:189], v171
	v_and_b32_e32 v244, 63, v0
	v_lshrrev_b32_e32 v245, 4, v244
	v_and_b32_e32 v244, 1, v244
	v_lshlrev_b32_e32 v244, 6, v244
	v_lshl_add_u32 v244, v245, 4, v244
	v_add_u32_e32 v244, s6, v244
	ds_read_b128 v[244:247], v244
	s_waitcnt lgkmcnt(3)
	v_pk_mul_f32 v[30:31], v[30:31], v[172:173]
	s_waitcnt lgkmcnt(2)
	v_pk_mul_f32 v[26:27], v[26:27], v[176:177]
	s_waitcnt lgkmcnt(1)
	v_pk_mul_f32 v[22:23], v[22:23], v[180:181]
	v_pk_mul_f32 v[32:33], v[32:33], v[174:175]
	v_pk_mul_f32 v[28:29], v[28:29], v[178:179]
	v_pk_mul_f32 v[24:25], v[24:25], v[182:183]
	s_waitcnt lgkmcnt(0)
	v_pk_mul_f32 v[20:21], v[20:21], v[188:189]
	v_pk_mul_f32 v[18:19], v[18:19], v[186:187]
	v_pk_mul_f32 v[46:47], v[46:47], v[172:173]
	v_pk_mul_f32 v[42:43], v[42:43], v[176:177]
	v_pk_mul_f32 v[38:39], v[38:39], v[180:181]
	v_pk_mul_f32 v[48:49], v[48:49], v[174:175]
	v_pk_mul_f32 v[44:45], v[44:45], v[178:179]
	v_pk_mul_f32 v[40:41], v[40:41], v[182:183]
	v_pk_mul_f32 v[36:37], v[36:37], v[188:189]
	v_pk_mul_f32 v[34:35], v[34:35], v[186:187]
	v_pk_mul_f32 v[62:63], v[62:63], v[172:173]
	v_pk_mul_f32 v[58:59], v[58:59], v[176:177]
	v_pk_mul_f32 v[54:55], v[54:55], v[180:181]
	v_pk_mul_f32 v[64:65], v[64:65], v[174:175]
	v_pk_mul_f32 v[60:61], v[60:61], v[178:179]
	v_pk_mul_f32 v[56:57], v[56:57], v[182:183]
	v_pk_mul_f32 v[52:53], v[52:53], v[188:189]
	v_pk_mul_f32 v[50:51], v[50:51], v[186:187]
	v_pk_mul_f32 v[78:79], v[78:79], v[172:173]
	v_pk_mul_f32 v[74:75], v[74:75], v[176:177]
	v_pk_mul_f32 v[70:71], v[70:71], v[180:181]
	v_pk_mul_f32 v[80:81], v[80:81], v[174:175]
	v_pk_mul_f32 v[76:77], v[76:77], v[178:179]
	v_pk_mul_f32 v[72:73], v[72:73], v[182:183]
	v_pk_mul_f32 v[68:69], v[68:69], v[188:189]
	v_pk_mul_f32 v[66:67], v[66:67], v[186:187]
	s_waitcnt lgkmcnt(0)
	v_pk_mul_f32 v[240:241], v[240:241], v[244:245]
	v_pk_mul_f32 v[242:243], v[242:243], v[246:247]

; __device__ __forceinline__ float softmax_shift(f32x16& p0, f32x16& p1, f32x16& negm, float pmax, bool first) {
;   asm volatile("s_nop 4" ::: "memory");
;   { auto rr = __builtin_amdgcn_permlane32_swap(__float_as_uint(pmax), __float_as_uint(pmax), false, false);
;     pmax = fmaxf(__uint_as_float(rr[0]), __uint_as_float(rr[1])); }
;   const float delta = first ? pmax : fmaxf(pmax, 0.f);
; #pragma unroll
;   for (int r = 0; r < 16; ++r) { p0[r] -= delta; p1[r] -= delta; negm[r] -= delta; }
;   return first ? 1.f : __builtin_amdgcn_exp2f(-delta);
; }
.LBB0_324:
	v_mov_b32_e32 v115, v114
	s_nop 1
	v_permlane32_swap_b32_e32 v114, v115
	v_max3_f32 v114, v114, v115, 0
	v_exp_f32_e64 v115, -v114
	s_nop 4
	s_nop 0
	v_cmp_gt_f32_e32 vcc, 1.0, v115
	s_cbranch_vccz .LBB0_328
	s_and_saveexec_b64 s[14:15], s[4:5]
	ds_write_b32 v165, v115
	s_or_b64 exec, exec, s[14:15]
	s_waitcnt lgkmcnt(0)
	v_add_u32_e32 v115, s6, v184
	ds_read_b128 v[116:119], v115 offset:96
	ds_read_b128 v[120:123], v115 offset:64
	ds_read_b128 v[124:127], v115 offset:32
	ds_read_b128 v[136:139], v115
	v_and_b32_e32 v244, 63, v0
	v_lshrrev_b32_e32 v245, 4, v244
	v_and_b32_e32 v244, 1, v244
	v_lshlrev_b32_e32 v244, 6, v244
	v_lshl_add_u32 v244, v245, 4, v244
	v_add_u32_e32 v244, s6, v244
	ds_read_b128 v[244:247], v244
	s_waitcnt lgkmcnt(3)
	v_pk_mul_f32 v[30:31], v[30:31], v[116:117]
	s_waitcnt lgkmcnt(2)
	v_pk_mul_f32 v[26:27], v[26:27], v[120:121]
	s_waitcnt lgkmcnt(1)
	v_pk_mul_f32 v[22:23], v[22:23], v[124:125]
	v_pk_mul_f32 v[32:33], v[32:33], v[118:119]
	v_pk_mul_f32 v[28:29], v[28:29], v[122:123]
	v_pk_mul_f32 v[24:25], v[24:25], v[126:127]
	s_waitcnt lgkmcnt(0)
	v_pk_mul_f32 v[20:21], v[20:21], v[138:139]
	v_pk_mul_f32 v[18:19], v[18:19], v[136:137]
	v_pk_mul_f32 v[46:47], v[46:47], v[116:117]
	v_pk_mul_f32 v[42:43], v[42:43], v[120:121]
	v_pk_mul_f32 v[38:39], v[38:39], v[124:125]
	v_pk_mul_f32 v[48:49], v[48:49], v[118:119]
	v_pk_mul_f32 v[44:45], v[44:45], v[122:123]
	v_pk_mul_f32 v[40:41], v[40:41], v[126:127]
	v_pk_mul_f32 v[36:37], v[36:37], v[138:139]
	v_pk_mul_f32 v[34:35], v[34:35], v[136:137]
	v_pk_mul_f32 v[62:63], v[62:63], v[116:117]
	v_pk_mul_f32 v[58:59], v[58:59], v[120:121]
	v_pk_mul_f32 v[54:55], v[54:55], v[124:125]
	v_pk_mul_f32 v[64:65], v[64:65], v[118:119]
	v_pk_mul_f32 v[60:61], v[60:61], v[122:123]
	v_pk_mul_f32 v[56:57], v[56:57], v[126:127]
	v_pk_mul_f32 v[52:53], v[52:53], v[138:139]
	v_pk_mul_f32 v[50:51], v[50:51], v[136:137]
	v_pk_mul_f32 v[78:79], v[78:79], v[116:117]
	v_pk_mul_f32 v[74:75], v[74:75], v[120:121]
	v_pk_mul_f32 v[70:71], v[70:71], v[124:125]
	v_pk_mul_f32 v[80:81], v[80:81], v[118:119]
	v_pk_mul_f32 v[76:77], v[76:77], v[122:123]
	v_pk_mul_f32 v[72:73], v[72:73], v[126:127]
	v_pk_mul_f32 v[68:69], v[68:69], v[138:139]
	v_pk_mul_f32 v[66:67], v[66:67], v[136:137]
	s_waitcnt lgkmcnt(0)
	v_pk_mul_f32 v[240:241], v[240:241], v[244:245]
	v_pk_mul_f32 v[242:243], v[242:243], v[246:247]

; __device__ __forceinline__ float softmax_shift(f32x16& p0, f32x16& p1, f32x16& negm, float pmax, bool first) {
;   asm volatile("s_nop 4" ::: "memory");
;   { auto rr = __builtin_amdgcn_permlane32_swap(__float_as_uint(pmax), __float_as_uint(pmax), false, false);
;     pmax = fmaxf(__uint_as_float(rr[0]), __uint_as_float(rr[1])); }
;   const float delta = first ? pmax : fmaxf(pmax, 0.f);
; #pragma unroll
;   for (int r = 0; r < 16; ++r) { p0[r] -= delta; p1[r] -= delta; negm[r] -= delta; }
;   return first ? 1.f : __builtin_amdgcn_exp2f(-delta);
; }
.LBB0_329:
	v_mov_b32_e32 v172, v171
	s_nop 1
	v_permlane32_swap_b32_e32 v171, v172
	v_max3_f32 v171, v171, v172, 0
	v_exp_f32_e64 v172, -v171
	s_nop 4
	s_nop 0
	v_cmp_gt_f32_e32 vcc, 1.0, v172
	s_cbranch_vccz .LBB0_333
	s_and_saveexec_b64 s[8:9], s[4:5]
	ds_write_b32 v166, v172
	s_or_b64 exec, exec, s[8:9]
	s_waitcnt lgkmcnt(0)
	v_add_u32_e32 v186, s6, v184
	ds_read_b128 v[172:175], v186 offset:96
	ds_read_b128 v[176:179], v186 offset:64
	ds_read_b128 v[180:183], v186 offset:32
	ds_read_b128 v[186:189], v186
	v_and_b32_e32 v244, 63, v0
	v_lshrrev_b32_e32 v245, 4, v244
	v_and_b32_e32 v244, 1, v244
	v_lshlrev_b32_e32 v244, 6, v244
	v_lshl_add_u32 v244, v245, 4, v244
	v_add_u32_e32 v244, s6, v244
	ds_read_b128 v[244:247], v244
	s_waitcnt lgkmcnt(3)
	v_pk_mul_f32 v[78:79], v[78:79], v[172:173]
	s_waitcnt lgkmcnt(2)
	v_pk_mul_f32 v[74:75], v[74:75], v[176:177]
	s_waitcnt lgkmcnt(1)
	v_pk_mul_f32 v[70:71], v[70:71], v[180:181]
	v_pk_mul_f32 v[80:81], v[80:81], v[174:175]
	v_pk_mul_f32 v[76:77], v[76:77], v[178:179]
	v_pk_mul_f32 v[72:73], v[72:73], v[182:183]
	s_waitcnt lgkmcnt(0)
	v_pk_mul_f32 v[68:69], v[68:69], v[188:189]
	v_pk_mul_f32 v[66:67], v[66:67], v[186:187]
	v_pk_mul_f32 v[62:63], v[62:63], v[172:173]
	v_pk_mul_f32 v[58:59], v[58:59], v[176:177]
	v_pk_mul_f32 v[54:55], v[54:55], v[180:181]
	v_pk_mul_f32 v[64:65], v[64:65], v[174:175]
	v_pk_mul_f32 v[60:61], v[60:61], v[178:179]
	v_pk_mul_f32 v[56:57], v[56:57], v[182:183]
	v_pk_mul_f32 v[52:53], v[52:53], v[188:189]
	v_pk_mul_f32 v[50:51], v[50:51], v[186:187]
	v_pk_mul_f32 v[46:47], v[46:47], v[172:173]
	v_pk_mul_f32 v[42:43], v[42:43], v[176:177]
	v_pk_mul_f32 v[38:39], v[38:39], v[180:181]
	v_pk_mul_f32 v[48:49], v[48:49], v[174:175]
	v_pk_mul_f32 v[44:45], v[44:45], v[178:179]
	v_pk_mul_f32 v[40:41], v[40:41], v[182:183]
	v_pk_mul_f32 v[36:37], v[36:37], v[188:189]
	v_pk_mul_f32 v[34:35], v[34:35], v[186:187]
	v_pk_mul_f32 v[14:15], v[14:15], v[172:173]
	v_pk_mul_f32 v[10:11], v[10:11], v[176:177]
	v_pk_mul_f32 v[6:7], v[6:7], v[180:181]
	v_pk_mul_f32 v[16:17], v[16:17], v[174:175]
	v_pk_mul_f32 v[12:13], v[12:13], v[178:179]
	v_pk_mul_f32 v[8:9], v[8:9], v[182:183]
	v_pk_mul_f32 v[4:5], v[4:5], v[188:189]
	v_pk_mul_f32 v[2:3], v[2:3], v[186:187]
	s_waitcnt lgkmcnt(0)
	v_pk_mul_f32 v[240:241], v[240:241], v[244:245]
	v_pk_mul_f32 v[242:243], v[242:243], v[246:247]

; __device__ __forceinline__ float softmax_shift(f32x16& p0, f32x16& p1, f32x16& negm, float pmax, bool first) {
;   asm volatile("s_nop 4" ::: "memory");
;   { auto rr = __builtin_amdgcn_permlane32_swap(__float_as_uint(pmax), __float_as_uint(pmax), false, false);
;     pmax = fmaxf(__uint_as_float(rr[0]), __uint_as_float(rr[1])); }
;   const float delta = first ? pmax : fmaxf(pmax, 0.f);
; #pragma unroll
;   for (int r = 0; r < 16; ++r) { p0[r] -= delta; p1[r] -= delta; negm[r] -= delta; }
;   return first ? 1.f : __builtin_amdgcn_exp2f(-delta);
; }
.LBB0_334:
	v_mov_b32_e32 v115, v114
	s_nop 1
	v_permlane32_swap_b32_e32 v114, v115
	v_max3_f32 v114, v114, v115, 0
	v_exp_f32_e64 v115, -v114
	s_nop 4
	s_nop 0
	v_cmp_gt_f32_e32 vcc, 1.0, v115
	s_cbranch_vccz .LBB0_338
	s_and_saveexec_b64 s[8:9], s[4:5]
	ds_write_b32 v166, v115
	s_or_b64 exec, exec, s[8:9]
	s_waitcnt lgkmcnt(0)
	v_add_u32_e32 v115, s6, v184
	ds_read_b128 v[116:119], v115 offset:96
	ds_read_b128 v[120:123], v115 offset:64
	ds_read_b128 v[124:127], v115 offset:32
	ds_read_b128 v[136:139], v115
	v_and_b32_e32 v244, 63, v0
	v_lshrrev_b32_e32 v245, 4, v244
	v_and_b32_e32 v244, 1, v244
	v_lshlrev_b32_e32 v244, 6, v244
	v_lshl_add_u32 v244, v245, 4, v244
	v_add_u32_e32 v244, s6, v244
	ds_read_b128 v[244:247], v244
	s_waitcnt lgkmcnt(3)
	v_pk_mul_f32 v[78:79], v[78:79], v[116:117]
	s_waitcnt lgkmcnt(2)
	v_pk_mul_f32 v[74:75], v[74:75], v[120:121]
	s_waitcnt lgkmcnt(1)
	v_pk_mul_f32 v[70:71], v[70:71], v[124:125]
	v_pk_mul_f32 v[80:81], v[80:81], v[118:119]
	v_pk_mul_f32 v[76:77], v[76:77], v[122:123]
	v_pk_mul_f32 v[72:73], v[72:73], v[126:127]
	s_waitcnt lgkmcnt(0)
	v_pk_mul_f32 v[68:69], v[68:69], v[138:139]
	v_pk_mul_f32 v[66:67], v[66:67], v[136:137]
	v_pk_mul_f32 v[62:63], v[62:63], v[116:117]
	v_pk_mul_f32 v[58:59], v[58:59], v[120:121]
	v_pk_mul_f32 v[54:55], v[54:55], v[124:125]
	v_pk_mul_f32 v[64:65], v[64:65], v[118:119]
	v_pk_mul_f32 v[60:61], v[60:61], v[122:123]
	v_pk_mul_f32 v[56:57], v[56:57], v[126:127]
	v_pk_mul_f32 v[52:53], v[52:53], v[138:139]
	v_pk_mul_f32 v[50:51], v[50:51], v[136:137]
	v_pk_mul_f32 v[46:47], v[46:47], v[116:117]
	v_pk_mul_f32 v[42:43], v[42:43], v[120:121]
	v_pk_mul_f32 v[38:39], v[38:39], v[124:125]
	v_pk_mul_f32 v[48:49], v[48:49], v[118:119]
	v_pk_mul_f32 v[44:45], v[44:45], v[122:123]
	v_pk_mul_f32 v[40:41], v[40:41], v[126:127]
	v_pk_mul_f32 v[36:37], v[36:37], v[138:139]
	v_pk_mul_f32 v[34:35], v[34:35], v[136:137]
	v_pk_mul_f32 v[14:15], v[14:15], v[116:117]
	v_pk_mul_f32 v[10:11], v[10:11], v[120:121]
	v_pk_mul_f32 v[6:7], v[6:7], v[124:125]
	v_pk_mul_f32 v[16:17], v[16:17], v[118:119]
	v_pk_mul_f32 v[12:13], v[12:13], v[122:123]
	v_pk_mul_f32 v[8:9], v[8:9], v[126:127]
	v_pk_mul_f32 v[4:5], v[4:5], v[138:139]
	v_pk_mul_f32 v[2:3], v[2:3], v[136:137]
	s_waitcnt lgkmcnt(0)
	v_pk_mul_f32 v[240:241], v[240:241], v[244:245]
	v_pk_mul_f32 v[242:243], v[242:243], v[246:247]
